# wt1: dpp6 + write-through (sc1) 16-byte epilogue stores in IN / conv+attention / expert-down phases (less dirty L2 at the grid barriers)
# baseline (speedup 1.0000x reference)
; __device__ __forceinline__ float rcpf_(float x) { float r = __builtin_amdgcn_rcpf(x); asm volatile("s_nop 0" : "+v"(r)); return r; }
; #define EFENCE() asm volatile("" ::: "memory")
;     __device__ __forceinline__ bool operator()(f32x4 (&acc)[2][2][4][2], const pg8::Unit& u, int wr, int wc, int fr, int fq) const {
;     ...
;         } else {
;             const int colb = (pn - 24) * 128 + wc * 32 + 8 * fq;
; #pragma unroll
;             for (int ai = 0; ai < 2; ++ai)
; #pragma unroll
;                 for (int m = 0; m < 4; ++m) { const int row = row0 + ai * 128 + m * 16; const float rsv = RS_AT(ai, m);
;                     f32x4 r0, r1, g0, g1;
; #pragma unroll
;                     for (int j = 0; j < 4; ++j) { const float e00 = 1.0f + __expf(-acc[ai][0][m][0][j] * rsv), e01 = 1.0f + __expf(-acc[ai][0][m][1][j] * rsv), e10 = 1.0f + __expf(-acc[ai][1][m][0][j] * rsv), e11 = 1.0f + __expf(-acc[ai][1][m][1][j] * rsv);
;                         r0[j] = e10 * rcpf_(e00); r1[j] = e11 * rcpf_(e01); g0[j] = rcpf_(e10); g1[j] = rcpf_(e11); }
;                     st8(G + (size_t)row * 2048 + colb, r0, r1); st8(G + (size_t)row * 2048 + 1024 + colb, g0, g1); EFENCE(); }
.LBB0_726:
	s_cmp_gt_u32 s29, 15
	s_cbranch_scc0 .LBB0_732
	s_lshl_b32 s11, s29, 7
	s_cmp_gt_u32 s29, 23
	s_cbranch_scc0 .LBB0_729
	v_mul_f32_e64 v128, v198, -v124
	v_mul_f32_e64 v129, v198, -v120
	v_mul_f32_e32 v128, 0x3fb8aa3b, v128
	v_mul_f32_e32 v129, 0x3fb8aa3b, v129
	v_exp_f32_e32 v128, v128
	v_exp_f32_e32 v129, v129
	v_mul_f32_e64 v130, v198, -v116
	v_mul_f32_e64 v131, v198, -v112
	v_mul_f32_e32 v130, 0x3fb8aa3b, v130
	v_mul_f32_e32 v131, 0x3fb8aa3b, v131
	v_exp_f32_e32 v130, v130
	v_exp_f32_e32 v131, v131
	v_add_f32_e32 v128, 1.0, v128
	v_add_f32_e32 v129, 1.0, v129
	v_rcp_f32_e32 v128, v128
	v_rcp_f32_e32 v129, v129
	v_add_f32_e32 v130, 1.0, v130
	v_add_f32_e32 v131, 1.0, v131
	s_nop 0
	s_nop 0
	v_rcp_f32_e32 v136, v130
	v_mul_f32_e32 v132, v130, v128
	v_mul_f32_e32 v133, v131, v129
	v_mul_f32_e64 v128, v198, -v125
	v_mul_f32_e64 v129, v198, -v121
	v_mul_f32_e32 v128, 0x3fb8aa3b, v128
	v_mul_f32_e32 v129, 0x3fb8aa3b, v129
	v_rcp_f32_e32 v137, v131
	v_exp_f32_e32 v128, v128
	v_exp_f32_e32 v129, v129
	v_mul_f32_e64 v130, v198, -v117
	v_mul_f32_e64 v131, v198, -v113
	v_mul_f32_e32 v130, 0x3fb8aa3b, v130
	v_mul_f32_e32 v131, 0x3fb8aa3b, v131
	v_exp_f32_e32 v130, v130
	v_exp_f32_e32 v131, v131
	v_add_f32_e32 v128, 1.0, v128
	v_add_f32_e32 v129, 1.0, v129
	v_rcp_f32_e32 v128, v128
	v_rcp_f32_e32 v129, v129
	s_nop 0
	s_nop 0
	v_add_f32_e32 v130, 1.0, v130
	v_add_f32_e32 v131, 1.0, v131
	s_nop 0
	s_nop 0
	v_rcp_f32_e32 v140, v130
	v_mul_f32_e32 v138, v130, v128
	v_mul_f32_e32 v139, v131, v129
	v_mul_f32_e64 v128, v198, -v126
	v_mul_f32_e64 v129, v198, -v122
	v_mul_f32_e32 v128, 0x3fb8aa3b, v128
	v_mul_f32_e32 v129, 0x3fb8aa3b, v129
	v_rcp_f32_e32 v141, v131
	v_exp_f32_e32 v128, v128
	v_exp_f32_e32 v129, v129
	v_mul_f32_e64 v130, v198, -v118
	v_mul_f32_e64 v131, v198, -v114
	v_mul_f32_e32 v130, 0x3fb8aa3b, v130
	v_mul_f32_e32 v131, 0x3fb8aa3b, v131
	v_exp_f32_e32 v130, v130
	v_exp_f32_e32 v131, v131
	v_add_f32_e32 v128, 1.0, v128
	v_add_f32_e32 v129, 1.0, v129
	v_rcp_f32_e32 v128, v128
	v_rcp_f32_e32 v129, v129
	s_nop 0
	s_nop 0
	v_add_f32_e32 v130, 1.0, v130
	v_add_f32_e32 v131, 1.0, v131
	s_nop 0
	s_nop 0
	v_rcp_f32_e32 v143, v130
	v_mul_f32_e32 v142, v130, v128
	v_mul_f32_e64 v128, v198, -v127
	v_mul_f32_e32 v145, v131, v129
	v_mul_f32_e64 v129, v198, -v123
	v_mul_f32_e32 v128, 0x3fb8aa3b, v128
	v_mul_f32_e32 v129, 0x3fb8aa3b, v129
	v_rcp_f32_e32 v144, v131
	v_exp_f32_e32 v128, v128
	v_exp_f32_e32 v129, v129
	v_mul_f32_e64 v130, v198, -v119
	v_mul_f32_e64 v131, v198, -v115
	v_mul_f32_e32 v130, 0x3fb8aa3b, v130
	v_mul_f32_e32 v131, 0x3fb8aa3b, v131
	v_exp_f32_e32 v130, v130
	v_exp_f32_e32 v131, v131
	v_add_f32_e32 v128, 1.0, v128
	v_add_f32_e32 v129, 1.0, v129
	v_rcp_f32_e32 v128, v128
	v_rcp_f32_e32 v129, v129
	s_nop 0
	s_nop 0
	v_add_f32_e32 v130, 1.0, v130
	v_add_f32_e32 v131, 1.0, v131
	s_nop 0
	s_nop 0
	v_readlane_b32 s2, v251, 50
	v_add_u32_e32 v160, s11, v213
	v_mul_f32_e32 v147, v130, v128
	v_mul_f32_e32 v153, v131, v129
	v_lshlrev_b64 v[128:129], 12, v[184:185]
	v_readlane_b32 s3, v251, 51
	v_rcp_f32_e32 v149, v130
	v_rcp_f32_e32 v151, v131
	v_lshl_add_u64 v[130:131], s[2:3], 0, v[128:129]
	v_lshlrev_b64 v[128:129], 1, v[160:161]
	s_nop 0
	s_nop 0
	v_lshl_add_u64 v[134:135], v[130:131], 0, v[128:129]
	v_cvt_pk_bf16_f32 v130, v132, v138
	v_cvt_pk_bf16_f32 v131, v142, v147
	v_cvt_pk_bf16_f32 v132, v133, v139
	v_cvt_pk_bf16_f32 v133, v145, v153
	global_store_dwordx4 v[134:135], v[130:133], off sc1
	s_mov_b64 s[4:5], 0
	s_nop 0
	v_cvt_pk_bf16_f32 v130, v136, v140
	v_cvt_pk_bf16_f32 v131, v143, v149
	v_cvt_pk_bf16_f32 v132, v137, v141
	v_mul_f32_e64 v136, v154, -v108
	v_mul_f32_e64 v137, v154, -v104
	v_cvt_pk_bf16_f32 v133, v144, v151
	v_mul_f32_e32 v136, 0x3fb8aa3b, v136
	v_mul_f32_e32 v137, 0x3fb8aa3b, v137
	v_exp_f32_e32 v136, v136
	v_exp_f32_e32 v137, v137
	global_store_dwordx4 v[134:135], v[130:133], off offset:2048 sc1
	v_mul_f32_e64 v134, v154, -v99
	v_mul_f32_e32 v134, 0x3fb8aa3b, v134
	v_mul_f32_e64 v132, v154, -v100
	v_mul_f32_e64 v133, v154, -v96
	v_mul_f32_e32 v132, 0x3fb8aa3b, v132
	v_mul_f32_e32 v133, 0x3fb8aa3b, v133
	v_exp_f32_e32 v132, v132
	v_exp_f32_e32 v133, v133
	v_add_f32_e32 v130, 1.0, v136
	v_add_f32_e32 v131, 1.0, v137
	v_rcp_f32_e32 v130, v130
	v_rcp_f32_e32 v131, v131
	v_add_f32_e32 v132, 1.0, v132
	v_add_f32_e32 v133, 1.0, v133
	s_nop 0
	s_nop 0
	v_rcp_f32_e32 v138, v132
	v_mul_f32_e32 v136, v132, v130
	v_mul_f32_e32 v137, v133, v131
	v_mul_f32_e64 v130, v154, -v109
	v_mul_f32_e64 v131, v154, -v105
	v_mul_f32_e32 v130, 0x3fb8aa3b, v130
	v_mul_f32_e32 v131, 0x3fb8aa3b, v131
	v_rcp_f32_e32 v139, v133
	v_exp_f32_e32 v130, v130
	v_exp_f32_e32 v131, v131
	v_mul_f32_e64 v132, v154, -v101
	v_mul_f32_e64 v133, v154, -v97
	v_mul_f32_e32 v132, 0x3fb8aa3b, v132
	v_mul_f32_e32 v133, 0x3fb8aa3b, v133
	v_exp_f32_e32 v132, v132
	v_exp_f32_e32 v133, v133
	v_add_f32_e32 v130, 1.0, v130
	v_add_f32_e32 v131, 1.0, v131
	v_rcp_f32_e32 v130, v130
	v_rcp_f32_e32 v131, v131
	s_nop 0
	s_nop 0
	v_add_f32_e32 v132, 1.0, v132
	v_add_f32_e32 v133, 1.0, v133
	s_nop 0
	s_nop 0
	v_rcp_f32_e32 v142, v132
	v_mul_f32_e32 v140, v132, v130
	v_mul_f32_e32 v141, v133, v131
	v_mul_f32_e64 v130, v154, -v110
	v_mul_f32_e64 v131, v154, -v106
	v_mul_f32_e32 v130, 0x3fb8aa3b, v130
	v_mul_f32_e32 v131, 0x3fb8aa3b, v131
	v_rcp_f32_e32 v143, v133
	v_exp_f32_e32 v130, v130
	v_exp_f32_e32 v131, v131
	v_mul_f32_e64 v132, v154, -v102
	v_mul_f32_e64 v133, v154, -v98
	v_mul_f32_e32 v132, 0x3fb8aa3b, v132
	v_mul_f32_e32 v133, 0x3fb8aa3b, v133
	v_exp_f32_e32 v132, v132
	v_exp_f32_e32 v133, v133
	v_add_f32_e32 v130, 1.0, v130
	v_add_f32_e32 v131, 1.0, v131
; __device__ __forceinline__ float rcpf_(float x) { float r = __builtin_amdgcn_rcpf(x); asm volatile("s_nop 0" : "+v"(r)); return r; }
; #define EFENCE() asm volatile("" ::: "memory")
;     __device__ __forceinline__ bool operator()(f32x4 (&acc)[2][2][4][2], const pg8::Unit& u, int wr, int wc, int fr, int fq) const {
;     ...
;         } else {
;             const int colb = (pn - 24) * 128 + wc * 32 + 8 * fq;
; #pragma unroll
;             for (int ai = 0; ai < 2; ++ai)
; #pragma unroll
;                 for (int m = 0; m < 4; ++m) { const int row = row0 + ai * 128 + m * 16; const float rsv = RS_AT(ai, m);
;                     f32x4 r0, r1, g0, g1;
; #pragma unroll
;                     for (int j = 0; j < 4; ++j) { const float e00 = 1.0f + __expf(-acc[ai][0][m][0][j] * rsv), e01 = 1.0f + __expf(-acc[ai][0][m][1][j] * rsv), e10 = 1.0f + __expf(-acc[ai][1][m][0][j] * rsv), e11 = 1.0f + __expf(-acc[ai][1][m][1][j] * rsv);
;                         r0[j] = e10 * rcpf_(e00); r1[j] = e11 * rcpf_(e01); g0[j] = rcpf_(e10); g1[j] = rcpf_(e11); }
;                     st8(G + (size_t)row * 2048 + colb, r0, r1); st8(G + (size_t)row * 2048 + 1024 + colb, g0, g1); EFENCE(); }
	v_rcp_f32_e32 v130, v130
	v_rcp_f32_e32 v131, v131
	s_nop 0
	s_nop 0
	v_add_f32_e32 v132, 1.0, v132
	v_add_f32_e32 v133, 1.0, v133
	s_nop 0
	s_nop 0
	v_rcp_f32_e32 v147, v133
	v_mul_f32_e32 v144, v132, v130
	v_mul_f32_e64 v130, v154, -v111
	v_mul_f32_e32 v133, v133, v131
	v_mul_f32_e64 v131, v154, -v107
	v_mul_f32_e32 v130, 0x3fb8aa3b, v130
	v_mul_f32_e32 v131, 0x3fb8aa3b, v131
	v_rcp_f32_e32 v145, v132
	v_exp_f32_e32 v130, v130
	v_exp_f32_e32 v131, v131
	v_mul_f32_e64 v132, v154, -v103
	v_mul_f32_e32 v132, 0x3fb8aa3b, v132
	v_exp_f32_e32 v132, v132
	v_exp_f32_e32 v134, v134
	v_add_f32_e32 v130, 1.0, v130
	v_add_f32_e32 v131, 1.0, v131
	v_rcp_f32_e32 v130, v130
	v_rcp_f32_e32 v131, v131
	s_nop 0
	s_nop 0
	v_add_f32_e32 v132, 1.0, v132
	v_add_f32_e32 v134, 1.0, v134
	s_nop 0
	s_nop 0
	v_rcp_f32_e32 v151, v132
	v_mul_f32_e32 v149, v132, v130
	v_mul_f32_e32 v155, v134, v131
	v_lshlrev_b64 v[130:131], 12, v[196:197]
	v_rcp_f32_e32 v153, v134
	v_lshl_add_u64 v[130:131], s[2:3], 0, v[130:131]
	s_nop 0
	s_nop 0
	v_lshl_add_u64 v[134:135], v[130:131], 0, v[128:129]
	v_cvt_pk_bf16_f32 v130, v136, v140
	v_cvt_pk_bf16_f32 v131, v144, v149
	v_cvt_pk_bf16_f32 v132, v137, v141
	v_cvt_pk_bf16_f32 v133, v133, v155
	v_mul_f32_e64 v136, v202, -v92
	v_mul_f32_e64 v137, v202, -v88
	global_store_dwordx4 v[134:135], v[130:133], off sc1
	v_mul_f32_e32 v136, 0x3fb8aa3b, v136
	v_mul_f32_e32 v137, 0x3fb8aa3b, v137
	v_cvt_pk_bf16_f32 v130, v138, v142
	v_cvt_pk_bf16_f32 v131, v145, v151
	v_cvt_pk_bf16_f32 v132, v139, v143
	v_cvt_pk_bf16_f32 v133, v147, v153
	v_exp_f32_e32 v136, v136
	v_exp_f32_e32 v137, v137
	global_store_dwordx4 v[134:135], v[130:133], off offset:2048 sc1
	v_mul_f32_e64 v134, v202, -v83
	v_mul_f32_e32 v134, 0x3fb8aa3b, v134
	v_mul_f32_e64 v132, v202, -v84
	v_mul_f32_e64 v133, v202, -v80
	v_mul_f32_e32 v132, 0x3fb8aa3b, v132
	v_mul_f32_e32 v133, 0x3fb8aa3b, v133
	v_exp_f32_e32 v132, v132
	v_exp_f32_e32 v133, v133
	v_add_f32_e32 v130, 1.0, v136
	v_add_f32_e32 v131, 1.0, v137
	v_rcp_f32_e32 v130, v130
	v_rcp_f32_e32 v131, v131
	v_add_f32_e32 v132, 1.0, v132
	v_add_f32_e32 v133, 1.0, v133
	s_nop 0
	s_nop 0
	v_rcp_f32_e32 v138, v132
	v_mul_f32_e32 v136, v132, v130
	v_mul_f32_e32 v137, v133, v131
	v_mul_f32_e64 v130, v202, -v93
	v_mul_f32_e64 v131, v202, -v89
	v_mul_f32_e32 v130, 0x3fb8aa3b, v130
	v_mul_f32_e32 v131, 0x3fb8aa3b, v131
	v_rcp_f32_e32 v139, v133
	v_exp_f32_e32 v130, v130
	v_exp_f32_e32 v131, v131
	v_mul_f32_e64 v132, v202, -v85
	v_mul_f32_e64 v133, v202, -v81
	v_mul_f32_e32 v132, 0x3fb8aa3b, v132
	v_mul_f32_e32 v133, 0x3fb8aa3b, v133
	v_exp_f32_e32 v132, v132
	v_exp_f32_e32 v133, v133
	v_add_f32_e32 v130, 1.0, v130
	v_add_f32_e32 v131, 1.0, v131
	v_rcp_f32_e32 v130, v130
	v_rcp_f32_e32 v131, v131
	s_nop 0
	s_nop 0
	v_add_f32_e32 v132, 1.0, v132
	v_add_f32_e32 v133, 1.0, v133
	s_nop 0
	s_nop 0
	v_rcp_f32_e32 v142, v132
	v_mul_f32_e32 v140, v132, v130
	v_mul_f32_e32 v141, v133, v131
	v_mul_f32_e64 v130, v202, -v94
	v_mul_f32_e64 v131, v202, -v90
	v_mul_f32_e32 v130, 0x3fb8aa3b, v130
	v_mul_f32_e32 v131, 0x3fb8aa3b, v131
	v_rcp_f32_e32 v143, v133
	v_exp_f32_e32 v130, v130
	v_exp_f32_e32 v131, v131
	v_mul_f32_e64 v132, v202, -v86
	v_mul_f32_e64 v133, v202, -v82
	v_mul_f32_e32 v132, 0x3fb8aa3b, v132
	v_mul_f32_e32 v133, 0x3fb8aa3b, v133
	v_exp_f32_e32 v132, v132
	v_exp_f32_e32 v133, v133
	v_add_f32_e32 v130, 1.0, v130
	v_add_f32_e32 v131, 1.0, v131
	v_rcp_f32_e32 v130, v130
	v_rcp_f32_e32 v131, v131
	s_nop 0
	s_nop 0
	v_add_f32_e32 v132, 1.0, v132
	v_add_f32_e32 v133, 1.0, v133
	s_nop 0
	s_nop 0
	v_rcp_f32_e32 v147, v133
	v_mul_f32_e32 v144, v132, v130
	v_mul_f32_e64 v130, v202, -v95
	v_mul_f32_e32 v133, v133, v131
	v_mul_f32_e64 v131, v202, -v91
	v_mul_f32_e32 v130, 0x3fb8aa3b, v130
	v_mul_f32_e32 v131, 0x3fb8aa3b, v131
	v_rcp_f32_e32 v145, v132
	v_exp_f32_e32 v130, v130
	v_exp_f32_e32 v131, v131
	v_mul_f32_e64 v132, v202, -v87
	v_mul_f32_e32 v132, 0x3fb8aa3b, v132
	v_exp_f32_e32 v132, v132
	v_exp_f32_e32 v134, v134
	v_add_f32_e32 v130, 1.0, v130
	v_add_f32_e32 v131, 1.0, v131
	v_rcp_f32_e32 v130, v130
	v_rcp_f32_e32 v131, v131
	s_nop 0
	s_nop 0
	v_add_f32_e32 v132, 1.0, v132
	v_add_f32_e32 v134, 1.0, v134
	s_nop 0
	s_nop 0
	v_rcp_f32_e32 v151, v132
	v_mul_f32_e32 v149, v132, v130
	v_mul_f32_e32 v155, v134, v131
	v_lshlrev_b64 v[130:131], 12, v[188:189]
	v_rcp_f32_e32 v153, v134
	v_lshl_add_u64 v[130:131], s[2:3], 0, v[130:131]
	s_nop 0
	s_nop 0
	v_lshl_add_u64 v[134:135], v[130:131], 0, v[128:129]
	v_cvt_pk_bf16_f32 v130, v136, v140
	v_cvt_pk_bf16_f32 v131, v144, v149
	v_cvt_pk_bf16_f32 v132, v137, v141
	v_cvt_pk_bf16_f32 v133, v133, v155
	v_mul_f32_e64 v136, v200, -v76
	v_mul_f32_e64 v137, v200, -v72
	global_store_dwordx4 v[134:135], v[130:133], off sc1
	v_mul_f32_e32 v136, 0x3fb8aa3b, v136
	v_mul_f32_e32 v137, 0x3fb8aa3b, v137
	v_cvt_pk_bf16_f32 v130, v138, v142
	v_cvt_pk_bf16_f32 v131, v145, v151
	v_cvt_pk_bf16_f32 v132, v139, v143
	v_cvt_pk_bf16_f32 v133, v147, v153
	v_exp_f32_e32 v136, v136
	v_exp_f32_e32 v137, v137
	global_store_dwordx4 v[134:135], v[130:133], off offset:2048 sc1
	v_mul_f32_e64 v134, v200, -v67
	v_mul_f32_e32 v134, 0x3fb8aa3b, v134
	v_mul_f32_e64 v132, v200, -v68
	v_mul_f32_e64 v133, v200, -v64
	v_mul_f32_e32 v132, 0x3fb8aa3b, v132
	v_mul_f32_e32 v133, 0x3fb8aa3b, v133
	v_exp_f32_e32 v132, v132
	v_exp_f32_e32 v133, v133
	v_add_f32_e32 v130, 1.0, v136
	v_add_f32_e32 v131, 1.0, v137
	v_rcp_f32_e32 v130, v130
	v_rcp_f32_e32 v131, v131
	v_add_f32_e32 v132, 1.0, v132
	v_add_f32_e32 v133, 1.0, v133
	s_nop 0
	s_nop 0
	v_rcp_f32_e32 v138, v132
	v_mul_f32_e32 v136, v132, v130
	v_mul_f32_e32 v137, v133, v131
	v_mul_f32_e64 v130, v200, -v77
; __device__ __forceinline__ float rcpf_(float x) { float r = __builtin_amdgcn_rcpf(x); asm volatile("s_nop 0" : "+v"(r)); return r; }
; #define EFENCE() asm volatile("" ::: "memory")
;     __device__ __forceinline__ bool operator()(f32x4 (&acc)[2][2][4][2], const pg8::Unit& u, int wr, int wc, int fr, int fq) const {
;     ...
;         } else {
;             const int colb = (pn - 24) * 128 + wc * 32 + 8 * fq;
; #pragma unroll
;             for (int ai = 0; ai < 2; ++ai)
; #pragma unroll
;                 for (int m = 0; m < 4; ++m) { const int row = row0 + ai * 128 + m * 16; const float rsv = RS_AT(ai, m);
;                     f32x4 r0, r1, g0, g1;
; #pragma unroll
;                     for (int j = 0; j < 4; ++j) { const float e00 = 1.0f + __expf(-acc[ai][0][m][0][j] * rsv), e01 = 1.0f + __expf(-acc[ai][0][m][1][j] * rsv), e10 = 1.0f + __expf(-acc[ai][1][m][0][j] * rsv), e11 = 1.0f + __expf(-acc[ai][1][m][1][j] * rsv);
;                         r0[j] = e10 * rcpf_(e00); r1[j] = e11 * rcpf_(e01); g0[j] = rcpf_(e10); g1[j] = rcpf_(e11); }
;                     st8(G + (size_t)row * 2048 + colb, r0, r1); st8(G + (size_t)row * 2048 + 1024 + colb, g0, g1); EFENCE(); }
	v_mul_f32_e64 v131, v200, -v73
	v_mul_f32_e32 v130, 0x3fb8aa3b, v130
	v_mul_f32_e32 v131, 0x3fb8aa3b, v131
	v_rcp_f32_e32 v139, v133
	v_exp_f32_e32 v130, v130
	v_exp_f32_e32 v131, v131
	v_mul_f32_e64 v132, v200, -v69
	v_mul_f32_e64 v133, v200, -v65
	v_mul_f32_e32 v132, 0x3fb8aa3b, v132
	v_mul_f32_e32 v133, 0x3fb8aa3b, v133
	v_exp_f32_e32 v132, v132
	v_exp_f32_e32 v133, v133
	v_add_f32_e32 v130, 1.0, v130
	v_add_f32_e32 v131, 1.0, v131
	v_rcp_f32_e32 v130, v130
	v_rcp_f32_e32 v131, v131
	s_nop 0
	s_nop 0
	v_add_f32_e32 v132, 1.0, v132
	v_add_f32_e32 v133, 1.0, v133
	s_nop 0
	s_nop 0
	v_rcp_f32_e32 v142, v132
	v_mul_f32_e32 v140, v132, v130
	v_mul_f32_e32 v141, v133, v131
	v_mul_f32_e64 v130, v200, -v78
	v_mul_f32_e64 v131, v200, -v74
	v_mul_f32_e32 v130, 0x3fb8aa3b, v130
	v_mul_f32_e32 v131, 0x3fb8aa3b, v131
	v_rcp_f32_e32 v143, v133
	v_exp_f32_e32 v130, v130
	v_exp_f32_e32 v131, v131
	v_mul_f32_e64 v132, v200, -v70
	v_mul_f32_e64 v133, v200, -v66
	v_mul_f32_e32 v132, 0x3fb8aa3b, v132
	v_mul_f32_e32 v133, 0x3fb8aa3b, v133
	v_exp_f32_e32 v132, v132
	v_exp_f32_e32 v133, v133
	v_add_f32_e32 v130, 1.0, v130
	v_add_f32_e32 v131, 1.0, v131
	v_rcp_f32_e32 v130, v130
	v_rcp_f32_e32 v131, v131
	s_nop 0
	s_nop 0
	v_add_f32_e32 v132, 1.0, v132
	v_add_f32_e32 v133, 1.0, v133
	s_nop 0
	s_nop 0
	v_rcp_f32_e32 v147, v133
	v_mul_f32_e32 v144, v132, v130
	v_mul_f32_e64 v130, v200, -v79
	v_mul_f32_e32 v133, v133, v131
	v_mul_f32_e64 v131, v200, -v75
	v_mul_f32_e32 v130, 0x3fb8aa3b, v130
	v_mul_f32_e32 v131, 0x3fb8aa3b, v131
	v_rcp_f32_e32 v145, v132
	v_exp_f32_e32 v130, v130
	v_exp_f32_e32 v131, v131
	v_mul_f32_e64 v132, v200, -v71
	v_mul_f32_e32 v132, 0x3fb8aa3b, v132
	v_exp_f32_e32 v132, v132
	v_exp_f32_e32 v134, v134
	v_add_f32_e32 v130, 1.0, v130
	v_add_f32_e32 v131, 1.0, v131
	v_rcp_f32_e32 v130, v130
	v_rcp_f32_e32 v131, v131
	s_nop 0
	s_nop 0
	v_add_f32_e32 v132, 1.0, v132
	v_add_f32_e32 v134, 1.0, v134
	s_nop 0
	s_nop 0
	v_rcp_f32_e32 v151, v132
	v_mul_f32_e32 v149, v132, v130
	v_mul_f32_e32 v155, v134, v131
	v_lshlrev_b64 v[130:131], 12, v[186:187]
	v_rcp_f32_e32 v153, v134
	v_lshl_add_u64 v[130:131], s[2:3], 0, v[130:131]
	s_nop 0
	s_nop 0
	v_lshl_add_u64 v[134:135], v[130:131], 0, v[128:129]
	v_cvt_pk_bf16_f32 v130, v136, v140
	v_cvt_pk_bf16_f32 v131, v144, v149
	v_cvt_pk_bf16_f32 v132, v137, v141
	v_cvt_pk_bf16_f32 v133, v133, v155
	v_mul_f32_e64 v136, v152, -v60
	v_mul_f32_e64 v137, v152, -v56
	global_store_dwordx4 v[134:135], v[130:133], off sc1
	v_mul_f32_e32 v136, 0x3fb8aa3b, v136
	v_mul_f32_e32 v137, 0x3fb8aa3b, v137
	v_cvt_pk_bf16_f32 v130, v138, v142
	v_cvt_pk_bf16_f32 v131, v145, v151
	v_cvt_pk_bf16_f32 v132, v139, v143
	v_cvt_pk_bf16_f32 v133, v147, v153
	v_exp_f32_e32 v136, v136
	v_exp_f32_e32 v137, v137
	global_store_dwordx4 v[134:135], v[130:133], off offset:2048 sc1
	v_mul_f32_e64 v134, v152, -v51
	v_mul_f32_e32 v134, 0x3fb8aa3b, v134
	v_mul_f32_e64 v132, v152, -v52
	v_mul_f32_e64 v133, v152, -v48
	v_mul_f32_e32 v132, 0x3fb8aa3b, v132
	v_mul_f32_e32 v133, 0x3fb8aa3b, v133
	v_exp_f32_e32 v132, v132
	v_exp_f32_e32 v133, v133
	v_add_f32_e32 v130, 1.0, v136
	v_add_f32_e32 v131, 1.0, v137
	v_rcp_f32_e32 v130, v130
	v_rcp_f32_e32 v131, v131
	v_add_f32_e32 v132, 1.0, v132
	v_add_f32_e32 v133, 1.0, v133
	s_nop 0
	s_nop 0
	v_rcp_f32_e32 v138, v132
	v_mul_f32_e32 v136, v132, v130
	v_mul_f32_e32 v137, v133, v131
	v_mul_f32_e64 v130, v152, -v61
	v_mul_f32_e64 v131, v152, -v57
	v_mul_f32_e32 v130, 0x3fb8aa3b, v130
	v_mul_f32_e32 v131, 0x3fb8aa3b, v131
	v_rcp_f32_e32 v139, v133
	v_exp_f32_e32 v130, v130
	v_exp_f32_e32 v131, v131
	v_mul_f32_e64 v132, v152, -v53
	v_mul_f32_e64 v133, v152, -v49
	v_mul_f32_e32 v132, 0x3fb8aa3b, v132
	v_mul_f32_e32 v133, 0x3fb8aa3b, v133
	v_exp_f32_e32 v132, v132
	v_exp_f32_e32 v133, v133
	v_add_f32_e32 v130, 1.0, v130
	v_add_f32_e32 v131, 1.0, v131
	v_rcp_f32_e32 v130, v130
	v_rcp_f32_e32 v131, v131
	s_nop 0
	s_nop 0
	v_add_f32_e32 v132, 1.0, v132
	v_add_f32_e32 v133, 1.0, v133
	s_nop 0
	s_nop 0
	v_rcp_f32_e32 v142, v132
	v_mul_f32_e32 v140, v132, v130
	v_mul_f32_e32 v141, v133, v131
	v_mul_f32_e64 v130, v152, -v62
	v_mul_f32_e64 v131, v152, -v58
	v_mul_f32_e32 v130, 0x3fb8aa3b, v130
	v_mul_f32_e32 v131, 0x3fb8aa3b, v131
	v_rcp_f32_e32 v143, v133
	v_exp_f32_e32 v130, v130
	v_exp_f32_e32 v131, v131
	v_mul_f32_e64 v132, v152, -v54
	v_mul_f32_e64 v133, v152, -v50
	v_mul_f32_e32 v132, 0x3fb8aa3b, v132
	v_mul_f32_e32 v133, 0x3fb8aa3b, v133
	v_exp_f32_e32 v132, v132
	v_exp_f32_e32 v133, v133
	v_add_f32_e32 v130, 1.0, v130
	v_add_f32_e32 v131, 1.0, v131
	v_rcp_f32_e32 v130, v130
	v_rcp_f32_e32 v131, v131
	s_nop 0
	s_nop 0
	v_add_f32_e32 v132, 1.0, v132
	v_add_f32_e32 v133, 1.0, v133
	s_nop 0
	s_nop 0
	v_rcp_f32_e32 v147, v133
	v_mul_f32_e32 v144, v132, v130
	v_mul_f32_e64 v130, v152, -v63
	v_mul_f32_e32 v133, v133, v131
	v_mul_f32_e64 v131, v152, -v59
	v_mul_f32_e32 v130, 0x3fb8aa3b, v130
	v_mul_f32_e32 v131, 0x3fb8aa3b, v131
	v_rcp_f32_e32 v145, v132
	v_exp_f32_e32 v130, v130
	v_exp_f32_e32 v131, v131
	v_mul_f32_e64 v132, v152, -v55
	v_mul_f32_e32 v132, 0x3fb8aa3b, v132
	v_exp_f32_e32 v132, v132
	v_exp_f32_e32 v134, v134
	v_add_f32_e32 v130, 1.0, v130
	v_add_f32_e32 v131, 1.0, v131
	v_rcp_f32_e32 v130, v130
	v_rcp_f32_e32 v131, v131
	s_nop 0
	s_nop 0
	v_add_f32_e32 v132, 1.0, v132
	v_add_f32_e32 v134, 1.0, v134
	s_nop 0
	s_nop 0
	v_rcp_f32_e32 v151, v132
	v_mul_f32_e32 v149, v132, v130
	v_mul_f32_e32 v155, v134, v131
	v_lshlrev_b64 v[130:131], 12, v[182:183]
	v_rcp_f32_e32 v153, v134
	v_lshl_add_u64 v[130:131], s[2:3], 0, v[130:131]
	s_nop 0
	s_nop 0
	v_lshl_add_u64 v[134:135], v[130:131], 0, v[128:129]
; __device__ __forceinline__ float rcpf_(float x) { float r = __builtin_amdgcn_rcpf(x); asm volatile("s_nop 0" : "+v"(r)); return r; }
; #define EFENCE() asm volatile("" ::: "memory")
;     __device__ __forceinline__ bool operator()(f32x4 (&acc)[2][2][4][2], const pg8::Unit& u, int wr, int wc, int fr, int fq) const {
;     ...
;         } else {
;             const int colb = (pn - 24) * 128 + wc * 32 + 8 * fq;
; #pragma unroll
;             for (int ai = 0; ai < 2; ++ai)
; #pragma unroll
;                 for (int m = 0; m < 4; ++m) { const int row = row0 + ai * 128 + m * 16; const float rsv = RS_AT(ai, m);
;                     f32x4 r0, r1, g0, g1;
; #pragma unroll
;                     for (int j = 0; j < 4; ++j) { const float e00 = 1.0f + __expf(-acc[ai][0][m][0][j] * rsv), e01 = 1.0f + __expf(-acc[ai][0][m][1][j] * rsv), e10 = 1.0f + __expf(-acc[ai][1][m][0][j] * rsv), e11 = 1.0f + __expf(-acc[ai][1][m][1][j] * rsv);
;                         r0[j] = e10 * rcpf_(e00); r1[j] = e11 * rcpf_(e01); g0[j] = rcpf_(e10); g1[j] = rcpf_(e11); }
;                     st8(G + (size_t)row * 2048 + colb, r0, r1); st8(G + (size_t)row * 2048 + 1024 + colb, g0, g1); EFENCE(); }
	v_cvt_pk_bf16_f32 v130, v136, v140
	v_cvt_pk_bf16_f32 v131, v144, v149
	v_cvt_pk_bf16_f32 v132, v137, v141
	v_cvt_pk_bf16_f32 v133, v133, v155
	v_mul_f32_e64 v136, v150, -v44
	v_mul_f32_e64 v137, v150, -v40
	global_store_dwordx4 v[134:135], v[130:133], off sc1
	v_mul_f32_e32 v136, 0x3fb8aa3b, v136
	v_mul_f32_e32 v137, 0x3fb8aa3b, v137
	v_cvt_pk_bf16_f32 v130, v138, v142
	v_cvt_pk_bf16_f32 v131, v145, v151
	v_cvt_pk_bf16_f32 v132, v139, v143
	v_cvt_pk_bf16_f32 v133, v147, v153
	v_exp_f32_e32 v136, v136
	v_exp_f32_e32 v137, v137
	global_store_dwordx4 v[134:135], v[130:133], off offset:2048 sc1
	v_mul_f32_e64 v134, v150, -v35
	v_mul_f32_e32 v134, 0x3fb8aa3b, v134
	v_mul_f32_e64 v132, v150, -v36
	v_mul_f32_e64 v133, v150, -v32
	v_mul_f32_e32 v132, 0x3fb8aa3b, v132
	v_mul_f32_e32 v133, 0x3fb8aa3b, v133
	v_exp_f32_e32 v132, v132
	v_exp_f32_e32 v133, v133
	v_add_f32_e32 v130, 1.0, v136
	v_add_f32_e32 v131, 1.0, v137
	v_rcp_f32_e32 v130, v130
	v_rcp_f32_e32 v131, v131
	v_add_f32_e32 v132, 1.0, v132
	v_add_f32_e32 v133, 1.0, v133
	s_nop 0
	s_nop 0
	v_rcp_f32_e32 v138, v132
	v_mul_f32_e32 v136, v132, v130
	v_mul_f32_e32 v137, v133, v131
	v_mul_f32_e64 v130, v150, -v45
	v_mul_f32_e64 v131, v150, -v41
	v_mul_f32_e32 v130, 0x3fb8aa3b, v130
	v_mul_f32_e32 v131, 0x3fb8aa3b, v131
	v_rcp_f32_e32 v139, v133
	v_exp_f32_e32 v130, v130
	v_exp_f32_e32 v131, v131
	v_mul_f32_e64 v132, v150, -v37
	v_mul_f32_e64 v133, v150, -v33
	v_mul_f32_e32 v132, 0x3fb8aa3b, v132
	v_mul_f32_e32 v133, 0x3fb8aa3b, v133
	v_exp_f32_e32 v132, v132
	v_exp_f32_e32 v133, v133
	v_add_f32_e32 v130, 1.0, v130
	v_add_f32_e32 v131, 1.0, v131
	v_rcp_f32_e32 v130, v130
	v_rcp_f32_e32 v131, v131
	s_nop 0
	s_nop 0
	v_add_f32_e32 v132, 1.0, v132
	v_add_f32_e32 v133, 1.0, v133
	s_nop 0
	s_nop 0
	v_rcp_f32_e32 v142, v132
	v_mul_f32_e32 v140, v132, v130
	v_mul_f32_e32 v141, v133, v131
	v_mul_f32_e64 v130, v150, -v46
	v_mul_f32_e64 v131, v150, -v42
	v_mul_f32_e32 v130, 0x3fb8aa3b, v130
	v_mul_f32_e32 v131, 0x3fb8aa3b, v131
	v_rcp_f32_e32 v143, v133
	v_exp_f32_e32 v130, v130
	v_exp_f32_e32 v131, v131
	v_mul_f32_e64 v132, v150, -v38
	v_mul_f32_e64 v133, v150, -v34
	v_mul_f32_e32 v132, 0x3fb8aa3b, v132
	v_mul_f32_e32 v133, 0x3fb8aa3b, v133
	v_exp_f32_e32 v132, v132
	v_exp_f32_e32 v133, v133
	v_add_f32_e32 v130, 1.0, v130
	v_add_f32_e32 v131, 1.0, v131
	v_rcp_f32_e32 v130, v130
	v_rcp_f32_e32 v131, v131
	s_nop 0
	s_nop 0
	v_add_f32_e32 v132, 1.0, v132
	v_add_f32_e32 v133, 1.0, v133
	s_nop 0
	s_nop 0
	v_rcp_f32_e32 v147, v133
	v_mul_f32_e32 v144, v132, v130
	v_mul_f32_e64 v130, v150, -v47
	v_mul_f32_e32 v133, v133, v131
	v_mul_f32_e64 v131, v150, -v43
	v_mul_f32_e32 v130, 0x3fb8aa3b, v130
	v_mul_f32_e32 v131, 0x3fb8aa3b, v131
	v_rcp_f32_e32 v145, v132
	v_exp_f32_e32 v130, v130
	v_exp_f32_e32 v131, v131
	v_mul_f32_e64 v132, v150, -v39
	v_mul_f32_e32 v132, 0x3fb8aa3b, v132
	v_exp_f32_e32 v132, v132
	v_exp_f32_e32 v134, v134
	v_add_f32_e32 v130, 1.0, v130
	v_add_f32_e32 v131, 1.0, v131
	v_rcp_f32_e32 v130, v130
	v_rcp_f32_e32 v131, v131
	s_nop 0
	s_nop 0
	v_add_f32_e32 v132, 1.0, v132
	v_add_f32_e32 v134, 1.0, v134
	s_nop 0
	s_nop 0
	v_rcp_f32_e32 v151, v132
	v_mul_f32_e32 v149, v132, v130
	v_mul_f32_e32 v155, v134, v131
	v_lshlrev_b64 v[130:131], 12, v[180:181]
	v_rcp_f32_e32 v153, v134
	v_lshl_add_u64 v[130:131], s[2:3], 0, v[130:131]
	s_nop 0
	s_nop 0
	v_lshl_add_u64 v[134:135], v[130:131], 0, v[128:129]
	v_cvt_pk_bf16_f32 v130, v136, v140
	v_cvt_pk_bf16_f32 v131, v144, v149
	v_cvt_pk_bf16_f32 v132, v137, v141
	v_cvt_pk_bf16_f32 v133, v133, v155
	v_mul_f32_e64 v136, v148, -v28
	v_mul_f32_e64 v137, v148, -v24
	global_store_dwordx4 v[134:135], v[130:133], off sc1
	v_mul_f32_e32 v136, 0x3fb8aa3b, v136
	v_mul_f32_e32 v137, 0x3fb8aa3b, v137
	v_cvt_pk_bf16_f32 v130, v138, v142
	v_cvt_pk_bf16_f32 v131, v145, v151
	v_cvt_pk_bf16_f32 v132, v139, v143
	v_cvt_pk_bf16_f32 v133, v147, v153
	v_exp_f32_e32 v136, v136
	v_exp_f32_e32 v137, v137
	global_store_dwordx4 v[134:135], v[130:133], off offset:2048 sc1
	v_mul_f32_e64 v134, v148, -v19
	v_mul_f32_e32 v134, 0x3fb8aa3b, v134
	v_mul_f32_e64 v132, v148, -v20
	v_mul_f32_e64 v133, v148, -v16
	v_mul_f32_e32 v132, 0x3fb8aa3b, v132
	v_mul_f32_e32 v133, 0x3fb8aa3b, v133
	v_exp_f32_e32 v132, v132
	v_exp_f32_e32 v133, v133
	v_add_f32_e32 v130, 1.0, v136
	v_add_f32_e32 v131, 1.0, v137
	v_rcp_f32_e32 v130, v130
	v_rcp_f32_e32 v131, v131
	v_add_f32_e32 v132, 1.0, v132
	v_add_f32_e32 v133, 1.0, v133
	s_nop 0
	s_nop 0
	v_rcp_f32_e32 v138, v132
	v_mul_f32_e32 v136, v132, v130
	v_mul_f32_e32 v137, v133, v131
	v_mul_f32_e64 v130, v148, -v29
	v_mul_f32_e64 v131, v148, -v25
	v_mul_f32_e32 v130, 0x3fb8aa3b, v130
	v_mul_f32_e32 v131, 0x3fb8aa3b, v131
	v_rcp_f32_e32 v139, v133
	v_exp_f32_e32 v130, v130
	v_exp_f32_e32 v131, v131
	v_mul_f32_e64 v132, v148, -v21
	v_mul_f32_e64 v133, v148, -v17
	v_mul_f32_e32 v132, 0x3fb8aa3b, v132
	v_mul_f32_e32 v133, 0x3fb8aa3b, v133
	v_exp_f32_e32 v132, v132
	v_exp_f32_e32 v133, v133
	v_add_f32_e32 v130, 1.0, v130
	v_add_f32_e32 v131, 1.0, v131
	v_rcp_f32_e32 v130, v130
	v_rcp_f32_e32 v131, v131
	s_nop 0
	s_nop 0
	v_add_f32_e32 v132, 1.0, v132
	v_add_f32_e32 v133, 1.0, v133
	s_nop 0
	s_nop 0
	v_rcp_f32_e32 v142, v132
	v_mul_f32_e32 v140, v132, v130
	v_mul_f32_e32 v141, v133, v131
	v_mul_f32_e64 v130, v148, -v30
	v_mul_f32_e64 v131, v148, -v26
	v_mul_f32_e32 v130, 0x3fb8aa3b, v130
	v_mul_f32_e32 v131, 0x3fb8aa3b, v131
	v_rcp_f32_e32 v143, v133
	v_exp_f32_e32 v130, v130
	v_exp_f32_e32 v131, v131
	v_mul_f32_e64 v132, v148, -v22
	v_mul_f32_e64 v133, v148, -v18
	v_mul_f32_e32 v132, 0x3fb8aa3b, v132
	v_mul_f32_e32 v133, 0x3fb8aa3b, v133
	v_exp_f32_e32 v132, v132
; __device__ __forceinline__ float rcpf_(float x) { float r = __builtin_amdgcn_rcpf(x); asm volatile("s_nop 0" : "+v"(r)); return r; }
; #define EFENCE() asm volatile("" ::: "memory")
;     __device__ __forceinline__ bool operator()(f32x4 (&acc)[2][2][4][2], const pg8::Unit& u, int wr, int wc, int fr, int fq) const {
;     ...
;         } else {
;             const int colb = (pn - 24) * 128 + wc * 32 + 8 * fq;
; #pragma unroll
;             for (int ai = 0; ai < 2; ++ai)
; #pragma unroll
;                 for (int m = 0; m < 4; ++m) { const int row = row0 + ai * 128 + m * 16; const float rsv = RS_AT(ai, m);
;                     f32x4 r0, r1, g0, g1;
; #pragma unroll
;                     for (int j = 0; j < 4; ++j) { const float e00 = 1.0f + __expf(-acc[ai][0][m][0][j] * rsv), e01 = 1.0f + __expf(-acc[ai][0][m][1][j] * rsv), e10 = 1.0f + __expf(-acc[ai][1][m][0][j] * rsv), e11 = 1.0f + __expf(-acc[ai][1][m][1][j] * rsv);
;                         r0[j] = e10 * rcpf_(e00); r1[j] = e11 * rcpf_(e01); g0[j] = rcpf_(e10); g1[j] = rcpf_(e11); }
;                     st8(G + (size_t)row * 2048 + colb, r0, r1); st8(G + (size_t)row * 2048 + 1024 + colb, g0, g1); EFENCE(); }
	v_exp_f32_e32 v133, v133
	v_add_f32_e32 v130, 1.0, v130
	v_add_f32_e32 v131, 1.0, v131
	v_rcp_f32_e32 v130, v130
	v_rcp_f32_e32 v131, v131
	s_nop 0
	s_nop 0
	v_add_f32_e32 v132, 1.0, v132
	v_add_f32_e32 v133, 1.0, v133
	s_nop 0
	s_nop 0
	v_rcp_f32_e32 v147, v133
	v_mul_f32_e32 v144, v132, v130
	v_mul_f32_e64 v130, v148, -v31
	v_mul_f32_e32 v133, v133, v131
	v_mul_f32_e64 v131, v148, -v27
	v_mul_f32_e32 v130, 0x3fb8aa3b, v130
	v_mul_f32_e32 v131, 0x3fb8aa3b, v131
	v_rcp_f32_e32 v145, v132
	v_exp_f32_e32 v130, v130
	v_exp_f32_e32 v131, v131
	v_mul_f32_e64 v132, v148, -v23
	v_mul_f32_e32 v132, 0x3fb8aa3b, v132
	v_exp_f32_e32 v132, v132
	v_exp_f32_e32 v134, v134
	v_add_f32_e32 v130, 1.0, v130
	v_add_f32_e32 v131, 1.0, v131
	v_rcp_f32_e32 v130, v130
	v_rcp_f32_e32 v131, v131
	s_nop 0
	s_nop 0
	v_add_f32_e32 v132, 1.0, v132
	v_add_f32_e32 v134, 1.0, v134
	s_nop 0
	s_nop 0
	v_rcp_f32_e32 v151, v132
	v_mul_f32_e32 v149, v132, v130
	v_mul_f32_e32 v155, v134, v131
	v_lshlrev_b64 v[130:131], 12, v[178:179]
	v_rcp_f32_e32 v153, v134
	v_lshl_add_u64 v[130:131], s[2:3], 0, v[130:131]
	s_nop 0
	s_nop 0
	v_lshl_add_u64 v[134:135], v[130:131], 0, v[128:129]
	v_cvt_pk_bf16_f32 v130, v136, v140
	v_cvt_pk_bf16_f32 v131, v144, v149
	v_cvt_pk_bf16_f32 v132, v137, v141
	v_cvt_pk_bf16_f32 v133, v133, v155
	v_mul_f32_e64 v136, v146, -v12
	v_mul_f32_e64 v137, v146, -v8
	global_store_dwordx4 v[134:135], v[130:133], off sc1
	v_mul_f32_e32 v136, 0x3fb8aa3b, v136
	v_mul_f32_e32 v137, 0x3fb8aa3b, v137
	v_cvt_pk_bf16_f32 v130, v138, v142
	v_cvt_pk_bf16_f32 v131, v145, v151
	v_cvt_pk_bf16_f32 v132, v139, v143
	v_cvt_pk_bf16_f32 v133, v147, v153
	v_exp_f32_e32 v136, v136
	v_exp_f32_e32 v137, v137
	global_store_dwordx4 v[134:135], v[130:133], off offset:2048 sc1
	s_nop 1
	v_mul_f32_e64 v132, v146, -v4
	v_mul_f32_e64 v133, v146, -v0
	v_mul_f32_e32 v132, 0x3fb8aa3b, v132
	v_mul_f32_e32 v133, 0x3fb8aa3b, v133
	v_exp_f32_e32 v132, v132
	v_exp_f32_e32 v133, v133
	v_add_f32_e32 v130, 1.0, v136
	v_add_f32_e32 v131, 1.0, v137
	v_rcp_f32_e32 v130, v130
	v_rcp_f32_e32 v131, v131
	v_add_f32_e32 v132, 1.0, v132
	v_add_f32_e32 v133, 1.0, v133
	s_nop 0
	s_nop 0
	v_rcp_f32_e32 v136, v132
	v_mul_f32_e32 v134, v132, v130
	v_mul_f32_e32 v135, v133, v131
	v_mul_f32_e64 v130, v146, -v13
	v_mul_f32_e64 v131, v146, -v9
	v_mul_f32_e32 v130, 0x3fb8aa3b, v130
	v_mul_f32_e32 v131, 0x3fb8aa3b, v131
	v_rcp_f32_e32 v137, v133
	v_exp_f32_e32 v130, v130
	v_exp_f32_e32 v131, v131
	v_mul_f32_e64 v132, v146, -v5
	v_mul_f32_e64 v133, v146, -v1
	v_mul_f32_e32 v132, 0x3fb8aa3b, v132
	v_mul_f32_e32 v133, 0x3fb8aa3b, v133
	v_exp_f32_e32 v132, v132
	v_exp_f32_e32 v133, v133
	v_add_f32_e32 v130, 1.0, v130
	v_add_f32_e32 v131, 1.0, v131
	v_rcp_f32_e32 v130, v130
	v_rcp_f32_e32 v131, v131
	s_nop 0
	s_nop 0
	v_add_f32_e32 v132, 1.0, v132
	v_add_f32_e32 v133, 1.0, v133
	s_nop 0
	s_nop 0
	v_rcp_f32_e32 v140, v132
	v_mul_f32_e32 v138, v132, v130
	v_mul_f32_e32 v139, v133, v131
	v_mul_f32_e64 v130, v146, -v14
	v_mul_f32_e64 v131, v146, -v10
	v_mul_f32_e32 v130, 0x3fb8aa3b, v130
	v_mul_f32_e32 v131, 0x3fb8aa3b, v131
	v_rcp_f32_e32 v141, v133
	v_exp_f32_e32 v130, v130
	v_exp_f32_e32 v131, v131
	v_mul_f32_e64 v132, v146, -v6
	v_mul_f32_e64 v133, v146, -v2
	v_mul_f32_e32 v132, 0x3fb8aa3b, v132
	v_mul_f32_e32 v133, 0x3fb8aa3b, v133
	v_exp_f32_e32 v132, v132
	v_exp_f32_e32 v133, v133
	v_add_f32_e32 v130, 1.0, v130
	v_add_f32_e32 v131, 1.0, v131
	v_rcp_f32_e32 v130, v130
	v_rcp_f32_e32 v131, v131
	s_nop 0
	s_nop 0
	v_add_f32_e32 v132, 1.0, v132
	v_add_f32_e32 v133, 1.0, v133
	s_nop 0
	s_nop 0
	v_rcp_f32_e32 v143, v132
	v_mul_f32_e32 v142, v132, v130
	v_mul_f32_e64 v130, v146, -v15
	v_mul_f32_e32 v145, v133, v131
	v_mul_f32_e64 v131, v146, -v11
	v_mul_f32_e32 v130, 0x3fb8aa3b, v130
	v_mul_f32_e32 v131, 0x3fb8aa3b, v131
	v_rcp_f32_e32 v144, v133
	v_exp_f32_e32 v130, v130
	v_exp_f32_e32 v131, v131
	v_mul_f32_e64 v132, v146, -v7
	v_mul_f32_e64 v133, v146, -v3
	v_mul_f32_e32 v132, 0x3fb8aa3b, v132
	v_mul_f32_e32 v133, 0x3fb8aa3b, v133
	v_exp_f32_e32 v132, v132
	v_exp_f32_e32 v133, v133
	v_add_f32_e32 v130, 1.0, v130
	v_add_f32_e32 v131, 1.0, v131
	v_rcp_f32_e32 v130, v130
	v_rcp_f32_e32 v131, v131
	s_nop 0
	s_nop 0
	v_add_f32_e32 v132, 1.0, v132
	v_add_f32_e32 v133, 1.0, v133
	s_nop 0
	s_nop 0
	v_rcp_f32_e32 v149, v132
	v_mul_f32_e32 v147, v132, v130
	v_mul_f32_e32 v153, v133, v131
	v_lshlrev_b64 v[130:131], 12, v[176:177]
	v_rcp_f32_e32 v151, v133
	v_lshl_add_u64 v[130:131], s[2:3], 0, v[130:131]
	s_nop 0
	s_nop 0
	v_lshl_add_u64 v[132:133], v[130:131], 0, v[128:129]
	v_cvt_pk_bf16_f32 v128, v134, v138
	v_cvt_pk_bf16_f32 v129, v142, v147
	v_cvt_pk_bf16_f32 v130, v135, v139
	v_cvt_pk_bf16_f32 v131, v145, v153
	global_store_dwordx4 v[132:133], v[128:131], off sc1
	s_nop 1
	v_cvt_pk_bf16_f32 v128, v136, v140
	v_cvt_pk_bf16_f32 v129, v143, v149
	v_cvt_pk_bf16_f32 v130, v137, v141
	v_cvt_pk_bf16_f32 v131, v144, v151
	global_store_dwordx4 v[132:133], v[128:131], off offset:2048 sc1
;     __device__ __forceinline__ bool operator()(f32x4 (&acc)[2][2][4][2], const pg8::Unit& u, int wr, int wc, int fr, int fq) const {
;     ...
;         } else if (pn < 24) {
;             const int colb = (pn - 16) * 128 + wc * 32 + 8 * fq;
; #pragma unroll
;             for (int ai = 0; ai < 2; ++ai)
; #pragma unroll
;                 for (int m = 0; m < 4; ++m) { const int row = row0 + ai * 128 + m * 16; const float rsv = RS_AT(ai, m); const float r2 = rsv * rsv;
;                     st8(U + (size_t)row * DM + colb, acc[ai][0][m][0] * acc[ai][1][m][0] * r2, acc[ai][0][m][1] * acc[ai][1][m][1] * r2); }
.LBB0_729:
	s_andn2_b64 vcc, exec, s[4:5]
	s_cbranch_vccnz .LBB0_731
	v_readlane_b32 s2, v251, 46
	v_add_u32_e32 v160, s11, v214
	v_lshlrev_b64 v[128:129], 11, v[184:185]
	v_readlane_b32 s3, v251, 47
	v_mul_f32_e32 v130, v198, v198
	v_pk_mul_f32 v[136:137], v[124:125], v[116:117]
	v_lshl_add_u64 v[132:133], s[2:3], 0, v[128:129]
	v_lshlrev_b64 v[128:129], 1, v[160:161]
	v_lshl_add_u64 v[134:135], v[132:133], 0, v[128:129]
	v_pk_mul_f32 v[132:133], v[126:127], v[118:119]
	v_pk_mul_f32 v[138:139], v[122:123], v[114:115]
	v_pk_mul_f32 v[132:133], v[132:133], v[130:131] op_sel_hi:[1,0]
	v_pk_mul_f32 v[140:141], v[120:121], v[112:113]
	v_pk_mul_f32 v[136:137], v[136:137], v[130:131] op_sel_hi:[1,0]
	v_pk_mul_f32 v[138:139], v[138:139], v[130:131] op_sel_hi:[1,0]
	v_pk_mul_f32 v[140:141], v[140:141], v[130:131] op_sel_hi:[1,0]
	v_cvt_pk_bf16_f32 v130, v136, v137
	v_cvt_pk_bf16_f32 v131, v132, v133
	v_pk_mul_f32 v[136:137], v[108:109], v[100:101]
	v_cvt_pk_bf16_f32 v132, v140, v141
	v_cvt_pk_bf16_f32 v133, v138, v139
	global_store_dwordx4 v[134:135], v[130:133], off sc1
	v_pk_mul_f32 v[138:139], v[106:107], v[98:99]
	v_pk_mul_f32 v[140:141], v[104:105], v[96:97]
	v_lshlrev_b64 v[132:133], 11, v[196:197]
	v_lshl_add_u64 v[132:133], s[2:3], 0, v[132:133]
	v_mul_f32_e32 v130, v154, v154
	v_lshl_add_u64 v[134:135], v[132:133], 0, v[128:129]
	v_pk_mul_f32 v[132:133], v[110:111], v[102:103]
	v_pk_mul_f32 v[136:137], v[136:137], v[130:131] op_sel_hi:[1,0]
	v_pk_mul_f32 v[132:133], v[132:133], v[130:131] op_sel_hi:[1,0]
	v_pk_mul_f32 v[138:139], v[138:139], v[130:131] op_sel_hi:[1,0]
	v_pk_mul_f32 v[140:141], v[140:141], v[130:131] op_sel_hi:[1,0]
	v_cvt_pk_bf16_f32 v130, v136, v137
	v_cvt_pk_bf16_f32 v131, v132, v133
	v_pk_mul_f32 v[136:137], v[92:93], v[84:85]
	v_cvt_pk_bf16_f32 v132, v140, v141
	v_cvt_pk_bf16_f32 v133, v138, v139
	global_store_dwordx4 v[134:135], v[130:133], off sc1
	v_pk_mul_f32 v[138:139], v[90:91], v[82:83]
	v_pk_mul_f32 v[140:141], v[88:89], v[80:81]
	v_lshlrev_b64 v[132:133], 11, v[188:189]
	v_lshl_add_u64 v[132:133], s[2:3], 0, v[132:133]
	v_mul_f32_e32 v130, v202, v202
	v_lshl_add_u64 v[134:135], v[132:133], 0, v[128:129]
	v_pk_mul_f32 v[132:133], v[94:95], v[86:87]
	v_pk_mul_f32 v[136:137], v[136:137], v[130:131] op_sel_hi:[1,0]
	v_pk_mul_f32 v[132:133], v[132:133], v[130:131] op_sel_hi:[1,0]
	v_pk_mul_f32 v[138:139], v[138:139], v[130:131] op_sel_hi:[1,0]
	v_pk_mul_f32 v[140:141], v[140:141], v[130:131] op_sel_hi:[1,0]
	v_cvt_pk_bf16_f32 v130, v136, v137
	v_cvt_pk_bf16_f32 v131, v132, v133
	v_pk_mul_f32 v[136:137], v[76:77], v[68:69]
	v_cvt_pk_bf16_f32 v132, v140, v141
	v_cvt_pk_bf16_f32 v133, v138, v139
	global_store_dwordx4 v[134:135], v[130:133], off sc1
	v_pk_mul_f32 v[138:139], v[74:75], v[66:67]
	v_pk_mul_f32 v[140:141], v[72:73], v[64:65]
	v_lshlrev_b64 v[132:133], 11, v[186:187]
	v_lshl_add_u64 v[132:133], s[2:3], 0, v[132:133]
	v_mul_f32_e32 v130, v200, v200
	v_lshl_add_u64 v[134:135], v[132:133], 0, v[128:129]
	v_pk_mul_f32 v[132:133], v[78:79], v[70:71]
	v_pk_mul_f32 v[136:137], v[136:137], v[130:131] op_sel_hi:[1,0]
	v_pk_mul_f32 v[132:133], v[132:133], v[130:131] op_sel_hi:[1,0]
	v_pk_mul_f32 v[138:139], v[138:139], v[130:131] op_sel_hi:[1,0]
	v_pk_mul_f32 v[140:141], v[140:141], v[130:131] op_sel_hi:[1,0]
	v_cvt_pk_bf16_f32 v130, v136, v137
	v_cvt_pk_bf16_f32 v131, v132, v133
	v_pk_mul_f32 v[136:137], v[60:61], v[52:53]
	v_cvt_pk_bf16_f32 v132, v140, v141
	v_cvt_pk_bf16_f32 v133, v138, v139
	global_store_dwordx4 v[134:135], v[130:133], off sc1
	v_pk_mul_f32 v[138:139], v[58:59], v[50:51]
	v_pk_mul_f32 v[140:141], v[56:57], v[48:49]
	v_lshlrev_b64 v[132:133], 11, v[182:183]
	v_lshl_add_u64 v[132:133], s[2:3], 0, v[132:133]
	v_mul_f32_e32 v130, v152, v152
	v_lshl_add_u64 v[134:135], v[132:133], 0, v[128:129]
	v_pk_mul_f32 v[132:133], v[62:63], v[54:55]
	v_pk_mul_f32 v[136:137], v[136:137], v[130:131] op_sel_hi:[1,0]
	v_pk_mul_f32 v[132:133], v[132:133], v[130:131] op_sel_hi:[1,0]
	v_pk_mul_f32 v[138:139], v[138:139], v[130:131] op_sel_hi:[1,0]
	v_pk_mul_f32 v[140:141], v[140:141], v[130:131] op_sel_hi:[1,0]
	v_cvt_pk_bf16_f32 v130, v136, v137
	v_cvt_pk_bf16_f32 v131, v132, v133
	v_pk_mul_f32 v[136:137], v[44:45], v[36:37]
	v_cvt_pk_bf16_f32 v132, v140, v141
	v_cvt_pk_bf16_f32 v133, v138, v139
	global_store_dwordx4 v[134:135], v[130:133], off sc1
	v_pk_mul_f32 v[138:139], v[42:43], v[34:35]
	v_pk_mul_f32 v[140:141], v[40:41], v[32:33]
	v_lshlrev_b64 v[132:133], 11, v[180:181]
	v_lshl_add_u64 v[132:133], s[2:3], 0, v[132:133]
	v_mul_f32_e32 v130, v150, v150
	v_lshl_add_u64 v[134:135], v[132:133], 0, v[128:129]
	v_pk_mul_f32 v[132:133], v[46:47], v[38:39]
	v_pk_mul_f32 v[136:137], v[136:137], v[130:131] op_sel_hi:[1,0]
	v_pk_mul_f32 v[132:133], v[132:133], v[130:131] op_sel_hi:[1,0]
	v_pk_mul_f32 v[138:139], v[138:139], v[130:131] op_sel_hi:[1,0]
	v_pk_mul_f32 v[140:141], v[140:141], v[130:131] op_sel_hi:[1,0]
	v_cvt_pk_bf16_f32 v130, v136, v137
	v_cvt_pk_bf16_f32 v131, v132, v133
	v_pk_mul_f32 v[136:137], v[28:29], v[20:21]
	v_cvt_pk_bf16_f32 v132, v140, v141
	v_cvt_pk_bf16_f32 v133, v138, v139
	global_store_dwordx4 v[134:135], v[130:133], off sc1
	v_pk_mul_f32 v[138:139], v[26:27], v[18:19]
	v_pk_mul_f32 v[140:141], v[24:25], v[16:17]
	v_lshlrev_b64 v[132:133], 11, v[178:179]
	v_lshl_add_u64 v[132:133], s[2:3], 0, v[132:133]
	v_mul_f32_e32 v130, v148, v148
	v_lshl_add_u64 v[134:135], v[132:133], 0, v[128:129]
	v_pk_mul_f32 v[132:133], v[30:31], v[22:23]
	v_pk_mul_f32 v[136:137], v[136:137], v[130:131] op_sel_hi:[1,0]
	v_pk_mul_f32 v[132:133], v[132:133], v[130:131] op_sel_hi:[1,0]
	v_pk_mul_f32 v[138:139], v[138:139], v[130:131] op_sel_hi:[1,0]
	v_pk_mul_f32 v[140:141], v[140:141], v[130:131] op_sel_hi:[1,0]
	v_cvt_pk_bf16_f32 v130, v136, v137
	v_cvt_pk_bf16_f32 v131, v132, v133
	s_nop 0
	v_cvt_pk_bf16_f32 v132, v140, v141
	v_cvt_pk_bf16_f32 v133, v138, v139
	global_store_dwordx4 v[134:135], v[130:133], off sc1
	v_pk_mul_f32 v[134:135], v[12:13], v[4:5]
	v_pk_mul_f32 v[138:139], v[8:9], v[0:1]
	v_lshlrev_b64 v[132:133], 11, v[176:177]
	v_lshl_add_u64 v[132:133], s[2:3], 0, v[132:133]
	v_mul_f32_e32 v130, v146, v146
	v_lshl_add_u64 v[132:133], v[132:133], 0, v[128:129]
	v_pk_mul_f32 v[128:129], v[14:15], v[6:7]
	s_nop 0
	v_pk_mul_f32 v[136:137], v[128:129], v[130:131] op_sel_hi:[1,0]
	v_pk_mul_f32 v[128:129], v[134:135], v[130:131] op_sel_hi:[1,0]
	v_pk_mul_f32 v[134:135], v[10:11], v[2:3]
	v_cvt_pk_bf16_f32 v128, v128, v129
	v_cvt_pk_bf16_f32 v129, v136, v137
	s_nop 0
	v_pk_mul_f32 v[134:135], v[134:135], v[130:131] op_sel_hi:[1,0]
	v_pk_mul_f32 v[130:131], v[138:139], v[130:131] op_sel_hi:[1,0]
	s_nop 0
	v_cvt_pk_bf16_f32 v130, v130, v131
	v_cvt_pk_bf16_f32 v131, v134, v135
	global_store_dwordx4 v[132:133], v[128:131], off sc1

;     __device__ __forceinline__ bool operator()(f32x4 (&acc)[2][2][4][2], const pg8::Unit& u, int wr, int wc, int fr, int fq) const {
;     ...
;         } else if (pn < 16) {
;             bf16_t* dst = pn < 12 ? V : CB; const int colb = (pn & 3) * 256 + wc * 32 + 8 * fq;
; #pragma unroll
;             for (int ai = 0; ai < 2; ++ai)
; #pragma unroll
;                 for (int m = 0; m < 4; ++m) { const int row = row0 + ai * 128 + m * 16; const float rsv = RS_AT(ai, m);
; #pragma unroll
;                     for (int bj = 0; bj < 2; ++bj) st8(dst + (size_t)row * DM + colb + bj * 128, acc[ai][bj][m][0] * rsv, acc[ai][bj][m][1] * rsv); }
.LBB0_732:
	s_andn2_b64 vcc, exec, s[4:5]
	s_cbranch_vccnz .LBB0_734
	v_readlane_b32 s4, v251, 48
	s_cmp_lt_u32 s29, 12
	v_readlane_b32 s2, v251, 45
	v_readlane_b32 s5, v251, 49
	s_cselect_b32 s3, s2, s5
	v_readlane_b32 s2, v251, 44
	s_cselect_b32 s2, s2, s4
	s_lshl_b32 s4, s29, 8
	s_and_b32 s4, s4, 0x300
	v_or_b32_e32 v128, s4, v203
	v_lshlrev_b32_e32 v160, 1, v128
	v_lshl_add_u64 v[128:129], s[2:3], 0, v[160:161]
	v_lshlrev_b64 v[130:131], 11, v[184:185]
	v_lshl_add_u64 v[134:135], v[128:129], 0, v[130:131]
	v_pk_mul_f32 v[130:131], v[124:125], v[198:199] op_sel_hi:[1,0]
	v_pk_mul_f32 v[132:133], v[126:127], v[198:199] op_sel_hi:[1,0]
	v_cvt_pk_bf16_f32 v130, v130, v131
	v_pk_mul_f32 v[136:137], v[122:123], v[198:199] op_sel_hi:[1,0]
	v_cvt_pk_bf16_f32 v131, v132, v133
	v_pk_mul_f32 v[138:139], v[120:121], v[198:199] op_sel_hi:[1,0]
	s_nop 0
	v_cvt_pk_bf16_f32 v132, v138, v139
	v_cvt_pk_bf16_f32 v133, v136, v137
	global_store_dwordx4 v[134:135], v[130:133], off sc1
	v_pk_mul_f32 v[136:137], v[114:115], v[198:199] op_sel_hi:[1,0]
	v_pk_mul_f32 v[138:139], v[112:113], v[198:199] op_sel_hi:[1,0]
	v_pk_mul_f32 v[130:131], v[116:117], v[198:199] op_sel_hi:[1,0]
	v_pk_mul_f32 v[132:133], v[118:119], v[198:199] op_sel_hi:[1,0]
	v_cvt_pk_bf16_f32 v130, v130, v131
	s_nop 0
	v_cvt_pk_bf16_f32 v131, v132, v133
	v_cvt_pk_bf16_f32 v132, v138, v139
	v_cvt_pk_bf16_f32 v133, v136, v137
	global_store_dwordx4 v[134:135], v[130:133], off offset:256 sc1
	v_pk_mul_f32 v[136:137], v[106:107], v[154:155] op_sel_hi:[1,0]
	v_pk_mul_f32 v[138:139], v[104:105], v[154:155] op_sel_hi:[1,0]
	v_lshlrev_b64 v[130:131], 11, v[196:197]
	v_lshl_add_u64 v[134:135], v[128:129], 0, v[130:131]
	v_pk_mul_f32 v[130:131], v[108:109], v[154:155] op_sel_hi:[1,0]
	v_pk_mul_f32 v[132:133], v[110:111], v[154:155] op_sel_hi:[1,0]
	v_cvt_pk_bf16_f32 v130, v130, v131
	s_nop 0
	v_cvt_pk_bf16_f32 v131, v132, v133
	v_cvt_pk_bf16_f32 v132, v138, v139
	v_cvt_pk_bf16_f32 v133, v136, v137
	global_store_dwordx4 v[134:135], v[130:133], off sc1
	v_pk_mul_f32 v[136:137], v[98:99], v[154:155] op_sel_hi:[1,0]
	v_pk_mul_f32 v[138:139], v[96:97], v[154:155] op_sel_hi:[1,0]
	v_pk_mul_f32 v[130:131], v[100:101], v[154:155] op_sel_hi:[1,0]
	v_pk_mul_f32 v[132:133], v[102:103], v[154:155] op_sel_hi:[1,0]
	v_cvt_pk_bf16_f32 v130, v130, v131
	s_nop 0
	v_cvt_pk_bf16_f32 v131, v132, v133
	v_cvt_pk_bf16_f32 v132, v138, v139
	v_cvt_pk_bf16_f32 v133, v136, v137
	global_store_dwordx4 v[134:135], v[130:133], off offset:256 sc1
	v_pk_mul_f32 v[136:137], v[90:91], v[202:203] op_sel_hi:[1,0]
	v_pk_mul_f32 v[138:139], v[88:89], v[202:203] op_sel_hi:[1,0]
	v_lshlrev_b64 v[130:131], 11, v[188:189]
	v_lshl_add_u64 v[134:135], v[128:129], 0, v[130:131]
	v_pk_mul_f32 v[130:131], v[92:93], v[202:203] op_sel_hi:[1,0]
	v_pk_mul_f32 v[132:133], v[94:95], v[202:203] op_sel_hi:[1,0]
	v_cvt_pk_bf16_f32 v130, v130, v131
	s_nop 0
	v_cvt_pk_bf16_f32 v131, v132, v133
	v_cvt_pk_bf16_f32 v132, v138, v139
	v_cvt_pk_bf16_f32 v133, v136, v137
	global_store_dwordx4 v[134:135], v[130:133], off sc1
	v_pk_mul_f32 v[136:137], v[82:83], v[202:203] op_sel_hi:[1,0]
	v_pk_mul_f32 v[138:139], v[80:81], v[202:203] op_sel_hi:[1,0]
	v_pk_mul_f32 v[130:131], v[84:85], v[202:203] op_sel_hi:[1,0]
	v_pk_mul_f32 v[132:133], v[86:87], v[202:203] op_sel_hi:[1,0]
	v_cvt_pk_bf16_f32 v130, v130, v131
	s_nop 0
	v_cvt_pk_bf16_f32 v131, v132, v133
	v_cvt_pk_bf16_f32 v132, v138, v139
	v_cvt_pk_bf16_f32 v133, v136, v137
	global_store_dwordx4 v[134:135], v[130:133], off offset:256 sc1
	v_pk_mul_f32 v[136:137], v[74:75], v[200:201] op_sel_hi:[1,0]
	v_pk_mul_f32 v[138:139], v[72:73], v[200:201] op_sel_hi:[1,0]
	v_lshlrev_b64 v[130:131], 11, v[186:187]
	v_lshl_add_u64 v[134:135], v[128:129], 0, v[130:131]
	v_pk_mul_f32 v[130:131], v[76:77], v[200:201] op_sel_hi:[1,0]
	v_pk_mul_f32 v[132:133], v[78:79], v[200:201] op_sel_hi:[1,0]
	v_cvt_pk_bf16_f32 v130, v130, v131
	s_nop 0
	v_cvt_pk_bf16_f32 v131, v132, v133
	v_cvt_pk_bf16_f32 v132, v138, v139
	v_cvt_pk_bf16_f32 v133, v136, v137
	global_store_dwordx4 v[134:135], v[130:133], off sc1
	v_pk_mul_f32 v[136:137], v[66:67], v[200:201] op_sel_hi:[1,0]
	v_pk_mul_f32 v[138:139], v[64:65], v[200:201] op_sel_hi:[1,0]
	v_pk_mul_f32 v[130:131], v[68:69], v[200:201] op_sel_hi:[1,0]
	v_pk_mul_f32 v[132:133], v[70:71], v[200:201] op_sel_hi:[1,0]
;     __device__ __forceinline__ bool operator()(f32x4 (&acc)[2][2][4][2], const pg8::Unit& u, int wr, int wc, int fr, int fq) const {
;     ...
;         } else if (pn < 16) {
;             bf16_t* dst = pn < 12 ? V : CB; const int colb = (pn & 3) * 256 + wc * 32 + 8 * fq;
; #pragma unroll
;             for (int ai = 0; ai < 2; ++ai)
; #pragma unroll
;                 for (int m = 0; m < 4; ++m) { const int row = row0 + ai * 128 + m * 16; const float rsv = RS_AT(ai, m);
; #pragma unroll
;                     for (int bj = 0; bj < 2; ++bj) st8(dst + (size_t)row * DM + colb + bj * 128, acc[ai][bj][m][0] * rsv, acc[ai][bj][m][1] * rsv); }
	v_cvt_pk_bf16_f32 v130, v130, v131
	s_nop 0
	v_cvt_pk_bf16_f32 v131, v132, v133
	v_cvt_pk_bf16_f32 v132, v138, v139
	v_cvt_pk_bf16_f32 v133, v136, v137
	global_store_dwordx4 v[134:135], v[130:133], off offset:256 sc1
	v_pk_mul_f32 v[136:137], v[58:59], v[152:153] op_sel_hi:[1,0]
	v_pk_mul_f32 v[138:139], v[56:57], v[152:153] op_sel_hi:[1,0]
	v_lshlrev_b64 v[130:131], 11, v[182:183]
	v_lshl_add_u64 v[134:135], v[128:129], 0, v[130:131]
	v_pk_mul_f32 v[130:131], v[60:61], v[152:153] op_sel_hi:[1,0]
	v_pk_mul_f32 v[132:133], v[62:63], v[152:153] op_sel_hi:[1,0]
	v_cvt_pk_bf16_f32 v130, v130, v131
	s_nop 0
	v_cvt_pk_bf16_f32 v131, v132, v133
	v_cvt_pk_bf16_f32 v132, v138, v139
	v_cvt_pk_bf16_f32 v133, v136, v137
	global_store_dwordx4 v[134:135], v[130:133], off sc1
	v_pk_mul_f32 v[136:137], v[50:51], v[152:153] op_sel_hi:[1,0]
	v_pk_mul_f32 v[138:139], v[48:49], v[152:153] op_sel_hi:[1,0]
	v_pk_mul_f32 v[130:131], v[52:53], v[152:153] op_sel_hi:[1,0]
	v_pk_mul_f32 v[132:133], v[54:55], v[152:153] op_sel_hi:[1,0]
	v_cvt_pk_bf16_f32 v130, v130, v131
	s_nop 0
	v_cvt_pk_bf16_f32 v131, v132, v133
	v_cvt_pk_bf16_f32 v132, v138, v139
	v_cvt_pk_bf16_f32 v133, v136, v137
	global_store_dwordx4 v[134:135], v[130:133], off offset:256 sc1
	v_pk_mul_f32 v[136:137], v[42:43], v[150:151] op_sel_hi:[1,0]
	v_pk_mul_f32 v[138:139], v[40:41], v[150:151] op_sel_hi:[1,0]
	v_lshlrev_b64 v[130:131], 11, v[180:181]
	v_lshl_add_u64 v[134:135], v[128:129], 0, v[130:131]
	v_pk_mul_f32 v[130:131], v[44:45], v[150:151] op_sel_hi:[1,0]
	v_pk_mul_f32 v[132:133], v[46:47], v[150:151] op_sel_hi:[1,0]
	v_cvt_pk_bf16_f32 v130, v130, v131
	s_nop 0
	v_cvt_pk_bf16_f32 v131, v132, v133
	v_cvt_pk_bf16_f32 v132, v138, v139
	v_cvt_pk_bf16_f32 v133, v136, v137
	global_store_dwordx4 v[134:135], v[130:133], off sc1
	v_pk_mul_f32 v[136:137], v[34:35], v[150:151] op_sel_hi:[1,0]
	v_pk_mul_f32 v[138:139], v[32:33], v[150:151] op_sel_hi:[1,0]
	v_pk_mul_f32 v[130:131], v[36:37], v[150:151] op_sel_hi:[1,0]
	v_pk_mul_f32 v[132:133], v[38:39], v[150:151] op_sel_hi:[1,0]
	v_cvt_pk_bf16_f32 v130, v130, v131
	s_nop 0
	v_cvt_pk_bf16_f32 v131, v132, v133
	v_cvt_pk_bf16_f32 v132, v138, v139
	v_cvt_pk_bf16_f32 v133, v136, v137
	global_store_dwordx4 v[134:135], v[130:133], off offset:256 sc1
	v_pk_mul_f32 v[136:137], v[26:27], v[148:149] op_sel_hi:[1,0]
	v_pk_mul_f32 v[138:139], v[24:25], v[148:149] op_sel_hi:[1,0]
	v_lshlrev_b64 v[130:131], 11, v[178:179]
	v_lshl_add_u64 v[134:135], v[128:129], 0, v[130:131]
	v_pk_mul_f32 v[130:131], v[28:29], v[148:149] op_sel_hi:[1,0]
	v_pk_mul_f32 v[132:133], v[30:31], v[148:149] op_sel_hi:[1,0]
	v_cvt_pk_bf16_f32 v130, v130, v131
	s_nop 0
	v_cvt_pk_bf16_f32 v131, v132, v133
	v_cvt_pk_bf16_f32 v132, v138, v139
	v_cvt_pk_bf16_f32 v133, v136, v137
	global_store_dwordx4 v[134:135], v[130:133], off sc1
	v_pk_mul_f32 v[136:137], v[18:19], v[148:149] op_sel_hi:[1,0]
	v_pk_mul_f32 v[138:139], v[16:17], v[148:149] op_sel_hi:[1,0]
	v_pk_mul_f32 v[130:131], v[20:21], v[148:149] op_sel_hi:[1,0]
	v_pk_mul_f32 v[132:133], v[22:23], v[148:149] op_sel_hi:[1,0]
	v_cvt_pk_bf16_f32 v130, v130, v131
	s_nop 0
	v_cvt_pk_bf16_f32 v131, v132, v133
	v_cvt_pk_bf16_f32 v132, v138, v139
	v_cvt_pk_bf16_f32 v133, v136, v137
	global_store_dwordx4 v[134:135], v[130:133], off offset:256 sc1
	v_pk_mul_f32 v[134:135], v[10:11], v[146:147] op_sel_hi:[1,0]
	v_pk_mul_f32 v[136:137], v[8:9], v[146:147] op_sel_hi:[1,0]
	v_lshlrev_b64 v[130:131], 11, v[176:177]
	v_lshl_add_u64 v[132:133], v[128:129], 0, v[130:131]
	v_pk_mul_f32 v[130:131], v[14:15], v[146:147] op_sel_hi:[1,0]
	v_pk_mul_f32 v[128:129], v[12:13], v[146:147] op_sel_hi:[1,0]
	s_nop 0
	v_cvt_pk_bf16_f32 v128, v128, v129
	v_cvt_pk_bf16_f32 v129, v130, v131
	v_cvt_pk_bf16_f32 v130, v136, v137
	v_cvt_pk_bf16_f32 v131, v134, v135
	global_store_dwordx4 v[132:133], v[128:131], off sc1
	v_pk_mul_f32 v[134:135], v[2:3], v[146:147] op_sel_hi:[1,0]
	v_pk_mul_f32 v[136:137], v[0:1], v[146:147] op_sel_hi:[1,0]
	v_pk_mul_f32 v[130:131], v[6:7], v[146:147] op_sel_hi:[1,0]
	v_pk_mul_f32 v[128:129], v[4:5], v[146:147] op_sel_hi:[1,0]
	s_nop 0
	v_cvt_pk_bf16_f32 v128, v128, v129
	v_cvt_pk_bf16_f32 v129, v130, v131
	v_cvt_pk_bf16_f32 v130, v136, v137
	v_cvt_pk_bf16_f32 v131, v134, v135
	global_store_dwordx4 v[132:133], v[128:131], off offset:256 sc1

;     __device__ __forceinline__ bool operator()(f32x4 (&acc)[2][2][4][2], const pg8::Unit& u, int wr, int wc, int fr, int fq) const {
;     ...
;         if (pn < 8) {
;             bf16_t* dst = pn < 4 ? Q : Kb; const float sc = pn < 4 ? QSCALE : 1.0f; const int colb = (pn & 3) * 256 + wc * 32 + 8 * fq;
;             const bool rot = ((wc & 1) == 0) && (fq < 2);
; #pragma unroll
;             for (int ai = 0; ai < 2; ++ai)
; #pragma unroll
;               for (int mh = 0; mh < 2; ++mh) {
;                 f32x4 c4[2], s4[2];
; #pragma unroll
;                 for (int q = 0; q < 2; ++q) { c4[q] = (f32x4){1.f, 1.f, 1.f, 1.f}; s4[q] = (f32x4){0.f, 0.f, 0.f, 0.f};
;                     if (rot) { const int t = (row0 + ai * 128 + (2 * mh + q) * 16) & (SEQ - 1); c4[q] = *(const f32x4*)(cosT + t * 8 + 4 * fq); s4[q] = *(const f32x4*)(sinT + t * 8 + 4 * fq); } }
; #pragma unroll
;                 for (int q = 0; q < 2; ++q) { const int m = 2 * mh + q; const int row = row0 + ai * 128 + m * 16; const float rsv = RS_AT(ai, m);
; #pragma unroll
;                     for (int bj = 0; bj < 2; ++bj) { f32x4 x1 = acc[ai][bj][m][0] * rsv, x2 = acc[ai][bj][m][1] * rsv;
;                         const f32x4 y1 = x1 * c4[q] - x2 * s4[q], y2 = x2 * c4[q] + x1 * s4[q];
.LBB0_739:
	s_or_b64 exec, exec, s[4:5]
	s_cmp_lt_i32 s29, 4
	s_cselect_b64 vcc, -1, 0
	s_and_b64 s[2:3], vcc, exec
	v_readlane_b32 s2, v252, 16
	v_readlane_b32 s3, v252, 17
	v_readlane_b32 s4, v251, 43
	s_cselect_b32 s3, s3, s4
	v_readlane_b32 s4, v251, 42
	s_cselect_b32 s2, s2, s4
	s_lshl_b32 s4, s29, 8
	v_pk_mul_f32 v[122:123], v[122:123], v[198:199] op_sel_hi:[1,0]
	v_pk_mul_f32 v[120:121], v[120:121], v[198:199] op_sel_hi:[1,0]
	v_mov_b32_e32 v129, 0x3e38aa3b
	s_and_b32 s4, s4, 0x300
	v_pk_mul_f32 v[126:127], v[126:127], v[198:199] op_sel_hi:[1,0]
	v_pk_mul_f32 v[124:125], v[124:125], v[198:199] op_sel_hi:[1,0]
	s_waitcnt vmcnt(1)
	v_pk_mul_f32 v[192:193], v[122:123], v[140:141]
	v_pk_mul_f32 v[208:209], v[120:121], v[138:139]
	v_cndmask_b32_e32 v204, 1.0, v129, vcc
	v_or_b32_e32 v129, s4, v203
	s_waitcnt vmcnt(0)
; #define EFENCE() asm volatile("" ::: "memory")
;     __device__ __forceinline__ bool operator()(f32x4 (&acc)[2][2][4][2], const pg8::Unit& u, int wr, int wc, int fr, int fq) const {
;     ...
;             for (int ai = 0; ai < 2; ++ai)
; #pragma unroll
;               for (int mh = 0; mh < 2; ++mh) {
;                 f32x4 c4[2], s4[2];
; #pragma unroll
;                 for (int q = 0; q < 2; ++q) { c4[q] = (f32x4){1.f, 1.f, 1.f, 1.f}; s4[q] = (f32x4){0.f, 0.f, 0.f, 0.f};
;                     if (rot) { const int t = (row0 + ai * 128 + (2 * mh + q) * 16) & (SEQ - 1); c4[q] = *(const f32x4*)(cosT + t * 8 + 4 * fq); s4[q] = *(const f32x4*)(sinT + t * 8 + 4 * fq); } }
; #pragma unroll
;                 for (int q = 0; q < 2; ++q) { const int m = 2 * mh + q; const int row = row0 + ai * 128 + m * 16; const float rsv = RS_AT(ai, m);
; #pragma unroll
;                     for (int bj = 0; bj < 2; ++bj) { f32x4 x1 = acc[ai][bj][m][0] * rsv, x2 = acc[ai][bj][m][1] * rsv;
;                         const f32x4 y1 = x1 * c4[q] - x2 * s4[q], y2 = x2 * c4[q] + x1 * s4[q];
;                         if (rot) { x1 = y1; x2 = y2; }
;                         st8(dst + (size_t)row * DM + colb + bj * 128, x1 * sc, x2 * sc); } }
;                 EFENCE(); }
	v_pk_fma_f32 v[192:193], v[126:127], v[144:145], v[192:193]
	v_pk_fma_f32 v[208:209], v[124:125], v[142:143], v[208:209]
	v_pk_mul_f32 v[210:211], v[122:123], v[144:145]
	v_pk_mul_f32 v[216:217], v[120:121], v[142:143]
	v_lshlrev_b32_e32 v160, 1, v129
	v_pk_fma_f32 v[210:211], v[126:127], v[140:141], v[210:211] neg_lo:[0,0,1] neg_hi:[0,0,1]
	v_pk_fma_f32 v[216:217], v[124:125], v[138:139], v[216:217] neg_lo:[0,0,1] neg_hi:[0,0,1]
	v_cndmask_b32_e64 v123, v123, v193, s[0:1]
	v_cndmask_b32_e64 v122, v122, v192, s[0:1]
	v_cndmask_b32_e64 v121, v121, v209, s[0:1]
	v_cndmask_b32_e64 v120, v120, v208, s[0:1]
	v_lshl_add_u64 v[206:207], s[2:3], 0, v[160:161]
	v_lshlrev_b64 v[190:191], 11, v[184:185]
	v_cndmask_b32_e64 v127, v127, v211, s[0:1]
	v_cndmask_b32_e64 v126, v126, v210, s[0:1]
	v_cndmask_b32_e64 v125, v125, v217, s[0:1]
	v_cndmask_b32_e64 v124, v124, v216, s[0:1]
	v_pk_mul_f32 v[192:193], v[204:205], v[122:123] op_sel_hi:[0,1]
	v_pk_mul_f32 v[122:123], v[204:205], v[120:121] op_sel_hi:[0,1]
	v_lshl_add_u64 v[190:191], v[206:207], 0, v[190:191]
	v_pk_mul_f32 v[126:127], v[204:205], v[126:127] op_sel_hi:[0,1]
	v_pk_mul_f32 v[124:125], v[204:205], v[124:125] op_sel_hi:[0,1]
	v_cvt_pk_bf16_f32 v120, v124, v125
	v_cvt_pk_bf16_f32 v121, v126, v127
	v_cvt_pk_bf16_f32 v122, v122, v123
	v_cvt_pk_bf16_f32 v123, v192, v193
	v_pk_mul_f32 v[114:115], v[114:115], v[198:199] op_sel_hi:[1,0]
	v_pk_mul_f32 v[112:113], v[112:113], v[198:199] op_sel_hi:[1,0]
	global_store_dwordx4 v[190:191], v[120:123], off sc1
	v_pk_mul_f32 v[118:119], v[118:119], v[198:199] op_sel_hi:[1,0]
	v_pk_mul_f32 v[116:117], v[116:117], v[198:199] op_sel_hi:[1,0]
	v_pk_mul_f32 v[120:121], v[114:115], v[140:141]
	v_pk_mul_f32 v[122:123], v[112:113], v[138:139]
	v_pk_fma_f32 v[120:121], v[118:119], v[144:145], v[120:121]
	v_pk_fma_f32 v[122:123], v[116:117], v[142:143], v[122:123]
	v_pk_mul_f32 v[124:125], v[114:115], v[144:145]
	v_pk_mul_f32 v[126:127], v[112:113], v[142:143]
	v_pk_fma_f32 v[124:125], v[118:119], v[140:141], v[124:125] neg_lo:[0,0,1] neg_hi:[0,0,1]
	v_pk_fma_f32 v[126:127], v[116:117], v[138:139], v[126:127] neg_lo:[0,0,1] neg_hi:[0,0,1]
	v_cndmask_b32_e64 v115, v115, v121, s[0:1]
	v_cndmask_b32_e64 v114, v114, v120, s[0:1]
	v_cndmask_b32_e64 v113, v113, v123, s[0:1]
	v_cndmask_b32_e64 v112, v112, v122, s[0:1]
	v_cndmask_b32_e64 v119, v119, v125, s[0:1]
	v_cndmask_b32_e64 v118, v118, v124, s[0:1]
	v_cndmask_b32_e64 v117, v117, v127, s[0:1]
	v_cndmask_b32_e64 v116, v116, v126, s[0:1]
	v_pk_mul_f32 v[120:121], v[204:205], v[114:115] op_sel_hi:[0,1]
	v_pk_mul_f32 v[114:115], v[204:205], v[112:113] op_sel_hi:[0,1]
	v_pk_mul_f32 v[118:119], v[204:205], v[118:119] op_sel_hi:[0,1]
	v_pk_mul_f32 v[116:117], v[204:205], v[116:117] op_sel_hi:[0,1]
	v_cvt_pk_bf16_f32 v112, v116, v117
	v_cvt_pk_bf16_f32 v113, v118, v119
	v_cvt_pk_bf16_f32 v114, v114, v115
	v_cvt_pk_bf16_f32 v115, v120, v121
	v_pk_mul_f32 v[106:107], v[106:107], v[154:155] op_sel_hi:[1,0]
	v_pk_mul_f32 v[104:105], v[104:105], v[154:155] op_sel_hi:[1,0]
	global_store_dwordx4 v[190:191], v[112:115], off offset:256 sc1
	v_pk_mul_f32 v[110:111], v[110:111], v[154:155] op_sel_hi:[1,0]
	v_pk_mul_f32 v[108:109], v[108:109], v[154:155] op_sel_hi:[1,0]
	v_pk_mul_f32 v[114:115], v[104:105], v[130:131]
	v_pk_mul_f32 v[116:117], v[106:107], v[132:133]
	v_pk_fma_f32 v[114:115], v[108:109], v[134:135], v[114:115]
	v_pk_fma_f32 v[116:117], v[110:111], v[136:137], v[116:117]
	v_pk_mul_f32 v[118:119], v[104:105], v[134:135]
	v_pk_mul_f32 v[120:121], v[106:107], v[136:137]
	v_pk_fma_f32 v[118:119], v[108:109], v[130:131], v[118:119] neg_lo:[0,0,1] neg_hi:[0,0,1]
	v_pk_fma_f32 v[120:121], v[110:111], v[132:133], v[120:121] neg_lo:[0,0,1] neg_hi:[0,0,1]
	v_cndmask_b32_e64 v107, v107, v117, s[0:1]
	v_cndmask_b32_e64 v106, v106, v116, s[0:1]
	v_cndmask_b32_e64 v105, v105, v115, s[0:1]
	v_cndmask_b32_e64 v104, v104, v114, s[0:1]
	v_lshlrev_b64 v[112:113], 11, v[196:197]
	v_cndmask_b32_e64 v111, v111, v121, s[0:1]
	v_cndmask_b32_e64 v110, v110, v120, s[0:1]
	v_cndmask_b32_e64 v109, v109, v119, s[0:1]
	v_cndmask_b32_e64 v108, v108, v118, s[0:1]
	v_pk_mul_f32 v[114:115], v[204:205], v[106:107] op_sel_hi:[0,1]
	v_pk_mul_f32 v[106:107], v[204:205], v[104:105] op_sel_hi:[0,1]
	v_lshl_add_u64 v[112:113], v[206:207], 0, v[112:113]
	v_pk_mul_f32 v[110:111], v[204:205], v[110:111] op_sel_hi:[0,1]
	v_pk_mul_f32 v[108:109], v[204:205], v[108:109] op_sel_hi:[0,1]
	v_cvt_pk_bf16_f32 v104, v108, v109
	v_cvt_pk_bf16_f32 v105, v110, v111
	v_cvt_pk_bf16_f32 v106, v106, v107
	v_cvt_pk_bf16_f32 v107, v114, v115
	v_pk_mul_f32 v[98:99], v[98:99], v[154:155] op_sel_hi:[1,0]
	v_pk_mul_f32 v[96:97], v[96:97], v[154:155] op_sel_hi:[1,0]
	global_store_dwordx4 v[112:113], v[104:107], off sc1
	v_pk_mul_f32 v[102:103], v[102:103], v[154:155] op_sel_hi:[1,0]
	v_pk_mul_f32 v[100:101], v[100:101], v[154:155] op_sel_hi:[1,0]
	v_pk_mul_f32 v[104:105], v[96:97], v[130:131]
	v_pk_mul_f32 v[106:107], v[98:99], v[132:133]
	v_pk_fma_f32 v[104:105], v[100:101], v[134:135], v[104:105]
	v_pk_fma_f32 v[106:107], v[102:103], v[136:137], v[106:107]
	v_pk_mul_f32 v[108:109], v[96:97], v[134:135]
	v_pk_mul_f32 v[110:111], v[98:99], v[136:137]
	v_pk_fma_f32 v[108:109], v[100:101], v[130:131], v[108:109] neg_lo:[0,0,1] neg_hi:[0,0,1]
	v_pk_fma_f32 v[110:111], v[102:103], v[132:133], v[110:111] neg_lo:[0,0,1] neg_hi:[0,0,1]
	v_cndmask_b32_e64 v99, v99, v107, s[0:1]
	v_cndmask_b32_e64 v98, v98, v106, s[0:1]
	v_cndmask_b32_e64 v97, v97, v105, s[0:1]
	v_cndmask_b32_e64 v96, v96, v104, s[0:1]
	v_cndmask_b32_e64 v103, v103, v111, s[0:1]
	v_cndmask_b32_e64 v102, v102, v110, s[0:1]
	v_cndmask_b32_e64 v101, v101, v109, s[0:1]
	v_cndmask_b32_e64 v100, v100, v108, s[0:1]
	v_pk_mul_f32 v[104:105], v[204:205], v[98:99] op_sel_hi:[0,1]
	v_pk_mul_f32 v[98:99], v[204:205], v[96:97] op_sel_hi:[0,1]
	v_pk_mul_f32 v[102:103], v[204:205], v[102:103] op_sel_hi:[0,1]
	v_pk_mul_f32 v[100:101], v[204:205], v[100:101] op_sel_hi:[0,1]
	v_cvt_pk_bf16_f32 v96, v100, v101
	v_cvt_pk_bf16_f32 v97, v102, v103
	v_cvt_pk_bf16_f32 v98, v98, v99
	v_cvt_pk_bf16_f32 v99, v104, v105
	global_store_dwordx4 v[112:113], v[96:99], off offset:256 sc1
	v_mov_b32_e32 v128, 1.0
	v_mov_b32_e32 v100, 0
	v_mov_b32_e32 v96, 0
	v_mov_b32_e32 v101, 0
	v_mov_b32_e32 v102, 0
	v_mov_b32_e32 v103, 0
	v_mov_b32_e32 v104, 1.0
	v_mov_b32_e32 v105, 1.0
	v_mov_b32_e32 v106, 1.0
	v_mov_b32_e32 v107, 1.0
	s_and_saveexec_b64 s[4:5], s[0:1]
	s_cbranch_execz .LBB0_741
	v_and_b32_e32 v160, 0xf9e0, v147
	v_lshl_add_u64 v[98:99], v[168:169], 0, v[160:161]
	v_lshl_add_u64 v[100:101], v[170:171], 0, v[160:161]
	global_load_dwordx4 v[104:107], v[98:99], off offset:1024
	s_nop 0
	global_load_dwordx4 v[100:103], v[100:101], off offset:1024

; #define EFENCE() asm volatile("" ::: "memory")
;     __device__ __forceinline__ bool operator()(f32x4 (&acc)[2][2][4][2], const pg8::Unit& u, int wr, int wc, int fr, int fq) const {
;     ...
;             for (int ai = 0; ai < 2; ++ai)
; #pragma unroll
;               for (int mh = 0; mh < 2; ++mh) {
;                 f32x4 c4[2], s4[2];
; #pragma unroll
;                 for (int q = 0; q < 2; ++q) { c4[q] = (f32x4){1.f, 1.f, 1.f, 1.f}; s4[q] = (f32x4){0.f, 0.f, 0.f, 0.f};
;                     if (rot) { const int t = (row0 + ai * 128 + (2 * mh + q) * 16) & (SEQ - 1); c4[q] = *(const f32x4*)(cosT + t * 8 + 4 * fq); s4[q] = *(const f32x4*)(sinT + t * 8 + 4 * fq); } }
; #pragma unroll
;                 for (int q = 0; q < 2; ++q) { const int m = 2 * mh + q; const int row = row0 + ai * 128 + m * 16; const float rsv = RS_AT(ai, m);
; #pragma unroll
;                     for (int bj = 0; bj < 2; ++bj) { f32x4 x1 = acc[ai][bj][m][0] * rsv, x2 = acc[ai][bj][m][1] * rsv;
;                         const f32x4 y1 = x1 * c4[q] - x2 * s4[q], y2 = x2 * c4[q] + x1 * s4[q];
;                         if (rot) { x1 = y1; x2 = y2; }
;                         st8(dst + (size_t)row * DM + colb + bj * 128, x1 * sc, x2 * sc); } }
;                 EFENCE(); }
.LBB0_743:
	s_or_b64 exec, exec, s[4:5]
	v_pk_mul_f32 v[90:91], v[90:91], v[202:203] op_sel_hi:[1,0]
	v_pk_mul_f32 v[88:89], v[88:89], v[202:203] op_sel_hi:[1,0]
	v_pk_mul_f32 v[94:95], v[94:95], v[202:203] op_sel_hi:[1,0]
	v_pk_mul_f32 v[92:93], v[92:93], v[202:203] op_sel_hi:[1,0]
	s_waitcnt vmcnt(1)
	v_pk_mul_f32 v[110:111], v[90:91], v[106:107]
	v_pk_mul_f32 v[112:113], v[88:89], v[104:105]
	s_waitcnt vmcnt(0)
	v_pk_fma_f32 v[110:111], v[94:95], v[102:103], v[110:111]
	v_pk_fma_f32 v[112:113], v[92:93], v[100:101], v[112:113]
	v_pk_mul_f32 v[114:115], v[90:91], v[102:103]
	v_pk_mul_f32 v[116:117], v[88:89], v[100:101]
	v_mov_b32_e32 v205, v204
	v_pk_fma_f32 v[114:115], v[94:95], v[106:107], v[114:115] neg_lo:[0,0,1] neg_hi:[0,0,1]
	v_pk_fma_f32 v[116:117], v[92:93], v[104:105], v[116:117] neg_lo:[0,0,1] neg_hi:[0,0,1]
	v_cndmask_b32_e64 v91, v91, v111, s[0:1]
	v_cndmask_b32_e64 v90, v90, v110, s[0:1]
	v_cndmask_b32_e64 v89, v89, v113, s[0:1]
	v_cndmask_b32_e64 v88, v88, v112, s[0:1]
	v_mov_b32_e32 v110, v204
	v_mov_b32_e32 v111, v204
	v_lshlrev_b64 v[108:109], 11, v[188:189]
	v_cndmask_b32_e64 v95, v95, v115, s[0:1]
	v_cndmask_b32_e64 v94, v94, v114, s[0:1]
	v_cndmask_b32_e64 v93, v93, v117, s[0:1]
	v_cndmask_b32_e64 v92, v92, v116, s[0:1]
	v_pk_mul_f32 v[112:113], v[110:111], v[90:91]
	v_pk_mul_f32 v[90:91], v[204:205], v[88:89]
	v_lshl_add_u64 v[108:109], v[206:207], 0, v[108:109]
	v_pk_mul_f32 v[94:95], v[110:111], v[94:95]
	v_pk_mul_f32 v[92:93], v[204:205], v[92:93]
	v_pk_mul_f32 v[82:83], v[82:83], v[202:203] op_sel_hi:[1,0]
	v_cvt_pk_bf16_f32 v88, v92, v93
	v_cvt_pk_bf16_f32 v89, v94, v95
	v_cvt_pk_bf16_f32 v90, v90, v91
	v_cvt_pk_bf16_f32 v91, v112, v113
	v_pk_mul_f32 v[80:81], v[80:81], v[202:203] op_sel_hi:[1,0]
	global_store_dwordx4 v[108:109], v[88:91], off sc1
	v_pk_mul_f32 v[86:87], v[86:87], v[202:203] op_sel_hi:[1,0]
	v_pk_mul_f32 v[84:85], v[84:85], v[202:203] op_sel_hi:[1,0]
	v_pk_mul_f32 v[88:89], v[82:83], v[106:107]
	v_pk_mul_f32 v[90:91], v[80:81], v[104:105]
	v_pk_fma_f32 v[88:89], v[86:87], v[102:103], v[88:89]
	v_pk_fma_f32 v[90:91], v[84:85], v[100:101], v[90:91]
	v_pk_mul_f32 v[92:93], v[82:83], v[102:103]
	v_pk_mul_f32 v[94:95], v[80:81], v[100:101]
	v_pk_fma_f32 v[92:93], v[86:87], v[106:107], v[92:93] neg_lo:[0,0,1] neg_hi:[0,0,1]
	v_pk_fma_f32 v[94:95], v[84:85], v[104:105], v[94:95] neg_lo:[0,0,1] neg_hi:[0,0,1]
	v_cndmask_b32_e64 v83, v83, v89, s[0:1]
	v_cndmask_b32_e64 v82, v82, v88, s[0:1]
	v_cndmask_b32_e64 v81, v81, v91, s[0:1]
	v_cndmask_b32_e64 v80, v80, v90, s[0:1]
	v_cndmask_b32_e64 v87, v87, v93, s[0:1]
	v_cndmask_b32_e64 v86, v86, v92, s[0:1]
	v_cndmask_b32_e64 v85, v85, v95, s[0:1]
	v_cndmask_b32_e64 v84, v84, v94, s[0:1]
	v_pk_mul_f32 v[88:89], v[110:111], v[82:83]
	v_pk_mul_f32 v[82:83], v[204:205], v[80:81]
	v_pk_mul_f32 v[86:87], v[110:111], v[86:87]
	v_pk_mul_f32 v[84:85], v[204:205], v[84:85]
	v_pk_mul_f32 v[74:75], v[74:75], v[200:201] op_sel_hi:[1,0]
	v_cvt_pk_bf16_f32 v80, v84, v85
	v_cvt_pk_bf16_f32 v81, v86, v87
	v_cvt_pk_bf16_f32 v82, v82, v83
	v_cvt_pk_bf16_f32 v83, v88, v89
	v_pk_mul_f32 v[72:73], v[72:73], v[200:201] op_sel_hi:[1,0]
	global_store_dwordx4 v[108:109], v[80:83], off offset:256 sc1
	v_pk_mul_f32 v[78:79], v[78:79], v[200:201] op_sel_hi:[1,0]
	v_pk_mul_f32 v[76:77], v[76:77], v[200:201] op_sel_hi:[1,0]
	v_pk_mul_f32 v[82:83], v[72:73], v[128:129]
	v_pk_mul_f32 v[84:85], v[74:75], v[130:131]
	v_pk_fma_f32 v[82:83], v[76:77], v[96:97], v[82:83]
	v_pk_fma_f32 v[84:85], v[78:79], v[98:99], v[84:85]
	v_pk_mul_f32 v[86:87], v[72:73], v[96:97]
	v_pk_mul_f32 v[88:89], v[74:75], v[98:99]
	v_pk_fma_f32 v[86:87], v[76:77], v[128:129], v[86:87] neg_lo:[0,0,1] neg_hi:[0,0,1]
	v_pk_fma_f32 v[88:89], v[78:79], v[130:131], v[88:89] neg_lo:[0,0,1] neg_hi:[0,0,1]
	v_cndmask_b32_e64 v75, v75, v85, s[0:1]
	v_cndmask_b32_e64 v74, v74, v84, s[0:1]
	v_cndmask_b32_e64 v73, v73, v83, s[0:1]
	v_cndmask_b32_e64 v72, v72, v82, s[0:1]
	v_lshlrev_b64 v[80:81], 11, v[186:187]
	v_cndmask_b32_e64 v79, v79, v89, s[0:1]
	v_cndmask_b32_e64 v78, v78, v88, s[0:1]
	v_cndmask_b32_e64 v77, v77, v87, s[0:1]
	v_cndmask_b32_e64 v76, v76, v86, s[0:1]
	v_pk_mul_f32 v[82:83], v[110:111], v[74:75]
	v_pk_mul_f32 v[74:75], v[204:205], v[72:73]
	v_lshl_add_u64 v[80:81], v[206:207], 0, v[80:81]
	v_pk_mul_f32 v[78:79], v[110:111], v[78:79]
	v_pk_mul_f32 v[76:77], v[204:205], v[76:77]
	v_pk_mul_f32 v[66:67], v[66:67], v[200:201] op_sel_hi:[1,0]
	v_cvt_pk_bf16_f32 v72, v76, v77
	v_cvt_pk_bf16_f32 v73, v78, v79
	v_cvt_pk_bf16_f32 v74, v74, v75
	v_cvt_pk_bf16_f32 v75, v82, v83
	v_pk_mul_f32 v[64:65], v[64:65], v[200:201] op_sel_hi:[1,0]
	global_store_dwordx4 v[80:81], v[72:75], off sc1
	v_pk_mul_f32 v[70:71], v[70:71], v[200:201] op_sel_hi:[1,0]
	v_pk_mul_f32 v[68:69], v[68:69], v[200:201] op_sel_hi:[1,0]
	v_pk_mul_f32 v[72:73], v[64:65], v[128:129]
	v_pk_mul_f32 v[74:75], v[66:67], v[130:131]
	v_pk_fma_f32 v[72:73], v[68:69], v[96:97], v[72:73]
	v_pk_fma_f32 v[74:75], v[70:71], v[98:99], v[74:75]
	v_pk_mul_f32 v[76:77], v[64:65], v[96:97]
	v_pk_mul_f32 v[78:79], v[66:67], v[98:99]
	v_pk_fma_f32 v[76:77], v[68:69], v[128:129], v[76:77] neg_lo:[0,0,1] neg_hi:[0,0,1]
	v_pk_fma_f32 v[78:79], v[70:71], v[130:131], v[78:79] neg_lo:[0,0,1] neg_hi:[0,0,1]
	v_cndmask_b32_e64 v67, v67, v75, s[0:1]
	v_cndmask_b32_e64 v66, v66, v74, s[0:1]
	v_cndmask_b32_e64 v65, v65, v73, s[0:1]
	v_cndmask_b32_e64 v64, v64, v72, s[0:1]
	v_cndmask_b32_e64 v71, v71, v79, s[0:1]
	v_cndmask_b32_e64 v70, v70, v78, s[0:1]
	v_cndmask_b32_e64 v69, v69, v77, s[0:1]
	v_cndmask_b32_e64 v68, v68, v76, s[0:1]
	v_pk_mul_f32 v[72:73], v[110:111], v[66:67]
	v_pk_mul_f32 v[66:67], v[204:205], v[64:65]
	v_pk_mul_f32 v[70:71], v[110:111], v[70:71]
	v_pk_mul_f32 v[68:69], v[204:205], v[68:69]
	v_mov_b32_e32 v74, 0
	v_cvt_pk_bf16_f32 v64, v68, v69
	v_cvt_pk_bf16_f32 v65, v70, v71
	v_cvt_pk_bf16_f32 v66, v66, v67
	v_cvt_pk_bf16_f32 v67, v72, v73
	global_store_dwordx4 v[80:81], v[64:67], off offset:256 sc1
	v_mov_b32_e32 v68, 0
	v_mov_b32_e32 v72, 0
	v_mov_b32_e32 v65, 0x400
	v_mov_b32_e32 v64, 1.0
	v_lshl_add_u32 v80, v184, 3, v65
	v_mov_b32_e32 v73, 0
	v_mov_b32_e32 v75, 0
	v_mov_b32_e32 v76, 1.0
	v_mov_b32_e32 v77, 1.0
	v_mov_b32_e32 v78, 1.0
	v_mov_b32_e32 v79, 1.0
	s_and_saveexec_b64 s[4:5], s[0:1]
	s_cbranch_execz .LBB0_745
	v_and_b32_e32 v65, 0x3e78, v80
	v_lshlrev_b32_e32 v160, 2, v65
	v_lshl_add_u64 v[66:67], v[168:169], 0, v[160:161]
	v_lshl_add_u64 v[70:71], v[170:171], 0, v[160:161]
	global_load_dwordx4 v[76:79], v[66:67], off
	global_load_dwordx4 v[72:75], v[70:71], off

; #define EFENCE() asm volatile("" ::: "memory")
;     __device__ __forceinline__ bool operator()(f32x4 (&acc)[2][2][4][2], const pg8::Unit& u, int wr, int wc, int fr, int fq) const {
;     ...
;             for (int ai = 0; ai < 2; ++ai)
; #pragma unroll
;               for (int mh = 0; mh < 2; ++mh) {
;                 f32x4 c4[2], s4[2];
; #pragma unroll
;                 for (int q = 0; q < 2; ++q) { c4[q] = (f32x4){1.f, 1.f, 1.f, 1.f}; s4[q] = (f32x4){0.f, 0.f, 0.f, 0.f};
;                     if (rot) { const int t = (row0 + ai * 128 + (2 * mh + q) * 16) & (SEQ - 1); c4[q] = *(const f32x4*)(cosT + t * 8 + 4 * fq); s4[q] = *(const f32x4*)(sinT + t * 8 + 4 * fq); } }
; #pragma unroll
;                 for (int q = 0; q < 2; ++q) { const int m = 2 * mh + q; const int row = row0 + ai * 128 + m * 16; const float rsv = RS_AT(ai, m);
; #pragma unroll
;                     for (int bj = 0; bj < 2; ++bj) { f32x4 x1 = acc[ai][bj][m][0] * rsv, x2 = acc[ai][bj][m][1] * rsv;
;                         const f32x4 y1 = x1 * c4[q] - x2 * s4[q], y2 = x2 * c4[q] + x1 * s4[q];
;                         if (rot) { x1 = y1; x2 = y2; }
;                         st8(dst + (size_t)row * DM + colb + bj * 128, x1 * sc, x2 * sc); } }
;                 EFENCE(); }
.LBB0_747:
	s_or_b64 exec, exec, s[4:5]
	v_pk_mul_f32 v[58:59], v[58:59], v[152:153] op_sel_hi:[1,0]
	v_pk_mul_f32 v[56:57], v[56:57], v[152:153] op_sel_hi:[1,0]
	v_pk_mul_f32 v[62:63], v[62:63], v[152:153] op_sel_hi:[1,0]
	v_pk_mul_f32 v[60:61], v[60:61], v[152:153] op_sel_hi:[1,0]
	s_waitcnt vmcnt(1)
	v_pk_mul_f32 v[84:85], v[58:59], v[78:79]
	v_pk_mul_f32 v[86:87], v[56:57], v[76:77]
	s_waitcnt vmcnt(0)
	v_pk_fma_f32 v[84:85], v[62:63], v[74:75], v[84:85]
	v_pk_fma_f32 v[86:87], v[60:61], v[72:73], v[86:87]
	v_pk_mul_f32 v[88:89], v[58:59], v[74:75]
	v_pk_mul_f32 v[90:91], v[56:57], v[72:73]
	v_pk_fma_f32 v[88:89], v[62:63], v[78:79], v[88:89] neg_lo:[0,0,1] neg_hi:[0,0,1]
	v_pk_fma_f32 v[90:91], v[60:61], v[76:77], v[90:91] neg_lo:[0,0,1] neg_hi:[0,0,1]
	v_cndmask_b32_e64 v59, v59, v85, s[0:1]
	v_cndmask_b32_e64 v58, v58, v84, s[0:1]
	v_cndmask_b32_e64 v57, v57, v87, s[0:1]
	v_cndmask_b32_e64 v56, v56, v86, s[0:1]
	v_mov_b32_e32 v84, v204
	v_mov_b32_e32 v85, v204
	v_lshlrev_b64 v[82:83], 11, v[182:183]
	v_cndmask_b32_e64 v63, v63, v89, s[0:1]
	v_cndmask_b32_e64 v62, v62, v88, s[0:1]
	v_cndmask_b32_e64 v61, v61, v91, s[0:1]
	v_cndmask_b32_e64 v60, v60, v90, s[0:1]
	v_pk_mul_f32 v[86:87], v[84:85], v[58:59]
	v_pk_mul_f32 v[58:59], v[204:205], v[56:57]
	v_lshl_add_u64 v[82:83], v[206:207], 0, v[82:83]
	v_pk_mul_f32 v[62:63], v[84:85], v[62:63]
	v_pk_mul_f32 v[60:61], v[204:205], v[60:61]
	v_pk_mul_f32 v[50:51], v[50:51], v[152:153] op_sel_hi:[1,0]
	v_cvt_pk_bf16_f32 v56, v60, v61
	v_cvt_pk_bf16_f32 v57, v62, v63
	v_cvt_pk_bf16_f32 v58, v58, v59
	v_cvt_pk_bf16_f32 v59, v86, v87
	v_pk_mul_f32 v[48:49], v[48:49], v[152:153] op_sel_hi:[1,0]
	global_store_dwordx4 v[82:83], v[56:59], off sc1
	v_pk_mul_f32 v[54:55], v[54:55], v[152:153] op_sel_hi:[1,0]
	v_pk_mul_f32 v[52:53], v[52:53], v[152:153] op_sel_hi:[1,0]
	v_pk_mul_f32 v[56:57], v[50:51], v[78:79]
	v_pk_mul_f32 v[58:59], v[48:49], v[76:77]
	v_pk_fma_f32 v[56:57], v[54:55], v[74:75], v[56:57]
	v_pk_fma_f32 v[58:59], v[52:53], v[72:73], v[58:59]
	v_pk_mul_f32 v[60:61], v[50:51], v[74:75]
	v_pk_mul_f32 v[62:63], v[48:49], v[72:73]
	v_pk_fma_f32 v[60:61], v[54:55], v[78:79], v[60:61] neg_lo:[0,0,1] neg_hi:[0,0,1]
	v_pk_fma_f32 v[62:63], v[52:53], v[76:77], v[62:63] neg_lo:[0,0,1] neg_hi:[0,0,1]
	v_cndmask_b32_e64 v51, v51, v57, s[0:1]
	v_cndmask_b32_e64 v50, v50, v56, s[0:1]
	v_cndmask_b32_e64 v49, v49, v59, s[0:1]
	v_cndmask_b32_e64 v48, v48, v58, s[0:1]
	v_cndmask_b32_e64 v55, v55, v61, s[0:1]
	v_cndmask_b32_e64 v54, v54, v60, s[0:1]
	v_cndmask_b32_e64 v53, v53, v63, s[0:1]
	v_cndmask_b32_e64 v52, v52, v62, s[0:1]
	v_pk_mul_f32 v[56:57], v[84:85], v[50:51]
	v_pk_mul_f32 v[50:51], v[204:205], v[48:49]
	v_pk_mul_f32 v[54:55], v[84:85], v[54:55]
	v_pk_mul_f32 v[52:53], v[204:205], v[52:53]
	v_pk_mul_f32 v[42:43], v[42:43], v[150:151] op_sel_hi:[1,0]
	v_cvt_pk_bf16_f32 v48, v52, v53
	v_cvt_pk_bf16_f32 v49, v54, v55
	v_cvt_pk_bf16_f32 v50, v50, v51
	v_cvt_pk_bf16_f32 v51, v56, v57
	v_pk_mul_f32 v[40:41], v[40:41], v[150:151] op_sel_hi:[1,0]
	global_store_dwordx4 v[82:83], v[48:51], off offset:256 sc1
	v_pk_mul_f32 v[46:47], v[46:47], v[150:151] op_sel_hi:[1,0]
	v_pk_mul_f32 v[44:45], v[44:45], v[150:151] op_sel_hi:[1,0]
	v_pk_mul_f32 v[50:51], v[40:41], v[64:65]
	v_pk_mul_f32 v[52:53], v[42:43], v[66:67]
	v_pk_fma_f32 v[50:51], v[44:45], v[68:69], v[50:51]
	v_pk_fma_f32 v[52:53], v[46:47], v[70:71], v[52:53]
	v_pk_mul_f32 v[54:55], v[40:41], v[68:69]
	v_pk_mul_f32 v[56:57], v[42:43], v[70:71]
	v_pk_fma_f32 v[54:55], v[44:45], v[64:65], v[54:55] neg_lo:[0,0,1] neg_hi:[0,0,1]
	v_pk_fma_f32 v[56:57], v[46:47], v[66:67], v[56:57] neg_lo:[0,0,1] neg_hi:[0,0,1]
	v_cndmask_b32_e64 v43, v43, v53, s[0:1]
	v_cndmask_b32_e64 v42, v42, v52, s[0:1]
	v_cndmask_b32_e64 v41, v41, v51, s[0:1]
	v_cndmask_b32_e64 v40, v40, v50, s[0:1]
	v_lshlrev_b64 v[48:49], 11, v[180:181]
	v_cndmask_b32_e64 v47, v47, v57, s[0:1]
	v_cndmask_b32_e64 v46, v46, v56, s[0:1]
	v_cndmask_b32_e64 v45, v45, v55, s[0:1]
	v_cndmask_b32_e64 v44, v44, v54, s[0:1]
	v_pk_mul_f32 v[50:51], v[84:85], v[42:43]
	v_pk_mul_f32 v[42:43], v[204:205], v[40:41]
	v_lshl_add_u64 v[48:49], v[206:207], 0, v[48:49]
	v_pk_mul_f32 v[46:47], v[84:85], v[46:47]
	v_pk_mul_f32 v[44:45], v[204:205], v[44:45]
	v_pk_mul_f32 v[34:35], v[34:35], v[150:151] op_sel_hi:[1,0]
	v_cvt_pk_bf16_f32 v40, v44, v45
	v_cvt_pk_bf16_f32 v41, v46, v47
	v_cvt_pk_bf16_f32 v42, v42, v43
	v_cvt_pk_bf16_f32 v43, v50, v51
	v_pk_mul_f32 v[32:33], v[32:33], v[150:151] op_sel_hi:[1,0]
	global_store_dwordx4 v[48:49], v[40:43], off sc1
	v_pk_mul_f32 v[38:39], v[38:39], v[150:151] op_sel_hi:[1,0]
	v_pk_mul_f32 v[36:37], v[36:37], v[150:151] op_sel_hi:[1,0]
	v_pk_mul_f32 v[40:41], v[32:33], v[64:65]
	v_pk_mul_f32 v[42:43], v[34:35], v[66:67]
	v_pk_fma_f32 v[40:41], v[36:37], v[68:69], v[40:41]
	v_pk_fma_f32 v[42:43], v[38:39], v[70:71], v[42:43]
	v_pk_mul_f32 v[44:45], v[32:33], v[68:69]
	v_pk_mul_f32 v[46:47], v[34:35], v[70:71]
	v_pk_fma_f32 v[44:45], v[36:37], v[64:65], v[44:45] neg_lo:[0,0,1] neg_hi:[0,0,1]
	v_pk_fma_f32 v[46:47], v[38:39], v[66:67], v[46:47] neg_lo:[0,0,1] neg_hi:[0,0,1]
	v_cndmask_b32_e64 v35, v35, v43, s[0:1]
	v_cndmask_b32_e64 v34, v34, v42, s[0:1]
	v_cndmask_b32_e64 v33, v33, v41, s[0:1]
	v_cndmask_b32_e64 v32, v32, v40, s[0:1]
	v_cndmask_b32_e64 v39, v39, v47, s[0:1]
	v_cndmask_b32_e64 v38, v38, v46, s[0:1]
	v_cndmask_b32_e64 v37, v37, v45, s[0:1]
	v_cndmask_b32_e64 v36, v36, v44, s[0:1]
	v_pk_mul_f32 v[40:41], v[84:85], v[34:35]
	v_pk_mul_f32 v[34:35], v[204:205], v[32:33]
	v_pk_mul_f32 v[38:39], v[84:85], v[38:39]
	v_pk_mul_f32 v[36:37], v[204:205], v[36:37]
	v_mov_b32_e32 v42, 0
	v_cvt_pk_bf16_f32 v32, v36, v37
	v_cvt_pk_bf16_f32 v33, v38, v39
	v_cvt_pk_bf16_f32 v34, v34, v35
	v_cvt_pk_bf16_f32 v35, v40, v41
	global_store_dwordx4 v[48:49], v[32:35], off offset:256 sc1
	v_mov_b32_e32 v36, 0
	v_mov_b32_e32 v40, 0
	v_mov_b32_e32 v32, 1.0
	v_mov_b32_e32 v41, 0
	v_mov_b32_e32 v43, 0
	v_mov_b32_e32 v44, 1.0
	v_mov_b32_e32 v45, 1.0
	v_mov_b32_e32 v46, 1.0
	v_mov_b32_e32 v47, 1.0
	s_and_saveexec_b64 s[4:5], s[0:1]
	s_cbranch_execz .LBB0_749
	v_and_b32_e32 v33, 0x3e78, v80
	v_lshlrev_b32_e32 v160, 2, v33
	v_lshl_add_u64 v[34:35], v[168:169], 0, v[160:161]
	v_lshl_add_u64 v[38:39], v[170:171], 0, v[160:161]
	global_load_dwordx4 v[44:47], v[34:35], off offset:1024
	global_load_dwordx4 v[40:43], v[38:39], off offset:1024

; #define EFENCE() asm volatile("" ::: "memory")
;     __device__ __forceinline__ bool operator()(f32x4 (&acc)[2][2][4][2], const pg8::Unit& u, int wr, int wc, int fr, int fq) const {
;     ...
;             for (int ai = 0; ai < 2; ++ai)
; #pragma unroll
;               for (int mh = 0; mh < 2; ++mh) {
;                 f32x4 c4[2], s4[2];
; #pragma unroll
;                 for (int q = 0; q < 2; ++q) { c4[q] = (f32x4){1.f, 1.f, 1.f, 1.f}; s4[q] = (f32x4){0.f, 0.f, 0.f, 0.f};
;                     if (rot) { const int t = (row0 + ai * 128 + (2 * mh + q) * 16) & (SEQ - 1); c4[q] = *(const f32x4*)(cosT + t * 8 + 4 * fq); s4[q] = *(const f32x4*)(sinT + t * 8 + 4 * fq); } }
; #pragma unroll
;                 for (int q = 0; q < 2; ++q) { const int m = 2 * mh + q; const int row = row0 + ai * 128 + m * 16; const float rsv = RS_AT(ai, m);
; #pragma unroll
;                     for (int bj = 0; bj < 2; ++bj) { f32x4 x1 = acc[ai][bj][m][0] * rsv, x2 = acc[ai][bj][m][1] * rsv;
;                         const f32x4 y1 = x1 * c4[q] - x2 * s4[q], y2 = x2 * c4[q] + x1 * s4[q];
;                         if (rot) { x1 = y1; x2 = y2; }
;                         st8(dst + (size_t)row * DM + colb + bj * 128, x1 * sc, x2 * sc); } }
;                 EFENCE(); }
.LBB0_751:
	s_or_b64 exec, exec, s[4:5]
	v_pk_mul_f32 v[26:27], v[26:27], v[148:149] op_sel_hi:[1,0]
	v_pk_mul_f32 v[24:25], v[24:25], v[148:149] op_sel_hi:[1,0]
	v_pk_mul_f32 v[30:31], v[30:31], v[148:149] op_sel_hi:[1,0]
	v_pk_mul_f32 v[28:29], v[28:29], v[148:149] op_sel_hi:[1,0]
	s_waitcnt vmcnt(1)
	v_pk_mul_f32 v[50:51], v[26:27], v[46:47]
	v_pk_mul_f32 v[52:53], v[24:25], v[44:45]
	s_waitcnt vmcnt(0)
	v_pk_fma_f32 v[50:51], v[30:31], v[42:43], v[50:51]
	v_pk_fma_f32 v[52:53], v[28:29], v[40:41], v[52:53]
	v_pk_mul_f32 v[54:55], v[26:27], v[42:43]
	v_pk_mul_f32 v[56:57], v[24:25], v[40:41]
	v_pk_fma_f32 v[54:55], v[30:31], v[46:47], v[54:55] neg_lo:[0,0,1] neg_hi:[0,0,1]
	v_pk_fma_f32 v[56:57], v[28:29], v[44:45], v[56:57] neg_lo:[0,0,1] neg_hi:[0,0,1]
	v_cndmask_b32_e64 v27, v27, v51, s[0:1]
	v_cndmask_b32_e64 v26, v26, v50, s[0:1]
	v_cndmask_b32_e64 v25, v25, v53, s[0:1]
	v_cndmask_b32_e64 v24, v24, v52, s[0:1]
	v_mov_b32_e32 v50, v204
	v_mov_b32_e32 v51, v204
	v_lshlrev_b64 v[48:49], 11, v[178:179]
	v_cndmask_b32_e64 v31, v31, v55, s[0:1]
	v_cndmask_b32_e64 v30, v30, v54, s[0:1]
	v_cndmask_b32_e64 v29, v29, v57, s[0:1]
	v_cndmask_b32_e64 v28, v28, v56, s[0:1]
	v_pk_mul_f32 v[52:53], v[50:51], v[26:27]
	v_pk_mul_f32 v[26:27], v[204:205], v[24:25]
	v_lshl_add_u64 v[48:49], v[206:207], 0, v[48:49]
	v_pk_mul_f32 v[30:31], v[50:51], v[30:31]
	v_pk_mul_f32 v[28:29], v[204:205], v[28:29]
	v_pk_mul_f32 v[18:19], v[18:19], v[148:149] op_sel_hi:[1,0]
	v_cvt_pk_bf16_f32 v24, v28, v29
	v_cvt_pk_bf16_f32 v25, v30, v31
	v_cvt_pk_bf16_f32 v26, v26, v27
	v_cvt_pk_bf16_f32 v27, v52, v53
	v_pk_mul_f32 v[16:17], v[16:17], v[148:149] op_sel_hi:[1,0]
	global_store_dwordx4 v[48:49], v[24:27], off sc1
	v_pk_mul_f32 v[22:23], v[22:23], v[148:149] op_sel_hi:[1,0]
	v_pk_mul_f32 v[20:21], v[20:21], v[148:149] op_sel_hi:[1,0]
	v_pk_mul_f32 v[24:25], v[18:19], v[46:47]
	v_pk_mul_f32 v[26:27], v[16:17], v[44:45]
	v_pk_fma_f32 v[24:25], v[22:23], v[42:43], v[24:25]
	v_pk_fma_f32 v[26:27], v[20:21], v[40:41], v[26:27]
	v_pk_mul_f32 v[28:29], v[18:19], v[42:43]
	v_pk_mul_f32 v[30:31], v[16:17], v[40:41]
	v_pk_fma_f32 v[28:29], v[22:23], v[46:47], v[28:29] neg_lo:[0,0,1] neg_hi:[0,0,1]
	v_pk_fma_f32 v[30:31], v[20:21], v[44:45], v[30:31] neg_lo:[0,0,1] neg_hi:[0,0,1]
	v_cndmask_b32_e64 v19, v19, v25, s[0:1]
	v_cndmask_b32_e64 v18, v18, v24, s[0:1]
	v_cndmask_b32_e64 v17, v17, v27, s[0:1]
	v_cndmask_b32_e64 v16, v16, v26, s[0:1]
	v_cndmask_b32_e64 v23, v23, v29, s[0:1]
	v_cndmask_b32_e64 v22, v22, v28, s[0:1]
	v_cndmask_b32_e64 v21, v21, v31, s[0:1]
	v_cndmask_b32_e64 v20, v20, v30, s[0:1]
	v_pk_mul_f32 v[24:25], v[50:51], v[18:19]
	v_pk_mul_f32 v[18:19], v[204:205], v[16:17]
	v_pk_mul_f32 v[22:23], v[50:51], v[22:23]
	v_pk_mul_f32 v[20:21], v[204:205], v[20:21]
	v_pk_mul_f32 v[10:11], v[10:11], v[146:147] op_sel_hi:[1,0]
	v_cvt_pk_bf16_f32 v16, v20, v21
	v_cvt_pk_bf16_f32 v17, v22, v23
	v_cvt_pk_bf16_f32 v18, v18, v19
	v_cvt_pk_bf16_f32 v19, v24, v25
	v_pk_mul_f32 v[8:9], v[8:9], v[146:147] op_sel_hi:[1,0]
	global_store_dwordx4 v[48:49], v[16:19], off offset:256 sc1
	v_pk_mul_f32 v[14:15], v[14:15], v[146:147] op_sel_hi:[1,0]
	v_pk_mul_f32 v[12:13], v[12:13], v[146:147] op_sel_hi:[1,0]
	v_pk_mul_f32 v[18:19], v[8:9], v[32:33]
	v_pk_mul_f32 v[20:21], v[10:11], v[34:35]
	v_pk_fma_f32 v[18:19], v[12:13], v[36:37], v[18:19]
	v_pk_fma_f32 v[20:21], v[14:15], v[38:39], v[20:21]
	v_pk_mul_f32 v[22:23], v[8:9], v[36:37]
	v_pk_mul_f32 v[24:25], v[10:11], v[38:39]
	v_pk_fma_f32 v[22:23], v[12:13], v[32:33], v[22:23] neg_lo:[0,0,1] neg_hi:[0,0,1]
	v_pk_fma_f32 v[24:25], v[14:15], v[34:35], v[24:25] neg_lo:[0,0,1] neg_hi:[0,0,1]
	v_cndmask_b32_e64 v11, v11, v21, s[0:1]
	v_cndmask_b32_e64 v10, v10, v20, s[0:1]
	v_cndmask_b32_e64 v9, v9, v19, s[0:1]
	v_cndmask_b32_e64 v8, v8, v18, s[0:1]
	v_lshlrev_b64 v[16:17], 11, v[176:177]
	v_cndmask_b32_e64 v15, v15, v25, s[0:1]
	v_cndmask_b32_e64 v14, v14, v24, s[0:1]
	v_cndmask_b32_e64 v13, v13, v23, s[0:1]
	v_cndmask_b32_e64 v12, v12, v22, s[0:1]
	v_pk_mul_f32 v[18:19], v[50:51], v[10:11]
	v_pk_mul_f32 v[10:11], v[204:205], v[8:9]
	v_lshl_add_u64 v[16:17], v[206:207], 0, v[16:17]
	v_pk_mul_f32 v[14:15], v[50:51], v[14:15]
	v_pk_mul_f32 v[12:13], v[204:205], v[12:13]
	v_pk_mul_f32 v[2:3], v[2:3], v[146:147] op_sel_hi:[1,0]
	v_cvt_pk_bf16_f32 v8, v12, v13
	v_cvt_pk_bf16_f32 v9, v14, v15
	v_cvt_pk_bf16_f32 v10, v10, v11
	v_cvt_pk_bf16_f32 v11, v18, v19
	v_pk_mul_f32 v[0:1], v[0:1], v[146:147] op_sel_hi:[1,0]
	global_store_dwordx4 v[16:17], v[8:11], off sc1
	v_pk_mul_f32 v[6:7], v[6:7], v[146:147] op_sel_hi:[1,0]
	v_pk_mul_f32 v[4:5], v[4:5], v[146:147] op_sel_hi:[1,0]
	v_pk_mul_f32 v[8:9], v[0:1], v[32:33]
	v_pk_mul_f32 v[10:11], v[2:3], v[34:35]
	v_pk_fma_f32 v[8:9], v[4:5], v[36:37], v[8:9]
	v_pk_fma_f32 v[10:11], v[6:7], v[38:39], v[10:11]
	v_pk_mul_f32 v[12:13], v[0:1], v[36:37]
	v_pk_mul_f32 v[14:15], v[2:3], v[38:39]
	v_pk_fma_f32 v[12:13], v[4:5], v[32:33], v[12:13] neg_lo:[0,0,1] neg_hi:[0,0,1]
	v_pk_fma_f32 v[14:15], v[6:7], v[34:35], v[14:15] neg_lo:[0,0,1] neg_hi:[0,0,1]
	v_cndmask_b32_e64 v3, v3, v11, s[0:1]
	v_cndmask_b32_e64 v2, v2, v10, s[0:1]
	v_cndmask_b32_e64 v1, v1, v9, s[0:1]
	v_cndmask_b32_e64 v0, v0, v8, s[0:1]
	v_cndmask_b32_e64 v7, v7, v15, s[0:1]
	v_cndmask_b32_e64 v6, v6, v14, s[0:1]
	v_cndmask_b32_e64 v5, v5, v13, s[0:1]
	v_cndmask_b32_e64 v4, v4, v12, s[0:1]
	v_pk_mul_f32 v[8:9], v[50:51], v[2:3]
	v_pk_mul_f32 v[2:3], v[204:205], v[0:1]
	v_pk_mul_f32 v[6:7], v[50:51], v[6:7]
	v_pk_mul_f32 v[4:5], v[204:205], v[4:5]
	s_nop 0
	v_cvt_pk_bf16_f32 v0, v4, v5
	v_cvt_pk_bf16_f32 v1, v6, v7
	v_cvt_pk_bf16_f32 v2, v2, v3
	v_cvt_pk_bf16_f32 v3, v8, v9
	global_store_dwordx4 v[16:17], v[0:3], off offset:256 sc1
	s_andn2_b64 vcc, exec, s[6:7]
	s_mov_b64 s[4:5], -1
	s_cbranch_vccnz .LBB0_712

; #define CV_LO(q_) (f32x4){bf_lo((q_).x), bf_hi((q_).x), bf_lo((q_).y), bf_hi((q_).y)}
; #define CV_HI(q_) (f32x4){bf_lo((q_).z), bf_hi((q_).z), bf_lo((q_).w), bf_hi((q_).w)}
; __device__ __forceinline__ void conv_rows(const bf16_t* U, const bf16_t* CB, const float* cw, bf16_t* YC, int gw, int NGW, int lane) {
;     ...
;         for (int c2 = 0; c2 < 2; ++c2) { const int col = c2 * 512 + lane * 8;
; #pragma unroll
;             for (int i = 0; i < 10; ++i) { const int t = t0 - 1 + i; const bool ok = (i == 0) ? ((t0 & (SEQ - 1)) != 0) : (i == 9) ? (((t0 + 8) & (SEQ - 1)) != 0) : true;
;                 ur[c2][i] = (u32x4){0u, 0u, 0u, 0u}; if (ok) ur[c2][i] = __builtin_nontemporal_load((const u32x4*)(U + (size_t)t * DM + col)); }
; #pragma unroll
;             for (int i = 0; i < 8; ++i) cr[c2][i] = __builtin_nontemporal_load((const u32x4*)(CB + (size_t)(t0 + i) * DM + col)); }
; #pragma unroll
;         for (int c2 = 0; c2 < 2; ++c2) { const int col = c2 * 512 + lane * 8;
;             const f32x4 w0a = *(const f32x4*)(cw + col), w0b = *(const f32x4*)(cw + col + 4), w1a = *(const f32x4*)(cw + DM + col), w1b = *(const f32x4*)(cw + DM + col + 4),
;                         w2a = *(const f32x4*)(cw + 2 * DM + col), w2b = *(const f32x4*)(cw + 2 * DM + col + 4);
;     ...
;             f32x4 pa = CV_LO(ur[c2][0]), pb = CV_HI(ur[c2][0]), ca = CV_LO(ur[c2][1]), cb_ = CV_HI(ur[c2][1]);
; #pragma unroll
;             for (int i = 0; i < 8; ++i) { const f32x4 na = CV_LO(ur[c2][i + 2]), nb = CV_HI(ur[c2][i + 2]), ga = CV_LO(cr[c2][i]), gb = CV_HI(cr[c2][i]);
;                 st8(YC + (size_t)(t0 + i) * DM + col, ga * (w0a * pa + w1a * ca + w2a * na), gb * (w0b * pb + w1b * cb_ + w2b * nb));
;                 pa = ca; pb = cb_; ca = na; cb_ = nb; }
.LBB0_803:
	v_lshl_add_u64 v[4:5], v[188:189], 0, s[20:21]
	global_load_dwordx4 v[68:71], v[4:5], off nt
	v_lshl_add_u64 v[4:5], v[188:189], 0, s[18:19]
	global_load_dwordx4 v[52:55], v[4:5], off nt
	v_lshl_add_u64 v[4:5], v[188:189], 0, s[16:17]
	global_load_dwordx4 v[44:47], v[4:5], off nt
	v_lshl_add_u64 v[4:5], v[188:189], 0, s[14:15]
	global_load_dwordx4 v[36:39], v[4:5], off nt
	v_lshl_add_u64 v[4:5], v[188:189], 0, s[12:13]
	global_load_dwordx4 v[28:31], v[4:5], off nt
	v_lshl_add_u64 v[4:5], v[188:189], 0, s[10:11]
	global_load_dwordx4 v[20:23], v[4:5], off nt
	v_lshl_add_u64 v[4:5], v[188:189], 0, s[6:7]
	global_load_dwordx4 v[12:15], v[4:5], off nt
	v_lshl_add_u64 v[4:5], v[188:189], 0, s[4:5]
	global_load_dwordx4 v[4:7], v[4:5], off nt
	s_nop 0
	global_load_dwordx4 v[88:91], v[174:175], off offset:16
	global_load_dwordx4 v[96:99], v[174:175], off
	global_load_dwordx4 v[92:95], v[176:177], off offset:16
	global_load_dwordx4 v[116:119], v[176:177], off
	global_load_dwordx4 v[108:111], v[178:179], off offset:16
	global_load_dwordx4 v[120:123], v[178:179], off
	s_waitcnt vmcnt(0)
	v_lshlrev_b32_e32 v200, 16, v162
	v_and_b32_e32 v201, 0xffff0000, v162
	v_lshlrev_b32_e32 v202, 16, v163
	v_and_b32_e32 v203, 0xffff0000, v163
	v_lshlrev_b32_e32 v190, 16, v152
	v_and_b32_e32 v191, 0xffff0000, v152
	v_lshlrev_b32_e32 v192, 16, v153
	v_and_b32_e32 v193, 0xffff0000, v153
	v_lshlrev_b32_e32 v162, 16, v156
	v_and_b32_e32 v163, 0xffff0000, v156
	v_lshlrev_b32_e32 v156, 16, v157
	v_and_b32_e32 v157, 0xffff0000, v157
	v_lshlrev_b32_e32 v208, 16, v154
	v_and_b32_e32 v209, 0xffff0000, v154
	v_lshlrev_b32_e32 v210, 16, v155
	v_and_b32_e32 v211, 0xffff0000, v155
	v_lshlrev_b32_e32 v198, 16, v164
	v_and_b32_e32 v199, 0xffff0000, v164
	v_lshlrev_b32_e32 v164, 16, v165
	v_and_b32_e32 v165, 0xffff0000, v165
	v_lshlrev_b32_e32 v152, 16, v158
	v_and_b32_e32 v153, 0xffff0000, v158
	v_lshlrev_b32_e32 v154, 16, v159
	v_and_b32_e32 v155, 0xffff0000, v159
	v_lshlrev_b32_e32 v158, 16, v166
	v_and_b32_e32 v159, 0xffff0000, v166
	v_lshlrev_b32_e32 v166, 16, v167
	v_and_b32_e32 v167, 0xffff0000, v167
	v_lshlrev_b32_e32 v214, 16, v168
	v_and_b32_e32 v215, 0xffff0000, v168
	v_lshlrev_b32_e32 v168, 16, v169
	v_and_b32_e32 v169, 0xffff0000, v169
	v_lshl_add_u64 v[216:217], v[180:181], 0, s[20:21]
	v_readlane_b32 s1, v252, 22
	s_add_i32 s30, s30, s54
	s_add_i32 s0, s0, s1
	s_cmpk_lt_i32 s30, 0x800
	v_pk_mul_f32 v[218:219], v[116:117], v[200:201]
	v_pk_mul_f32 v[220:221], v[118:119], v[202:203]
	v_pk_fma_f32 v[190:191], v[96:97], v[190:191], v[218:219]
	v_pk_fma_f32 v[192:193], v[98:99], v[192:193], v[220:221]
	v_pk_fma_f32 v[190:191], v[120:121], v[162:163], v[190:191]
	v_pk_fma_f32 v[192:193], v[122:123], v[156:157], v[192:193]
	v_pk_mul_f32 v[158:159], v[190:191], v[158:159]
	v_pk_mul_f32 v[192:193], v[192:193], v[166:167]
	v_pk_mul_f32 v[166:167], v[92:93], v[198:199]
	v_pk_mul_f32 v[190:191], v[94:95], v[164:165]
	v_pk_fma_f32 v[166:167], v[88:89], v[208:209], v[166:167]
	v_pk_fma_f32 v[190:191], v[90:91], v[210:211], v[190:191]
	v_pk_fma_f32 v[166:167], v[108:109], v[152:153], v[166:167]
	v_pk_fma_f32 v[190:191], v[110:111], v[154:155], v[190:191]
	v_pk_mul_f32 v[208:209], v[116:117], v[162:163]
	v_pk_mul_f32 v[190:191], v[190:191], v[168:169]
	v_pk_mul_f32 v[168:169], v[166:167], v[214:215]
	v_cvt_pk_bf16_f32 v166, v158, v159
	v_cvt_pk_bf16_f32 v167, v192, v193
	v_pk_mul_f32 v[210:211], v[118:119], v[156:157]
	v_cvt_pk_bf16_f32 v168, v168, v169
	v_cvt_pk_bf16_f32 v169, v190, v191
	global_store_dwordx4 v[216:217], v[166:169], off sc1
	v_lshlrev_b32_e32 v158, 16, v148
	v_and_b32_e32 v159, 0xffff0000, v148
	v_lshlrev_b32_e32 v166, 16, v149
	v_and_b32_e32 v167, 0xffff0000, v149
	v_pk_fma_f32 v[202:203], v[98:99], v[202:203], v[210:211]
	v_pk_fma_f32 v[200:201], v[96:97], v[200:201], v[208:209]
	v_lshlrev_b32_e32 v168, 16, v144
	v_and_b32_e32 v169, 0xffff0000, v144
	v_lshlrev_b32_e32 v144, 16, v145
	v_and_b32_e32 v145, 0xffff0000, v145
	v_pk_fma_f32 v[200:201], v[120:121], v[158:159], v[200:201]
	v_pk_fma_f32 v[202:203], v[122:123], v[166:167], v[202:203]
	v_lshlrev_b32_e32 v148, 16, v150
	v_pk_mul_f32 v[202:203], v[202:203], v[144:145]
	v_pk_mul_f32 v[144:145], v[200:201], v[168:169]
	v_pk_mul_f32 v[168:169], v[92:93], v[152:153]
	v_pk_mul_f32 v[200:201], v[94:95], v[154:155]
	v_and_b32_e32 v149, 0xffff0000, v150
	v_lshlrev_b32_e32 v150, 16, v151
	v_and_b32_e32 v151, 0xffff0000, v151
	v_pk_fma_f32 v[164:165], v[90:91], v[164:165], v[200:201]
	v_pk_fma_f32 v[168:169], v[88:89], v[198:199], v[168:169]
	v_lshlrev_b32_e32 v190, 16, v146
	v_and_b32_e32 v191, 0xffff0000, v146
	v_lshlrev_b32_e32 v146, 16, v147
	v_and_b32_e32 v147, 0xffff0000, v147
	v_pk_fma_f32 v[168:169], v[108:109], v[148:149], v[168:169]
	v_pk_fma_f32 v[164:165], v[110:111], v[150:151], v[164:165]
	v_lshl_add_u64 v[192:193], v[180:181], 0, s[18:19]
	v_pk_mul_f32 v[164:165], v[164:165], v[146:147]
	v_pk_mul_f32 v[146:147], v[168:169], v[190:191]
	v_cvt_pk_bf16_f32 v144, v144, v145
	v_cvt_pk_bf16_f32 v145, v202, v203
	v_pk_mul_f32 v[198:199], v[118:119], v[166:167]
	v_cvt_pk_bf16_f32 v146, v146, v147
	v_cvt_pk_bf16_f32 v147, v164, v165
	global_store_dwordx4 v[192:193], v[144:147], off sc1
	v_pk_mul_f32 v[192:193], v[116:117], v[158:159]
	v_pk_fma_f32 v[156:157], v[98:99], v[156:157], v[198:199]
	v_lshlrev_b32_e32 v144, 16, v136
	v_and_b32_e32 v145, 0xffff0000, v136
	v_lshlrev_b32_e32 v146, 16, v137
	v_and_b32_e32 v147, 0xffff0000, v137
	v_pk_fma_f32 v[162:163], v[96:97], v[162:163], v[192:193]
	v_lshlrev_b32_e32 v164, 16, v138
	v_and_b32_e32 v165, 0xffff0000, v138
	v_lshlrev_b32_e32 v168, 16, v139
; #define CV_LO(q_) (f32x4){bf_lo((q_).x), bf_hi((q_).x), bf_lo((q_).y), bf_hi((q_).y)}
; #define CV_HI(q_) (f32x4){bf_lo((q_).z), bf_hi((q_).z), bf_lo((q_).w), bf_hi((q_).w)}
; __device__ __forceinline__ void conv_rows(const bf16_t* U, const bf16_t* CB, const float* cw, bf16_t* YC, int gw, int NGW, int lane) {
;     ...
;         for (int c2 = 0; c2 < 2; ++c2) { const int col = c2 * 512 + lane * 8;
; #pragma unroll
;             for (int i = 0; i < 10; ++i) { const int t = t0 - 1 + i; const bool ok = (i == 0) ? ((t0 & (SEQ - 1)) != 0) : (i == 9) ? (((t0 + 8) & (SEQ - 1)) != 0) : true;
;                 ur[c2][i] = (u32x4){0u, 0u, 0u, 0u}; if (ok) ur[c2][i] = __builtin_nontemporal_load((const u32x4*)(U + (size_t)t * DM + col)); }
; #pragma unroll
;             for (int i = 0; i < 8; ++i) cr[c2][i] = __builtin_nontemporal_load((const u32x4*)(CB + (size_t)(t0 + i) * DM + col)); }
; #pragma unroll
;         for (int c2 = 0; c2 < 2; ++c2) { const int col = c2 * 512 + lane * 8;
;             const f32x4 w0a = *(const f32x4*)(cw + col), w0b = *(const f32x4*)(cw + col + 4), w1a = *(const f32x4*)(cw + DM + col), w1b = *(const f32x4*)(cw + DM + col + 4),
;                         w2a = *(const f32x4*)(cw + 2 * DM + col), w2b = *(const f32x4*)(cw + 2 * DM + col + 4);
;     ...
;             f32x4 pa = CV_LO(ur[c2][0]), pb = CV_HI(ur[c2][0]), ca = CV_LO(ur[c2][1]), cb_ = CV_HI(ur[c2][1]);
; #pragma unroll
;             for (int i = 0; i < 8; ++i) { const f32x4 na = CV_LO(ur[c2][i + 2]), nb = CV_HI(ur[c2][i + 2]), ga = CV_LO(cr[c2][i]), gb = CV_HI(cr[c2][i]);
;                 st8(YC + (size_t)(t0 + i) * DM + col, ga * (w0a * pa + w1a * ca + w2a * na), gb * (w0b * pb + w1b * cb_ + w2b * nb));
;                 pa = ca; pb = cb_; ca = na; cb_ = nb; }
	v_and_b32_e32 v169, 0xffff0000, v139
	v_lshlrev_b32_e32 v136, 16, v140
	v_and_b32_e32 v137, 0xffff0000, v140
	v_lshlrev_b32_e32 v138, 16, v141
	v_and_b32_e32 v139, 0xffff0000, v141
	v_pk_fma_f32 v[162:163], v[120:121], v[144:145], v[162:163]
	v_pk_fma_f32 v[156:157], v[122:123], v[146:147], v[156:157]
	v_pk_mul_f32 v[136:137], v[162:163], v[136:137]
	v_pk_mul_f32 v[138:139], v[156:157], v[138:139]
	v_pk_mul_f32 v[156:157], v[92:93], v[148:149]
	v_pk_mul_f32 v[162:163], v[94:95], v[150:151]
	v_pk_fma_f32 v[152:153], v[88:89], v[152:153], v[156:157]
	v_pk_fma_f32 v[154:155], v[90:91], v[154:155], v[162:163]
	v_lshlrev_b32_e32 v140, 16, v142
	v_and_b32_e32 v141, 0xffff0000, v142
	v_lshlrev_b32_e32 v142, 16, v143
	v_and_b32_e32 v143, 0xffff0000, v143
	v_pk_fma_f32 v[152:153], v[108:109], v[164:165], v[152:153]
	v_pk_fma_f32 v[154:155], v[110:111], v[168:169], v[154:155]
	v_lshl_add_u64 v[190:191], v[180:181], 0, s[16:17]
	v_pk_mul_f32 v[142:143], v[154:155], v[142:143]
	v_pk_mul_f32 v[140:141], v[152:153], v[140:141]
	v_cvt_pk_bf16_f32 v136, v136, v137
	v_cvt_pk_bf16_f32 v137, v138, v139
	v_pk_mul_f32 v[154:155], v[116:117], v[144:145]
	v_cvt_pk_bf16_f32 v138, v140, v141
	v_cvt_pk_bf16_f32 v139, v142, v143
	v_pk_mul_f32 v[156:157], v[118:119], v[146:147]
	global_store_dwordx4 v[190:191], v[136:139], off sc1
	v_pk_fma_f32 v[156:157], v[98:99], v[166:167], v[156:157]
	v_pk_fma_f32 v[154:155], v[96:97], v[158:159], v[154:155]
	v_lshlrev_b32_e32 v136, 16, v128
	v_and_b32_e32 v137, 0xffff0000, v128
	v_lshlrev_b32_e32 v138, 16, v129
	v_and_b32_e32 v139, 0xffff0000, v129
	v_lshlrev_b32_e32 v140, 16, v130
	v_and_b32_e32 v141, 0xffff0000, v130
	v_lshlrev_b32_e32 v142, 16, v131
	v_and_b32_e32 v143, 0xffff0000, v131
	v_lshlrev_b32_e32 v128, 16, v132
	v_and_b32_e32 v129, 0xffff0000, v132
	v_lshlrev_b32_e32 v130, 16, v133
	v_and_b32_e32 v131, 0xffff0000, v133
	v_pk_fma_f32 v[154:155], v[120:121], v[136:137], v[154:155]
	v_pk_fma_f32 v[156:157], v[122:123], v[138:139], v[156:157]
	v_pk_mul_f32 v[128:129], v[154:155], v[128:129]
	v_pk_mul_f32 v[130:131], v[156:157], v[130:131]
	v_pk_mul_f32 v[154:155], v[92:93], v[164:165]
	v_pk_mul_f32 v[156:157], v[94:95], v[168:169]
	v_pk_fma_f32 v[148:149], v[88:89], v[148:149], v[154:155]
	v_pk_fma_f32 v[150:151], v[90:91], v[150:151], v[156:157]
	v_lshlrev_b32_e32 v132, 16, v134
	v_and_b32_e32 v133, 0xffff0000, v134
	v_lshlrev_b32_e32 v134, 16, v135
	v_and_b32_e32 v135, 0xffff0000, v135
	v_lshl_add_u64 v[152:153], v[180:181], 0, s[14:15]
	v_pk_fma_f32 v[148:149], v[108:109], v[140:141], v[148:149]
	v_pk_fma_f32 v[150:151], v[110:111], v[142:143], v[150:151]
	v_pk_mul_f32 v[132:133], v[148:149], v[132:133]
	v_pk_mul_f32 v[134:135], v[150:151], v[134:135]
	v_cvt_pk_bf16_f32 v128, v128, v129
	v_cvt_pk_bf16_f32 v129, v130, v131
	v_cvt_pk_bf16_f32 v130, v132, v133
	v_pk_mul_f32 v[150:151], v[116:117], v[136:137]
	v_cvt_pk_bf16_f32 v131, v134, v135
	global_store_dwordx4 v[152:153], v[128:131], off sc1
	v_pk_mul_f32 v[152:153], v[118:119], v[138:139]
	v_pk_fma_f32 v[144:145], v[96:97], v[144:145], v[150:151]
	v_lshlrev_b32_e32 v128, 16, v112
	v_and_b32_e32 v129, 0xffff0000, v112
	v_lshlrev_b32_e32 v130, 16, v113
	v_and_b32_e32 v131, 0xffff0000, v113
	v_pk_fma_f32 v[146:147], v[98:99], v[146:147], v[152:153]
	v_lshlrev_b32_e32 v132, 16, v114
	v_and_b32_e32 v133, 0xffff0000, v114
	v_lshlrev_b32_e32 v134, 16, v115
	v_and_b32_e32 v135, 0xffff0000, v115
	v_lshlrev_b32_e32 v112, 16, v124
	v_and_b32_e32 v113, 0xffff0000, v124
	v_lshlrev_b32_e32 v114, 16, v125
	v_and_b32_e32 v115, 0xffff0000, v125
	v_pk_fma_f32 v[144:145], v[120:121], v[128:129], v[144:145]
	v_pk_fma_f32 v[146:147], v[122:123], v[130:131], v[146:147]
	v_pk_mul_f32 v[112:113], v[144:145], v[112:113]
	v_pk_mul_f32 v[114:115], v[146:147], v[114:115]
	v_pk_mul_f32 v[144:145], v[92:93], v[140:141]
	v_pk_mul_f32 v[146:147], v[94:95], v[142:143]
	v_pk_fma_f32 v[144:145], v[88:89], v[164:165], v[144:145]
	v_pk_fma_f32 v[146:147], v[90:91], v[168:169], v[146:147]
	v_lshlrev_b32_e32 v124, 16, v126
	v_and_b32_e32 v125, 0xffff0000, v126
	v_lshlrev_b32_e32 v126, 16, v127
	v_and_b32_e32 v127, 0xffff0000, v127
	v_lshl_add_u64 v[148:149], v[180:181], 0, s[12:13]
	v_pk_fma_f32 v[144:145], v[108:109], v[132:133], v[144:145]
	v_pk_fma_f32 v[146:147], v[110:111], v[134:135], v[146:147]
	v_pk_mul_f32 v[124:125], v[144:145], v[124:125]
	v_pk_mul_f32 v[126:127], v[146:147], v[126:127]
	v_cvt_pk_bf16_f32 v112, v112, v113
	v_cvt_pk_bf16_f32 v113, v114, v115
	v_cvt_pk_bf16_f32 v114, v124, v125
	v_pk_mul_f32 v[146:147], v[116:117], v[128:129]
	v_cvt_pk_bf16_f32 v115, v126, v127
	global_store_dwordx4 v[148:149], v[112:115], off sc1
	v_pk_mul_f32 v[148:149], v[118:119], v[130:131]
	v_pk_fma_f32 v[136:137], v[96:97], v[136:137], v[146:147]
	v_lshlrev_b32_e32 v112, 16, v100
	v_and_b32_e32 v113, 0xffff0000, v100
	v_lshlrev_b32_e32 v114, 16, v101
	v_and_b32_e32 v115, 0xffff0000, v101
	v_pk_fma_f32 v[138:139], v[98:99], v[138:139], v[148:149]
	v_lshlrev_b32_e32 v124, 16, v102
	v_and_b32_e32 v125, 0xffff0000, v102
	v_lshlrev_b32_e32 v126, 16, v103
	v_and_b32_e32 v127, 0xffff0000, v103
	v_lshlrev_b32_e32 v100, 16, v104
	v_and_b32_e32 v101, 0xffff0000, v104
	v_lshlrev_b32_e32 v102, 16, v105
	v_and_b32_e32 v103, 0xffff0000, v105
	v_pk_fma_f32 v[136:137], v[120:121], v[112:113], v[136:137]
	v_pk_fma_f32 v[138:139], v[122:123], v[114:115], v[138:139]
	v_pk_mul_f32 v[100:101], v[136:137], v[100:101]
	v_pk_mul_f32 v[102:103], v[138:139], v[102:103]
	v_pk_mul_f32 v[136:137], v[92:93], v[132:133]
	v_pk_mul_f32 v[138:139], v[94:95], v[134:135]
	v_pk_fma_f32 v[136:137], v[88:89], v[140:141], v[136:137]
; #define CV_LO(q_) (f32x4){bf_lo((q_).x), bf_hi((q_).x), bf_lo((q_).y), bf_hi((q_).y)}
; #define CV_HI(q_) (f32x4){bf_lo((q_).z), bf_hi((q_).z), bf_lo((q_).w), bf_hi((q_).w)}
; __device__ __forceinline__ void conv_rows(const bf16_t* U, const bf16_t* CB, const float* cw, bf16_t* YC, int gw, int NGW, int lane) {
;     ...
;         for (int c2 = 0; c2 < 2; ++c2) { const int col = c2 * 512 + lane * 8;
; #pragma unroll
;             for (int i = 0; i < 10; ++i) { const int t = t0 - 1 + i; const bool ok = (i == 0) ? ((t0 & (SEQ - 1)) != 0) : (i == 9) ? (((t0 + 8) & (SEQ - 1)) != 0) : true;
;                 ur[c2][i] = (u32x4){0u, 0u, 0u, 0u}; if (ok) ur[c2][i] = __builtin_nontemporal_load((const u32x4*)(U + (size_t)t * DM + col)); }
; #pragma unroll
;             for (int i = 0; i < 8; ++i) cr[c2][i] = __builtin_nontemporal_load((const u32x4*)(CB + (size_t)(t0 + i) * DM + col)); }
; #pragma unroll
;         for (int c2 = 0; c2 < 2; ++c2) { const int col = c2 * 512 + lane * 8;
;             const f32x4 w0a = *(const f32x4*)(cw + col), w0b = *(const f32x4*)(cw + col + 4), w1a = *(const f32x4*)(cw + DM + col), w1b = *(const f32x4*)(cw + DM + col + 4),
;                         w2a = *(const f32x4*)(cw + 2 * DM + col), w2b = *(const f32x4*)(cw + 2 * DM + col + 4);
;     ...
;             f32x4 pa = CV_LO(ur[c2][0]), pb = CV_HI(ur[c2][0]), ca = CV_LO(ur[c2][1]), cb_ = CV_HI(ur[c2][1]);
; #pragma unroll
;             for (int i = 0; i < 8; ++i) { const f32x4 na = CV_LO(ur[c2][i + 2]), nb = CV_HI(ur[c2][i + 2]), ga = CV_LO(cr[c2][i]), gb = CV_HI(cr[c2][i]);
;                 st8(YC + (size_t)(t0 + i) * DM + col, ga * (w0a * pa + w1a * ca + w2a * na), gb * (w0b * pb + w1b * cb_ + w2b * nb));
;                 pa = ca; pb = cb_; ca = na; cb_ = nb; }
	v_pk_fma_f32 v[138:139], v[90:91], v[142:143], v[138:139]
	v_lshlrev_b32_e32 v104, 16, v106
	v_and_b32_e32 v105, 0xffff0000, v106
	v_lshlrev_b32_e32 v106, 16, v107
	v_and_b32_e32 v107, 0xffff0000, v107
	v_pk_fma_f32 v[136:137], v[108:109], v[124:125], v[136:137]
	v_pk_fma_f32 v[138:139], v[110:111], v[126:127], v[138:139]
	v_lshl_add_u64 v[144:145], v[180:181], 0, s[10:11]
	v_pk_mul_f32 v[106:107], v[138:139], v[106:107]
	v_pk_mul_f32 v[104:105], v[136:137], v[104:105]
	v_cvt_pk_bf16_f32 v100, v100, v101
	v_cvt_pk_bf16_f32 v101, v102, v103
	v_pk_mul_f32 v[138:139], v[116:117], v[112:113]
	v_cvt_pk_bf16_f32 v102, v104, v105
	v_cvt_pk_bf16_f32 v103, v106, v107
	v_pk_mul_f32 v[140:141], v[118:119], v[114:115]
	global_store_dwordx4 v[144:145], v[100:103], off sc1
	v_pk_fma_f32 v[130:131], v[98:99], v[130:131], v[140:141]
	v_pk_fma_f32 v[128:129], v[96:97], v[128:129], v[138:139]
	v_lshlrev_b32_e32 v100, 16, v80
	v_and_b32_e32 v101, 0xffff0000, v80
	v_lshlrev_b32_e32 v102, 16, v81
	v_and_b32_e32 v103, 0xffff0000, v81
	v_lshlrev_b32_e32 v104, 16, v82
	v_and_b32_e32 v105, 0xffff0000, v82
	v_lshlrev_b32_e32 v106, 16, v83
	v_and_b32_e32 v107, 0xffff0000, v83
	v_lshlrev_b32_e32 v80, 16, v84
	v_and_b32_e32 v81, 0xffff0000, v84
	v_lshlrev_b32_e32 v82, 16, v85
	v_and_b32_e32 v83, 0xffff0000, v85
	v_pk_fma_f32 v[128:129], v[120:121], v[100:101], v[128:129]
	v_pk_fma_f32 v[130:131], v[122:123], v[102:103], v[130:131]
	v_pk_mul_f32 v[80:81], v[128:129], v[80:81]
	v_pk_mul_f32 v[82:83], v[130:131], v[82:83]
	v_pk_mul_f32 v[128:129], v[92:93], v[124:125]
	v_pk_mul_f32 v[130:131], v[94:95], v[126:127]
	v_pk_fma_f32 v[128:129], v[88:89], v[132:133], v[128:129]
	v_pk_fma_f32 v[130:131], v[90:91], v[134:135], v[130:131]
	v_lshlrev_b32_e32 v84, 16, v86
	v_and_b32_e32 v85, 0xffff0000, v86
	v_lshlrev_b32_e32 v86, 16, v87
	v_and_b32_e32 v87, 0xffff0000, v87
	v_lshl_add_u64 v[136:137], v[180:181], 0, s[6:7]
	v_pk_fma_f32 v[128:129], v[108:109], v[104:105], v[128:129]
	v_pk_fma_f32 v[130:131], v[110:111], v[106:107], v[130:131]
	v_cvt_pk_bf16_f32 v80, v80, v81
	v_cvt_pk_bf16_f32 v81, v82, v83
	v_pk_mul_f32 v[100:101], v[116:117], v[100:101]
	v_pk_mul_f32 v[102:103], v[118:119], v[102:103]
	v_pk_mul_f32 v[86:87], v[130:131], v[86:87]
	v_pk_mul_f32 v[84:85], v[128:129], v[84:85]
	v_pk_fma_f32 v[98:99], v[98:99], v[114:115], v[102:103]
	v_cvt_pk_bf16_f32 v82, v84, v85
	v_cvt_pk_bf16_f32 v83, v86, v87
	global_store_dwordx4 v[136:137], v[80:83], off sc1
	v_pk_fma_f32 v[96:97], v[96:97], v[112:113], v[100:101]
	v_lshlrev_b32_e32 v84, 16, v76
	v_lshlrev_b32_e32 v80, 16, v72
	v_and_b32_e32 v81, 0xffff0000, v72
	v_lshlrev_b32_e32 v72, 16, v73
	v_and_b32_e32 v73, 0xffff0000, v73
	v_and_b32_e32 v85, 0xffff0000, v76
	v_lshlrev_b32_e32 v76, 16, v77
	v_and_b32_e32 v77, 0xffff0000, v77
	v_pk_fma_f32 v[80:81], v[120:121], v[80:81], v[96:97]
	v_pk_fma_f32 v[72:73], v[122:123], v[72:73], v[98:99]
	v_lshlrev_b32_e32 v82, 16, v74
	v_pk_mul_f32 v[76:77], v[72:73], v[76:77]
	v_pk_mul_f32 v[72:73], v[80:81], v[84:85]
	v_pk_mul_f32 v[80:81], v[92:93], v[104:105]
	v_pk_mul_f32 v[84:85], v[94:95], v[106:107]
	v_and_b32_e32 v83, 0xffff0000, v74
	v_lshlrev_b32_e32 v74, 16, v75
	v_and_b32_e32 v75, 0xffff0000, v75
	v_pk_fma_f32 v[84:85], v[90:91], v[126:127], v[84:85]
	v_pk_fma_f32 v[80:81], v[88:89], v[124:125], v[80:81]
	v_lshlrev_b32_e32 v86, 16, v78
	v_and_b32_e32 v87, 0xffff0000, v78
	v_lshlrev_b32_e32 v78, 16, v79
	v_and_b32_e32 v79, 0xffff0000, v79
	v_pk_fma_f32 v[80:81], v[108:109], v[82:83], v[80:81]
	v_pk_fma_f32 v[74:75], v[110:111], v[74:75], v[84:85]
	v_lshl_add_u64 v[128:129], v[180:181], 0, s[4:5]
	v_pk_mul_f32 v[78:79], v[74:75], v[78:79]
	v_pk_mul_f32 v[74:75], v[80:81], v[86:87]
	v_cvt_pk_bf16_f32 v72, v72, v73
	v_cvt_pk_bf16_f32 v73, v76, v77
	v_lshlrev_b32_e32 v100, 16, v64
	v_cvt_pk_bf16_f32 v74, v74, v75
	v_cvt_pk_bf16_f32 v75, v78, v79
	global_store_dwordx4 v[128:129], v[72:75], off sc1
	global_load_dwordx4 v[72:75], v[174:175], off offset:2064
	s_nop 0
	global_load_dwordx4 v[84:87], v[174:175], off offset:2048
	global_load_dwordx4 v[76:79], v[182:183], off offset:16
	global_load_dwordx4 v[88:91], v[182:183], off
	global_load_dwordx4 v[80:83], v[184:185], off offset:16
	global_load_dwordx4 v[92:95], v[184:185], off
	v_and_b32_e32 v101, 0xffff0000, v64
	v_lshlrev_b32_e32 v64, 16, v65
	v_and_b32_e32 v65, 0xffff0000, v65
	v_lshlrev_b32_e32 v96, 16, v56
	v_and_b32_e32 v97, 0xffff0000, v56
	v_lshlrev_b32_e32 v56, 16, v57
	v_and_b32_e32 v57, 0xffff0000, v57
	v_lshlrev_b32_e32 v104, 16, v60
	v_and_b32_e32 v105, 0xffff0000, v60
	v_lshlrev_b32_e32 v60, 16, v61
	v_and_b32_e32 v61, 0xffff0000, v61
	v_lshlrev_b32_e32 v102, 16, v66
	v_and_b32_e32 v103, 0xffff0000, v66
	v_lshlrev_b32_e32 v66, 16, v67
	v_and_b32_e32 v67, 0xffff0000, v67
	v_lshlrev_b32_e32 v108, 16, v68
	v_and_b32_e32 v109, 0xffff0000, v68
	v_lshlrev_b32_e32 v68, 16, v69
	v_and_b32_e32 v69, 0xffff0000, v69
	v_lshlrev_b32_e32 v98, 16, v58
	v_and_b32_e32 v99, 0xffff0000, v58
	v_lshlrev_b32_e32 v58, 16, v59
	v_and_b32_e32 v59, 0xffff0000, v59
	v_lshlrev_b32_e32 v106, 16, v62
	v_and_b32_e32 v107, 0xffff0000, v62
	v_lshlrev_b32_e32 v62, 16, v63
	v_and_b32_e32 v63, 0xffff0000, v63
	v_lshlrev_b32_e32 v110, 16, v70
	v_and_b32_e32 v111, 0xffff0000, v70
	v_lshlrev_b32_e32 v70, 16, v71
	v_and_b32_e32 v71, 0xffff0000, v71
	v_lshl_add_u64 v[112:113], v[196:197], 0, s[20:21]
	s_waitcnt vmcnt(2)
	v_pk_mul_f32 v[114:115], v[88:89], v[100:101]
	v_pk_mul_f32 v[116:117], v[90:91], v[64:65]
	v_pk_fma_f32 v[96:97], v[84:85], v[96:97], v[114:115]
	v_pk_fma_f32 v[56:57], v[86:87], v[56:57], v[116:117]
	s_waitcnt vmcnt(0)
; #define CV_LO(q_) (f32x4){bf_lo((q_).x), bf_hi((q_).x), bf_lo((q_).y), bf_hi((q_).y)}
; #define CV_HI(q_) (f32x4){bf_lo((q_).z), bf_hi((q_).z), bf_lo((q_).w), bf_hi((q_).w)}
; __device__ __forceinline__ void conv_rows(const bf16_t* U, const bf16_t* CB, const float* cw, bf16_t* YC, int gw, int NGW, int lane) {
;     ...
;         for (int c2 = 0; c2 < 2; ++c2) { const int col = c2 * 512 + lane * 8;
; #pragma unroll
;             for (int i = 0; i < 10; ++i) { const int t = t0 - 1 + i; const bool ok = (i == 0) ? ((t0 & (SEQ - 1)) != 0) : (i == 9) ? (((t0 + 8) & (SEQ - 1)) != 0) : true;
;                 ur[c2][i] = (u32x4){0u, 0u, 0u, 0u}; if (ok) ur[c2][i] = __builtin_nontemporal_load((const u32x4*)(U + (size_t)t * DM + col)); }
; #pragma unroll
;             for (int i = 0; i < 8; ++i) cr[c2][i] = __builtin_nontemporal_load((const u32x4*)(CB + (size_t)(t0 + i) * DM + col)); }
; #pragma unroll
;         for (int c2 = 0; c2 < 2; ++c2) { const int col = c2 * 512 + lane * 8;
;             const f32x4 w0a = *(const f32x4*)(cw + col), w0b = *(const f32x4*)(cw + col + 4), w1a = *(const f32x4*)(cw + DM + col), w1b = *(const f32x4*)(cw + DM + col + 4),
;                         w2a = *(const f32x4*)(cw + 2 * DM + col), w2b = *(const f32x4*)(cw + 2 * DM + col + 4);
;     ...
;             f32x4 pa = CV_LO(ur[c2][0]), pb = CV_HI(ur[c2][0]), ca = CV_LO(ur[c2][1]), cb_ = CV_HI(ur[c2][1]);
; #pragma unroll
;             for (int i = 0; i < 8; ++i) { const f32x4 na = CV_LO(ur[c2][i + 2]), nb = CV_HI(ur[c2][i + 2]), ga = CV_LO(cr[c2][i]), gb = CV_HI(cr[c2][i]);
;                 st8(YC + (size_t)(t0 + i) * DM + col, ga * (w0a * pa + w1a * ca + w2a * na), gb * (w0b * pb + w1b * cb_ + w2b * nb));
;                 pa = ca; pb = cb_; ca = na; cb_ = nb; }
	v_pk_fma_f32 v[96:97], v[92:93], v[104:105], v[96:97]
	v_pk_fma_f32 v[56:57], v[94:95], v[60:61], v[56:57]
	s_nop 0
	v_pk_mul_f32 v[68:69], v[56:57], v[68:69]
	v_pk_mul_f32 v[56:57], v[96:97], v[108:109]
	v_pk_mul_f32 v[96:97], v[76:77], v[102:103]
	v_pk_mul_f32 v[108:109], v[78:79], v[66:67]
	v_pk_fma_f32 v[96:97], v[72:73], v[98:99], v[96:97]
	v_pk_fma_f32 v[58:59], v[74:75], v[58:59], v[108:109]
	v_pk_fma_f32 v[96:97], v[80:81], v[106:107], v[96:97]
	v_pk_fma_f32 v[58:59], v[82:83], v[62:63], v[58:59]
	v_cvt_pk_bf16_f32 v56, v56, v57
	v_cvt_pk_bf16_f32 v57, v68, v69
	v_pk_mul_f32 v[98:99], v[88:89], v[104:105]
	v_pk_mul_f32 v[70:71], v[58:59], v[70:71]
	v_pk_mul_f32 v[58:59], v[96:97], v[110:111]
	v_pk_mul_f32 v[108:109], v[90:91], v[60:61]
	v_cvt_pk_bf16_f32 v58, v58, v59
	v_cvt_pk_bf16_f32 v59, v70, v71
	global_store_dwordx4 v[112:113], v[56:59], off sc1
	v_pk_fma_f32 v[64:65], v[86:87], v[64:65], v[108:109]
	v_pk_fma_f32 v[98:99], v[84:85], v[100:101], v[98:99]
	v_lshlrev_b32_e32 v56, 16, v48
	v_and_b32_e32 v57, 0xffff0000, v48
	v_lshlrev_b32_e32 v58, 16, v49
	v_and_b32_e32 v59, 0xffff0000, v49
	v_lshlrev_b32_e32 v68, 16, v50
	v_and_b32_e32 v69, 0xffff0000, v50
	v_lshlrev_b32_e32 v70, 16, v51
	v_and_b32_e32 v71, 0xffff0000, v51
	v_lshlrev_b32_e32 v48, 16, v52
	v_and_b32_e32 v49, 0xffff0000, v52
	v_lshlrev_b32_e32 v50, 16, v53
	v_and_b32_e32 v51, 0xffff0000, v53
	v_pk_fma_f32 v[98:99], v[92:93], v[56:57], v[98:99]
	v_pk_fma_f32 v[64:65], v[94:95], v[58:59], v[64:65]
	v_pk_mul_f32 v[48:49], v[98:99], v[48:49]
	v_pk_mul_f32 v[50:51], v[64:65], v[50:51]
	v_pk_mul_f32 v[64:65], v[76:77], v[106:107]
	v_pk_mul_f32 v[98:99], v[78:79], v[62:63]
	v_pk_fma_f32 v[64:65], v[72:73], v[102:103], v[64:65]
	v_pk_fma_f32 v[66:67], v[74:75], v[66:67], v[98:99]
	v_lshlrev_b32_e32 v52, 16, v54
	v_and_b32_e32 v53, 0xffff0000, v54
	v_lshlrev_b32_e32 v54, 16, v55
	v_and_b32_e32 v55, 0xffff0000, v55
	v_lshl_add_u64 v[96:97], v[196:197], 0, s[18:19]
	v_pk_fma_f32 v[64:65], v[80:81], v[68:69], v[64:65]
	v_pk_fma_f32 v[66:67], v[82:83], v[70:71], v[66:67]
	v_pk_mul_f32 v[52:53], v[64:65], v[52:53]
	v_pk_mul_f32 v[54:55], v[66:67], v[54:55]
	v_cvt_pk_bf16_f32 v48, v48, v49
	v_cvt_pk_bf16_f32 v49, v50, v51
	v_cvt_pk_bf16_f32 v50, v52, v53
	v_pk_mul_f32 v[66:67], v[88:89], v[56:57]
	v_cvt_pk_bf16_f32 v51, v54, v55
	global_store_dwordx4 v[96:97], v[48:51], off sc1
	v_pk_mul_f32 v[96:97], v[90:91], v[58:59]
	v_pk_fma_f32 v[66:67], v[84:85], v[104:105], v[66:67]
	v_lshlrev_b32_e32 v48, 16, v40
	v_and_b32_e32 v49, 0xffff0000, v40
	v_lshlrev_b32_e32 v50, 16, v41
	v_and_b32_e32 v51, 0xffff0000, v41
	v_pk_fma_f32 v[60:61], v[86:87], v[60:61], v[96:97]
	v_lshlrev_b32_e32 v52, 16, v42
	v_and_b32_e32 v53, 0xffff0000, v42
	v_lshlrev_b32_e32 v54, 16, v43
	v_and_b32_e32 v55, 0xffff0000, v43
	v_lshlrev_b32_e32 v40, 16, v44
	v_and_b32_e32 v41, 0xffff0000, v44
	v_lshlrev_b32_e32 v42, 16, v45
	v_and_b32_e32 v43, 0xffff0000, v45
	v_pk_fma_f32 v[66:67], v[92:93], v[48:49], v[66:67]
	v_pk_fma_f32 v[60:61], v[94:95], v[50:51], v[60:61]
	v_pk_mul_f32 v[40:41], v[66:67], v[40:41]
	v_pk_mul_f32 v[42:43], v[60:61], v[42:43]
	v_pk_mul_f32 v[60:61], v[76:77], v[68:69]
	v_pk_mul_f32 v[66:67], v[78:79], v[70:71]
	v_pk_fma_f32 v[60:61], v[72:73], v[106:107], v[60:61]
	v_pk_fma_f32 v[62:63], v[74:75], v[62:63], v[66:67]
	v_lshlrev_b32_e32 v44, 16, v46
	v_and_b32_e32 v45, 0xffff0000, v46
	v_lshlrev_b32_e32 v46, 16, v47
	v_and_b32_e32 v47, 0xffff0000, v47
	v_lshl_add_u64 v[64:65], v[196:197], 0, s[16:17]
	v_pk_fma_f32 v[60:61], v[80:81], v[52:53], v[60:61]
	v_pk_fma_f32 v[62:63], v[82:83], v[54:55], v[62:63]
	v_pk_mul_f32 v[44:45], v[60:61], v[44:45]
	v_pk_mul_f32 v[46:47], v[62:63], v[46:47]
	v_cvt_pk_bf16_f32 v40, v40, v41
	v_cvt_pk_bf16_f32 v41, v42, v43
	v_cvt_pk_bf16_f32 v42, v44, v45
	v_pk_mul_f32 v[62:63], v[88:89], v[48:49]
	v_cvt_pk_bf16_f32 v43, v46, v47
	global_store_dwordx4 v[64:65], v[40:43], off sc1
	v_pk_mul_f32 v[64:65], v[90:91], v[50:51]
	v_pk_fma_f32 v[56:57], v[84:85], v[56:57], v[62:63]
	v_lshlrev_b32_e32 v40, 16, v32
	v_and_b32_e32 v41, 0xffff0000, v32
	v_lshlrev_b32_e32 v42, 16, v33
	v_and_b32_e32 v43, 0xffff0000, v33
	v_pk_fma_f32 v[58:59], v[86:87], v[58:59], v[64:65]
	v_lshlrev_b32_e32 v44, 16, v34
	v_and_b32_e32 v45, 0xffff0000, v34
	v_lshlrev_b32_e32 v46, 16, v35
	v_and_b32_e32 v47, 0xffff0000, v35
	v_lshlrev_b32_e32 v32, 16, v36
	v_and_b32_e32 v33, 0xffff0000, v36
	v_lshlrev_b32_e32 v34, 16, v37
	v_and_b32_e32 v35, 0xffff0000, v37
	v_pk_fma_f32 v[56:57], v[92:93], v[40:41], v[56:57]
	v_pk_fma_f32 v[58:59], v[94:95], v[42:43], v[58:59]
	v_pk_mul_f32 v[32:33], v[56:57], v[32:33]
	v_pk_mul_f32 v[34:35], v[58:59], v[34:35]
	v_pk_mul_f32 v[56:57], v[76:77], v[52:53]
	v_pk_mul_f32 v[58:59], v[78:79], v[54:55]
	v_pk_fma_f32 v[56:57], v[72:73], v[68:69], v[56:57]
	v_pk_fma_f32 v[58:59], v[74:75], v[70:71], v[58:59]
	v_lshlrev_b32_e32 v36, 16, v38
	v_and_b32_e32 v37, 0xffff0000, v38
	v_lshlrev_b32_e32 v38, 16, v39
	v_and_b32_e32 v39, 0xffff0000, v39
	v_lshl_add_u64 v[60:61], v[196:197], 0, s[14:15]
	v_pk_fma_f32 v[56:57], v[80:81], v[44:45], v[56:57]
	v_pk_fma_f32 v[58:59], v[82:83], v[46:47], v[58:59]
	v_pk_mul_f32 v[36:37], v[56:57], v[36:37]
	v_pk_mul_f32 v[38:39], v[58:59], v[38:39]
	v_cvt_pk_bf16_f32 v32, v32, v33
	v_cvt_pk_bf16_f32 v33, v34, v35
	v_cvt_pk_bf16_f32 v34, v36, v37
	v_pk_mul_f32 v[58:59], v[88:89], v[40:41]
	v_cvt_pk_bf16_f32 v35, v38, v39
	global_store_dwordx4 v[60:61], v[32:35], off sc1
	v_pk_mul_f32 v[60:61], v[90:91], v[42:43]
	v_pk_fma_f32 v[48:49], v[84:85], v[48:49], v[58:59]
	v_lshlrev_b32_e32 v32, 16, v24
	v_and_b32_e32 v33, 0xffff0000, v24
; #define CV_LO(q_) (f32x4){bf_lo((q_).x), bf_hi((q_).x), bf_lo((q_).y), bf_hi((q_).y)}
; #define CV_HI(q_) (f32x4){bf_lo((q_).z), bf_hi((q_).z), bf_lo((q_).w), bf_hi((q_).w)}
; __device__ __forceinline__ void conv_rows(const bf16_t* U, const bf16_t* CB, const float* cw, bf16_t* YC, int gw, int NGW, int lane) {
;     ...
;         for (int c2 = 0; c2 < 2; ++c2) { const int col = c2 * 512 + lane * 8;
; #pragma unroll
;             for (int i = 0; i < 10; ++i) { const int t = t0 - 1 + i; const bool ok = (i == 0) ? ((t0 & (SEQ - 1)) != 0) : (i == 9) ? (((t0 + 8) & (SEQ - 1)) != 0) : true;
;                 ur[c2][i] = (u32x4){0u, 0u, 0u, 0u}; if (ok) ur[c2][i] = __builtin_nontemporal_load((const u32x4*)(U + (size_t)t * DM + col)); }
; #pragma unroll
;             for (int i = 0; i < 8; ++i) cr[c2][i] = __builtin_nontemporal_load((const u32x4*)(CB + (size_t)(t0 + i) * DM + col)); }
; #pragma unroll
;         for (int c2 = 0; c2 < 2; ++c2) { const int col = c2 * 512 + lane * 8;
;             const f32x4 w0a = *(const f32x4*)(cw + col), w0b = *(const f32x4*)(cw + col + 4), w1a = *(const f32x4*)(cw + DM + col), w1b = *(const f32x4*)(cw + DM + col + 4),
;                         w2a = *(const f32x4*)(cw + 2 * DM + col), w2b = *(const f32x4*)(cw + 2 * DM + col + 4);
;     ...
;             f32x4 pa = CV_LO(ur[c2][0]), pb = CV_HI(ur[c2][0]), ca = CV_LO(ur[c2][1]), cb_ = CV_HI(ur[c2][1]);
; #pragma unroll
;             for (int i = 0; i < 8; ++i) { const f32x4 na = CV_LO(ur[c2][i + 2]), nb = CV_HI(ur[c2][i + 2]), ga = CV_LO(cr[c2][i]), gb = CV_HI(cr[c2][i]);
;                 st8(YC + (size_t)(t0 + i) * DM + col, ga * (w0a * pa + w1a * ca + w2a * na), gb * (w0b * pb + w1b * cb_ + w2b * nb));
;                 pa = ca; pb = cb_; ca = na; cb_ = nb; }
	v_lshlrev_b32_e32 v34, 16, v25
	v_and_b32_e32 v35, 0xffff0000, v25
	v_pk_fma_f32 v[50:51], v[86:87], v[50:51], v[60:61]
	v_lshlrev_b32_e32 v36, 16, v26
	v_and_b32_e32 v37, 0xffff0000, v26
	v_lshlrev_b32_e32 v38, 16, v27
	v_and_b32_e32 v39, 0xffff0000, v27
	v_lshlrev_b32_e32 v24, 16, v28
	v_and_b32_e32 v25, 0xffff0000, v28
	v_lshlrev_b32_e32 v26, 16, v29
	v_and_b32_e32 v27, 0xffff0000, v29
	v_pk_fma_f32 v[48:49], v[92:93], v[32:33], v[48:49]
	v_pk_fma_f32 v[50:51], v[94:95], v[34:35], v[50:51]
	v_pk_mul_f32 v[24:25], v[48:49], v[24:25]
	v_pk_mul_f32 v[26:27], v[50:51], v[26:27]
	v_pk_mul_f32 v[48:49], v[76:77], v[44:45]
	v_pk_mul_f32 v[50:51], v[78:79], v[46:47]
	v_pk_fma_f32 v[48:49], v[72:73], v[52:53], v[48:49]
	v_pk_fma_f32 v[50:51], v[74:75], v[54:55], v[50:51]
	v_lshlrev_b32_e32 v28, 16, v30
	v_and_b32_e32 v29, 0xffff0000, v30
	v_lshlrev_b32_e32 v30, 16, v31
	v_and_b32_e32 v31, 0xffff0000, v31
	v_pk_fma_f32 v[48:49], v[80:81], v[36:37], v[48:49]
	v_pk_fma_f32 v[50:51], v[82:83], v[38:39], v[50:51]
	v_lshl_add_u64 v[56:57], v[196:197], 0, s[12:13]
	v_pk_mul_f32 v[30:31], v[50:51], v[30:31]
	v_pk_mul_f32 v[28:29], v[48:49], v[28:29]
	v_cvt_pk_bf16_f32 v24, v24, v25
	v_cvt_pk_bf16_f32 v25, v26, v27
	v_pk_mul_f32 v[50:51], v[88:89], v[32:33]
	v_cvt_pk_bf16_f32 v26, v28, v29
	v_cvt_pk_bf16_f32 v27, v30, v31
	v_pk_mul_f32 v[52:53], v[90:91], v[34:35]
	global_store_dwordx4 v[56:57], v[24:27], off sc1
	v_pk_fma_f32 v[42:43], v[86:87], v[42:43], v[52:53]
	v_pk_fma_f32 v[40:41], v[84:85], v[40:41], v[50:51]
	v_lshlrev_b32_e32 v24, 16, v16
	v_and_b32_e32 v25, 0xffff0000, v16
	v_lshlrev_b32_e32 v26, 16, v17
	v_and_b32_e32 v27, 0xffff0000, v17
	v_lshlrev_b32_e32 v28, 16, v18
	v_and_b32_e32 v29, 0xffff0000, v18
	v_lshlrev_b32_e32 v30, 16, v19
	v_and_b32_e32 v31, 0xffff0000, v19
	v_lshlrev_b32_e32 v16, 16, v20
	v_and_b32_e32 v17, 0xffff0000, v20
	v_lshlrev_b32_e32 v18, 16, v21
	v_and_b32_e32 v19, 0xffff0000, v21
	v_pk_fma_f32 v[40:41], v[92:93], v[24:25], v[40:41]
	v_pk_fma_f32 v[42:43], v[94:95], v[26:27], v[42:43]
	v_pk_mul_f32 v[16:17], v[40:41], v[16:17]
	v_pk_mul_f32 v[18:19], v[42:43], v[18:19]
	v_pk_mul_f32 v[40:41], v[76:77], v[36:37]
	v_pk_mul_f32 v[42:43], v[78:79], v[38:39]
	v_pk_fma_f32 v[40:41], v[72:73], v[44:45], v[40:41]
	v_pk_fma_f32 v[42:43], v[74:75], v[46:47], v[42:43]
	v_lshlrev_b32_e32 v20, 16, v22
	v_and_b32_e32 v21, 0xffff0000, v22
	v_lshlrev_b32_e32 v22, 16, v23
	v_and_b32_e32 v23, 0xffff0000, v23
	v_pk_fma_f32 v[40:41], v[80:81], v[28:29], v[40:41]
	v_pk_fma_f32 v[42:43], v[82:83], v[30:31], v[42:43]
	v_lshl_add_u64 v[48:49], v[196:197], 0, s[10:11]
	v_pk_mul_f32 v[22:23], v[42:43], v[22:23]
	v_pk_mul_f32 v[20:21], v[40:41], v[20:21]
	v_cvt_pk_bf16_f32 v16, v16, v17
	v_cvt_pk_bf16_f32 v17, v18, v19
	v_pk_mul_f32 v[42:43], v[88:89], v[24:25]
	v_cvt_pk_bf16_f32 v18, v20, v21
	v_cvt_pk_bf16_f32 v19, v22, v23
	v_pk_mul_f32 v[44:45], v[90:91], v[26:27]
	global_store_dwordx4 v[48:49], v[16:19], off sc1
	v_pk_fma_f32 v[34:35], v[86:87], v[34:35], v[44:45]
	v_pk_fma_f32 v[32:33], v[84:85], v[32:33], v[42:43]
	v_lshlrev_b32_e32 v16, 16, v8
	v_and_b32_e32 v17, 0xffff0000, v8
	v_lshlrev_b32_e32 v18, 16, v9
	v_and_b32_e32 v19, 0xffff0000, v9
	v_lshlrev_b32_e32 v20, 16, v10
	v_and_b32_e32 v21, 0xffff0000, v10
	v_lshlrev_b32_e32 v22, 16, v11
	v_and_b32_e32 v23, 0xffff0000, v11
	v_lshlrev_b32_e32 v8, 16, v12
	v_and_b32_e32 v9, 0xffff0000, v12
	v_lshlrev_b32_e32 v10, 16, v13
	v_and_b32_e32 v11, 0xffff0000, v13
	v_pk_fma_f32 v[32:33], v[92:93], v[16:17], v[32:33]
	v_pk_fma_f32 v[34:35], v[94:95], v[18:19], v[34:35]
	v_pk_mul_f32 v[8:9], v[32:33], v[8:9]
	v_pk_mul_f32 v[10:11], v[34:35], v[10:11]
	v_pk_mul_f32 v[32:33], v[76:77], v[28:29]
	v_pk_mul_f32 v[34:35], v[78:79], v[30:31]
	v_pk_fma_f32 v[32:33], v[72:73], v[36:37], v[32:33]
	v_pk_fma_f32 v[34:35], v[74:75], v[38:39], v[34:35]
	v_lshlrev_b32_e32 v12, 16, v14
	v_and_b32_e32 v13, 0xffff0000, v14
	v_lshlrev_b32_e32 v14, 16, v15
	v_and_b32_e32 v15, 0xffff0000, v15
	v_lshl_add_u64 v[40:41], v[196:197], 0, s[6:7]
	v_pk_fma_f32 v[32:33], v[80:81], v[20:21], v[32:33]
	v_pk_fma_f32 v[34:35], v[82:83], v[22:23], v[34:35]
	v_cvt_pk_bf16_f32 v8, v8, v9
	v_cvt_pk_bf16_f32 v9, v10, v11
	v_pk_mul_f32 v[16:17], v[88:89], v[16:17]
	v_pk_mul_f32 v[18:19], v[90:91], v[18:19]
	v_pk_mul_f32 v[14:15], v[34:35], v[14:15]
	v_pk_mul_f32 v[12:13], v[32:33], v[12:13]
	v_pk_fma_f32 v[18:19], v[86:87], v[26:27], v[18:19]
	v_cvt_pk_bf16_f32 v10, v12, v13
	v_cvt_pk_bf16_f32 v11, v14, v15
	global_store_dwordx4 v[40:41], v[8:11], off sc1
	v_pk_fma_f32 v[16:17], v[84:85], v[24:25], v[16:17]
	v_lshlrev_b32_e32 v12, 16, v4
	v_lshlrev_b32_e32 v8, 16, v0
	v_and_b32_e32 v9, 0xffff0000, v0
	v_lshlrev_b32_e32 v0, 16, v1
	v_and_b32_e32 v1, 0xffff0000, v1
	v_and_b32_e32 v13, 0xffff0000, v4
	v_lshlrev_b32_e32 v4, 16, v5
	v_and_b32_e32 v5, 0xffff0000, v5
	v_pk_fma_f32 v[8:9], v[92:93], v[8:9], v[16:17]
	v_pk_fma_f32 v[0:1], v[94:95], v[0:1], v[18:19]
	v_lshlrev_b32_e32 v10, 16, v2
	v_pk_mul_f32 v[4:5], v[0:1], v[4:5]
	v_pk_mul_f32 v[0:1], v[8:9], v[12:13]
	v_pk_mul_f32 v[8:9], v[76:77], v[20:21]
	v_pk_mul_f32 v[12:13], v[78:79], v[22:23]
	v_and_b32_e32 v11, 0xffff0000, v2
	v_lshlrev_b32_e32 v2, 16, v3
	v_and_b32_e32 v3, 0xffff0000, v3
	v_pk_fma_f32 v[12:13], v[74:75], v[30:31], v[12:13]
	v_pk_fma_f32 v[8:9], v[72:73], v[28:29], v[8:9]
	v_lshlrev_b32_e32 v14, 16, v6
	v_and_b32_e32 v15, 0xffff0000, v6
	v_lshlrev_b32_e32 v6, 16, v7
	v_and_b32_e32 v7, 0xffff0000, v7
	v_pk_fma_f32 v[8:9], v[80:81], v[10:11], v[8:9]
	v_pk_fma_f32 v[2:3], v[82:83], v[2:3], v[12:13]
	v_lshl_add_u64 v[32:33], v[196:197], 0, s[4:5]
	v_pk_mul_f32 v[6:7], v[2:3], v[6:7]
	v_pk_mul_f32 v[2:3], v[8:9], v[14:15]
	v_cvt_pk_bf16_f32 v0, v0, v1
	v_cvt_pk_bf16_f32 v1, v4, v5
	s_nop 0
	v_cvt_pk_bf16_f32 v2, v2, v3
	v_cvt_pk_bf16_f32 v3, v6, v7
	global_store_dwordx4 v[32:33], v[0:3], off sc1
	s_cbranch_scc0 .LBB0_814

; __device__ __forceinline__ float bf_lo(unsigned w) { return __uint_as_float(w << 16); }
; __device__ __forceinline__ float bf_hi(unsigned w) { return __uint_as_float(w & 0xffff0000u); }
; __device__ __forceinline__ int crow(int r, int hi) { return (r & 3) + 8 * (r >> 2) + 4 * hi; }
; __device__ __forceinline__ void diff_pass(const bf16_t* __restrict__ Qb, const bf16_t* __restrict__ Kh, const bf16_t* __restrict__ Vh, int seq, char* lds, f32x16 (&o)[4], const int wave_) {
;     ...
;     if (hi == 0) li_l[r32] = l_reg; asm volatile("s_waitcnt lgkmcnt(0)" ::: "memory");
; #pragma unroll
;     for (int r = 0; r < 16; ++r) { const float rl = __builtin_amdgcn_rcpf(li_l[crow(r, hi)]);
; #pragma unroll
;         for (int d = 0; d < 4; ++d) o[d][r] *= rl; }
; __device__ __forceinline__ void diff_unit(int b, int h, int qb, const bf16_t* Q, const bf16_t* K, const bf16_t* V, bf16_t* YA, float lam, float omli, const float* subln, char* lds, const int wave_) {
;     ...
;     for (int r = 0; r < 16; ++r) { float s = 0.f;
; #pragma unroll
;         for (int d = 0; d < 4; ++d) { const unsigned pw = park[(d * 8 + (r >> 1)) * 64]; const float a = (r & 1) ? bf_hi(pw) : bf_lo(pw); const float v = a - lam * o[d][r]; o[d][r] = v; s += v * v; }
;         ss[r] = s; }
.LBB0_821:
	s_or_b64 exec, exec, s[10:11]
	s_waitcnt lgkmcnt(0)
	v_add_u32_e32 v65, v217, v160
	ds_read_b128 v[66:69], v65
	ds_read_b128 v[80:83], v65 offset:32
	s_mov_b32 s2, 0xf800000
	v_and_b32_e32 v64, 31, v207
	s_lshl_b32 s64, s38, 1
	s_waitcnt lgkmcnt(1)
	v_rcp_f32_e32 v66, v66
	s_nop 0
	v_mul_f32_e32 v79, v0, v66
	v_rcp_f32_e32 v0, v67
	v_mul_f32_e32 v73, v32, v66
	v_mul_f32_e32 v76, v48, v66
	v_mul_f32_e32 v16, v16, v66
	v_mul_f32_e32 v92, v1, v0
	v_mul_f32_e32 v93, v49, v0
	v_mul_f32_e32 v94, v33, v0
	v_mul_f32_e32 v95, v17, v0
	v_rcp_f32_e32 v0, v68
	s_nop 0
	v_mul_f32_e32 v96, v2, v0
	v_mul_f32_e32 v97, v50, v0
	v_mul_f32_e32 v98, v34, v0
	v_mul_f32_e32 v99, v18, v0
	v_rcp_f32_e32 v0, v69
	s_nop 0
	v_mul_f32_e32 v100, v3, v0
	v_mul_f32_e32 v101, v51, v0
	v_mul_f32_e32 v102, v35, v0
	v_mul_f32_e32 v103, v19, v0
	s_waitcnt lgkmcnt(0)
	v_rcp_f32_e32 v0, v80
	s_nop 0
	v_mul_f32_e32 v35, v4, v0
	v_mul_f32_e32 v34, v52, v0
	v_mul_f32_e32 v33, v36, v0
	v_mul_f32_e32 v32, v20, v0
	v_rcp_f32_e32 v0, v81
	s_nop 0
	v_mul_f32_e32 v36, v5, v0
	v_mul_f32_e32 v70, v53, v0
	v_mul_f32_e32 v68, v37, v0
	v_mul_f32_e32 v66, v21, v0
	v_rcp_f32_e32 v0, v82
	s_nop 0
	v_mul_f32_e32 v80, v6, v0
	v_mul_f32_e32 v78, v54, v0
	v_mul_f32_e32 v74, v38, v0
	v_mul_f32_e32 v72, v22, v0
	v_rcp_f32_e32 v0, v83
	s_nop 0
	v_mul_f32_e32 v91, v7, v0
	v_mul_f32_e32 v90, v55, v0
	v_mul_f32_e32 v77, v39, v0
	v_mul_f32_e32 v75, v23, v0
	ds_read_b128 v[0:3], v65 offset:64
	s_waitcnt lgkmcnt(0)
	v_rcp_f32_e32 v0, v0
	s_nop 0
	v_mul_f32_e32 v53, v8, v0
	v_mul_f32_e32 v51, v56, v0
	v_mul_f32_e32 v54, v40, v0
	v_mul_f32_e32 v55, v24, v0
	v_rcp_f32_e32 v0, v1
	s_nop 0
	v_mul_f32_e32 v52, v9, v0
	v_mul_f32_e32 v49, v57, v0
	v_mul_f32_e32 v50, v41, v0
	v_mul_f32_e32 v48, v25, v0
	v_rcp_f32_e32 v0, v2
	s_nop 0
	v_mul_f32_e32 v56, v10, v0
	v_mul_f32_e32 v41, v58, v0
	v_mul_f32_e32 v40, v42, v0
	v_mul_f32_e32 v7, v26, v0
	v_rcp_f32_e32 v0, v3
	s_nop 0
	v_mul_f32_e32 v5, v11, v0
	ds_read_b128 v[8:11], v65 offset:96
	v_mul_f32_e32 v3, v59, v0
	s_waitcnt lgkmcnt(0)
	ds_read2st64_b32 v[24:25], v216 offset0:8 offset1:9
	v_mul_f32_e32 v1, v43, v0
	s_waitcnt lgkmcnt(1)
	v_rcp_f32_e32 v8, v8
	v_mul_f32_e32 v0, v27, v0
	ds_read2st64_b32 v[26:27], v216 offset0:16 offset1:17
	ds_read2st64_b32 v[42:43], v216 offset0:10 offset1:11
	v_mul_f32_e32 v2, v12, v8
	v_mul_f32_e32 v4, v60, v8
	v_mul_f32_e32 v6, v44, v8
	v_mul_f32_e32 v59, v28, v8
	v_rcp_f32_e32 v8, v9
	s_nop 0
	v_mul_f32_e32 v67, v13, v8
	v_mul_f32_e32 v61, v61, v8
	v_mul_f32_e32 v65, v45, v8
	v_mul_f32_e32 v60, v29, v8
	v_rcp_f32_e32 v8, v10
	ds_read2st64_b32 v[28:29], v216 offset0:24 offset1:25
	ds_read2st64_b32 v[44:45], v216 offset0:18 offset1:19
	v_mul_f32_e32 v85, v14, v8
	v_mul_f32_e32 v71, v62, v8
	v_mul_f32_e32 v84, v46, v8
	v_mul_f32_e32 v69, v30, v8
	v_rcp_f32_e32 v8, v11
	s_nop 0
	v_mul_f32_e32 v89, v15, v8
	v_mul_f32_e32 v88, v63, v8
	v_mul_f32_e32 v87, v47, v8
	v_mul_f32_e32 v86, v31, v8
	ds_read2st64_b32 v[8:9], v216 offset1:1
	ds_read2st64_b32 v[46:47], v216 offset0:26 offset1:27
	ds_read2st64_b32 v[62:63], v216 offset0:12 offset1:13
	s_waitcnt lgkmcnt(2)
	v_lshlrev_b32_e32 v10, 16, v8
	v_and_b32_e32 v8, 0xffff0000, v8
	v_fma_f32 v21, -v197, v79, v10
	v_lshlrev_b32_e32 v10, 16, v24
	v_fma_f32 v20, -v197, v92, v8
	v_and_b32_e32 v8, 0xffff0000, v24
	v_fma_f32 v19, -v197, v76, v10
	v_lshlrev_b32_e32 v10, 16, v26
	v_fma_f32 v17, -v197, v93, v8
	v_and_b32_e32 v8, 0xffff0000, v26
	v_fma_f32 v22, -v197, v73, v10
	v_lshlrev_b32_e32 v10, 16, v28
	v_fma_f32 v18, -v197, v94, v8
	v_and_b32_e32 v8, 0xffff0000, v28
	v_fma_f32 v23, -v197, v16, v10
	v_fma_f32 v16, -v197, v95, v8
	v_lshlrev_b32_e32 v8, 16, v9
	v_fma_f32 v15, -v197, v96, v8
	v_lshlrev_b32_e32 v8, 16, v25
	v_fma_f32 v13, -v197, v97, v8
	v_lshlrev_b32_e32 v8, 16, v27
	v_fma_f32 v14, -v197, v98, v8
	v_lshlrev_b32_e32 v8, 16, v29
	v_fma_f32 v12, -v197, v99, v8
	v_and_b32_e32 v8, 0xffff0000, v9
	v_fma_f32 v11, -v197, v100, v8
	v_and_b32_e32 v8, 0xffff0000, v25
	ds_read2st64_b32 v[24:25], v216 offset0:2 offset1:3
	v_fma_f32 v9, -v197, v101, v8
	v_and_b32_e32 v8, 0xffff0000, v27
	v_fma_f32 v10, -v197, v102, v8
	v_and_b32_e32 v8, 0xffff0000, v29
	s_waitcnt lgkmcnt(0)
	v_lshlrev_b32_e32 v26, 16, v24
	v_fma_f32 v37, -v197, v35, v26
	v_lshlrev_b32_e32 v26, 16, v42
	v_and_b32_e32 v24, 0xffff0000, v24
	v_fma_f32 v35, -v197, v34, v26
	v_lshlrev_b32_e32 v26, 16, v44
	v_fma_f32 v36, -v197, v36, v24
	v_and_b32_e32 v24, 0xffff0000, v42
	v_fma_f32 v38, -v197, v33, v26
	v_fma_f32 v33, -v197, v70, v24
	v_and_b32_e32 v24, 0xffff0000, v44
	v_lshlrev_b32_e32 v26, 16, v46
	v_fma_f32 v34, -v197, v68, v24
	v_and_b32_e32 v24, 0xffff0000, v46
	v_fma_f32 v39, -v197, v32, v26
	v_fma_f32 v32, -v197, v66, v24
	v_lshlrev_b32_e32 v24, 16, v25
	v_fma_f32 v31, -v197, v80, v24
	v_lshlrev_b32_e32 v24, 16, v43
	v_fma_f32 v29, -v197, v78, v24
	v_lshlrev_b32_e32 v24, 16, v45
	v_fma_f32 v30, -v197, v74, v24
	v_lshlrev_b32_e32 v24, 16, v47
	v_fma_f32 v28, -v197, v72, v24
	v_and_b32_e32 v24, 0xffff0000, v25
	v_fma_f32 v27, -v197, v91, v24
	v_and_b32_e32 v24, 0xffff0000, v43
	ds_read2st64_b32 v[42:43], v216 offset0:4 offset1:5
	ds_read2st64_b32 v[92:93], v216 offset0:28 offset1:29
	v_fma_f32 v25, -v197, v90, v24
	ds_read2st64_b32 v[90:91], v216 offset0:20 offset1:21
	v_and_b32_e32 v24, 0xffff0000, v45
	s_waitcnt lgkmcnt(2)
	v_lshlrev_b32_e32 v44, 16, v42
	v_and_b32_e32 v42, 0xffff0000, v42
	v_fma_f32 v52, -v197, v52, v42
	v_and_b32_e32 v42, 0xffff0000, v62
	v_fma_f32 v49, -v197, v49, v42
	s_waitcnt lgkmcnt(0)
; __device__ __forceinline__ float bf_lo(unsigned w) { return __uint_as_float(w << 16); }
; __device__ __forceinline__ float bf_hi(unsigned w) { return __uint_as_float(w & 0xffff0000u); }
; __device__ __forceinline__ float sum32(float v) { v += swz_xor<1>(v); v += swz_xor<2>(v); v += swz_xor<4>(v); v += swz_xor<8>(v); v += swz_xor<16>(v); return v; }
; __device__ __forceinline__ void diff_unit(int b, int h, int qb, const bf16_t* Q, const bf16_t* K, const bf16_t* V, bf16_t* YA, float lam, float omli, const float* subln, char* lds, const int wave_) {
;     ...
;     for (int r = 0; r < 16; ++r) { float s = 0.f;
; #pragma unroll
;         for (int d = 0; d < 4; ++d) { const unsigned pw = park[(d * 8 + (r >> 1)) * 64]; const float a = (r & 1) ? bf_hi(pw) : bf_lo(pw); const float v = a - lam * o[d][r]; o[d][r] = v; s += v * v; }
;         ss[r] = s; }
; #pragma unroll
;     for (int r = 0; r < 16; ++r) {
;         ss[r] = sum32(ss[r]);
;         ss[r] = omli / sqrtf(ss[r] * (1.0f / 128.0f) + EPS); }
	v_and_b32_e32 v42, 0xffff0000, v90
	v_fma_f32 v50, -v197, v50, v42
	v_and_b32_e32 v42, 0xffff0000, v92
	v_fma_f32 v48, -v197, v48, v42
	v_lshlrev_b32_e32 v42, 16, v43
	v_fma_f32 v26, -v197, v77, v24
	v_and_b32_e32 v24, 0xffff0000, v47
	v_fma_f32 v53, -v197, v53, v44
	v_lshlrev_b32_e32 v44, 16, v62
	v_fma_f32 v47, -v197, v56, v42
	v_lshlrev_b32_e32 v42, 16, v63
	v_fma_f32 v51, -v197, v51, v44
	v_lshlrev_b32_e32 v44, 16, v90
	v_fma_f32 v45, -v197, v41, v42
	v_lshlrev_b32_e32 v41, 16, v91
	v_fma_f32 v54, -v197, v54, v44
	v_lshlrev_b32_e32 v44, 16, v92
	v_fma_f32 v46, -v197, v40, v41
	v_lshlrev_b32_e32 v40, 16, v93
	v_fma_f32 v55, -v197, v55, v44
	v_fma_f32 v44, -v197, v7, v40
	v_and_b32_e32 v7, 0xffff0000, v43
	v_fma_f32 v43, -v197, v5, v7
	v_and_b32_e32 v5, 0xffff0000, v63
	v_fma_f32 v41, -v197, v3, v5
	v_and_b32_e32 v3, 0xffff0000, v91
	v_fma_f32 v42, -v197, v1, v3
	v_and_b32_e32 v1, 0xffff0000, v93
	v_fma_f32 v40, -v197, v0, v1
	ds_read2st64_b32 v[0:1], v216 offset0:6 offset1:7
	v_mul_f32_e32 v83, v19, v19
	v_fmac_f32_e32 v83, v21, v21
	v_fmac_f32_e32 v83, v22, v22
	v_fmac_f32_e32 v83, v23, v23
	s_waitcnt lgkmcnt(0)
	v_lshlrev_b32_e32 v3, 16, v0
	v_fma_f32 v56, -v197, v2, v3
	ds_read2st64_b32 v[2:3], v216 offset0:14 offset1:15
	v_and_b32_e32 v0, 0xffff0000, v0
	v_fma_f32 v67, -v197, v67, v0
	v_mul_f32_e32 v82, v17, v17
	v_fmac_f32_e32 v82, v20, v20
	s_waitcnt lgkmcnt(0)
	v_lshlrev_b32_e32 v5, 16, v2
	v_fma_f32 v57, -v197, v4, v5
	ds_read2st64_b32 v[4:5], v216 offset0:22 offset1:23
	v_and_b32_e32 v0, 0xffff0000, v2
	v_fma_f32 v61, -v197, v61, v0
	v_fmac_f32_e32 v82, v18, v18
	v_fmac_f32_e32 v82, v16, v16
	s_waitcnt lgkmcnt(0)
	v_lshlrev_b32_e32 v7, 16, v4
	v_fma_f32 v58, -v197, v6, v7
	ds_read2st64_b32 v[6:7], v216 offset0:30 offset1:31
	v_and_b32_e32 v0, 0xffff0000, v4
	v_fma_f32 v63, -v197, v65, v0
	v_mul_f32_e32 v81, v13, v13
	v_fmac_f32_e32 v81, v15, v15
	s_waitcnt lgkmcnt(0)
	v_and_b32_e32 v0, 0xffff0000, v6
	v_lshlrev_b32_e32 v62, 16, v6
	v_fma_f32 v65, -v197, v60, v0
	v_lshlrev_b32_e32 v0, 16, v1
	v_fma_f32 v66, -v197, v59, v62
	v_fma_f32 v62, -v197, v85, v0
	v_lshlrev_b32_e32 v0, 16, v3
	v_fma_f32 v59, -v197, v71, v0
	v_lshlrev_b32_e32 v0, 16, v5
	v_fma_f32 v60, -v197, v84, v0
	v_lshlrev_b32_e32 v0, 16, v7
	v_fma_f32 v6, -v197, v69, v0
	v_and_b32_e32 v0, 0xffff0000, v1
	v_fma_f32 v4, -v197, v89, v0
	v_and_b32_e32 v0, 0xffff0000, v3
	v_fma_f32 v1, -v197, v88, v0
	v_and_b32_e32 v0, 0xffff0000, v5
	v_fma_f32 v2, -v197, v87, v0
	v_and_b32_e32 v0, 0xffff0000, v7
	s_waitcnt lgkmcnt(0)
	s_nop 1
	v_add_f32_dpp v3, v83, v83 quad_perm:[1,0,3,2] row_mask:0xf bank_mask:0xf
	v_fmac_f32_e32 v81, v14, v14
	v_fmac_f32_e32 v81, v12, v12
	v_mul_f32_e32 v73, v9, v9
	v_fmac_f32_e32 v73, v11, v11
	s_waitcnt lgkmcnt(0)
	s_nop 1
	v_add_f32_dpp v3, v3, v3 quad_perm:[2,3,0,1] row_mask:0xf bank_mask:0xf
	v_fmac_f32_e32 v73, v10, v10
	v_fma_f32 v8, -v197, v103, v8
	v_fmac_f32_e32 v73, v8, v8
	v_mul_f32_e32 v76, v35, v35
	s_waitcnt lgkmcnt(0)
	s_nop 1
	v_add_f32_dpp v3, v3, v3 row_half_mirror row_mask:0xf bank_mask:0xf
	v_fmac_f32_e32 v76, v37, v37
	v_fmac_f32_e32 v76, v38, v38
	v_fmac_f32_e32 v76, v39, v39
	v_mul_f32_e32 v79, v33, v33
	s_waitcnt lgkmcnt(0)
	s_nop 1
	v_add_f32_dpp v3, v3, v3 row_mirror row_mask:0xf bank_mask:0xf
	v_mov_b32_e32 v5, v3
	v_fmac_f32_e32 v79, v36, v36
	v_fmac_f32_e32 v79, v34, v34
	v_fmac_f32_e32 v79, v32, v32
	v_mul_f32_e32 v80, v29, v29
	s_waitcnt lgkmcnt(0)
	s_nop 1
	v_permlane16_swap_b32_e32 v5, v3
	v_add_f32_e32 v3, v3, v5
	v_fmamk_f32 v3, v3, 0x3c000000, v212
	v_cmp_gt_f32_e32 vcc, s2, v3
	v_mul_f32_e32 v5, 0x4f800000, v3
	v_fmac_f32_e32 v80, v31, v31
	v_cndmask_b32_e32 v3, v3, v5, vcc
	v_sqrt_f32_e32 v5, v3
	v_fmac_f32_e32 v80, v30, v30
	v_fmac_f32_e32 v80, v28, v28
	v_mul_f32_e32 v78, v25, v25
	v_add_u32_e32 v7, -1, v5
	v_fma_f32 v83, -v7, v5, v3
	v_cmp_ge_f32_e64 s[0:1], 0, v83
	v_add_u32_e32 v83, 1, v5
	v_fmac_f32_e32 v78, v27, v27
	v_cndmask_b32_e64 v7, v5, v7, s[0:1]
	v_fma_f32 v5, -v83, v5, v3
	v_cmp_lt_f32_e64 s[0:1], 0, v5
	v_fmac_f32_e32 v78, v26, v26
	v_fma_f32 v24, -v197, v75, v24
	v_cndmask_b32_e64 v5, v7, v83, s[0:1]
	v_mul_f32_e32 v7, 0x37800000, v5
	v_cndmask_b32_e32 v5, v5, v7, vcc
	v_cmp_class_f32_e32 vcc, v3, v248
	v_fmac_f32_e32 v78, v24, v24
	v_mul_f32_e32 v77, v51, v51
	v_cndmask_b32_e32 v3, v5, v3, vcc
	v_div_scale_f32 v5, s[0:1], v3, v3, v206
	v_rcp_f32_e32 v7, v5
	v_fmac_f32_e32 v77, v53, v53
	v_fmac_f32_e32 v77, v54, v54
	v_fmac_f32_e32 v77, v55, v55
	v_fma_f32 v83, -v5, v7, 1.0
	v_fmac_f32_e32 v7, v83, v7
	v_div_scale_f32 v83, vcc, v206, v3, v206
	v_mul_f32_e32 v84, v83, v7
	v_fma_f32 v85, -v5, v84, v83
	v_fmac_f32_e32 v84, v85, v7
	v_fma_f32 v5, -v5, v84, v83
	v_div_fmas_f32 v5, v5, v7, v84
	v_div_fixup_f32 v3, v5, v3, v206
	v_mul_f32_e32 v75, v49, v49
	v_fmac_f32_e32 v75, v52, v52
	v_fmac_f32_e32 v75, v50, v50
	v_fmac_f32_e32 v75, v48, v48
	s_waitcnt lgkmcnt(0)
	s_nop 1
	v_add_f32_dpp v5, v82, v82 quad_perm:[1,0,3,2] row_mask:0xf bank_mask:0xf
	v_mul_f32_e32 v72, v45, v45
	v_fmac_f32_e32 v72, v47, v47
	v_fmac_f32_e32 v72, v46, v46
	v_fmac_f32_e32 v72, v44, v44
	s_waitcnt lgkmcnt(0)
	s_nop 1
	v_add_f32_dpp v5, v5, v5 quad_perm:[2,3,0,1] row_mask:0xf bank_mask:0xf
	v_mul_f32_e32 v68, v41, v41
	v_fmac_f32_e32 v68, v43, v43
	v_fmac_f32_e32 v68, v42, v42
	v_fmac_f32_e32 v68, v40, v40
	s_waitcnt lgkmcnt(0)
	s_nop 1
	v_add_f32_dpp v5, v5, v5 row_half_mirror row_mask:0xf bank_mask:0xf
	v_mul_f32_e32 v70, v57, v57
	v_fmac_f32_e32 v70, v56, v56
	v_fmac_f32_e32 v70, v58, v58
	v_fmac_f32_e32 v70, v66, v66
	s_waitcnt lgkmcnt(0)
; __device__ __forceinline__ float sum32(float v) { v += swz_xor<1>(v); v += swz_xor<2>(v); v += swz_xor<4>(v); v += swz_xor<8>(v); v += swz_xor<16>(v); return v; }
; __device__ __forceinline__ void diff_unit(int b, int h, int qb, const bf16_t* Q, const bf16_t* K, const bf16_t* V, bf16_t* YA, float lam, float omli, const float* subln, char* lds, const int wave_) {
;     ...
;     for (int r = 0; r < 16; ++r) {
;         ss[r] = sum32(ss[r]);
;         ss[r] = omli / sqrtf(ss[r] * (1.0f / 128.0f) + EPS); }
	s_nop 1
	v_add_f32_dpp v5, v5, v5 row_mirror row_mask:0xf bank_mask:0xf
	v_mov_b32_e32 v7, v5
	v_mul_f32_e32 v74, v61, v61
	v_fmac_f32_e32 v74, v67, v67
	v_fmac_f32_e32 v74, v63, v63
	v_fmac_f32_e32 v74, v65, v65
	s_waitcnt lgkmcnt(0)
	s_nop 1
	v_permlane16_swap_b32_e32 v7, v5
	v_add_f32_e32 v5, v5, v7
	v_fmamk_f32 v5, v5, 0x3c000000, v212
	v_cmp_gt_f32_e32 vcc, s2, v5
	v_mul_f32_e32 v7, 0x4f800000, v5
	v_mul_f32_e32 v71, v59, v59
	v_cndmask_b32_e32 v5, v5, v7, vcc
	v_sqrt_f32_e32 v7, v5
	v_fmac_f32_e32 v71, v62, v62
	v_fmac_f32_e32 v71, v60, v60
	v_fmac_f32_e32 v71, v6, v6
	v_add_u32_e32 v82, -1, v7
	v_fma_f32 v83, -v82, v7, v5
	v_cmp_ge_f32_e64 s[0:1], 0, v83
	v_add_u32_e32 v83, 1, v7
	v_mul_f32_e32 v69, v1, v1
	v_cndmask_b32_e64 v82, v7, v82, s[0:1]
	v_fma_f32 v7, -v83, v7, v5
	v_cmp_lt_f32_e64 s[0:1], 0, v7
	v_fmac_f32_e32 v69, v4, v4
	v_fmac_f32_e32 v69, v2, v2
	v_cndmask_b32_e64 v7, v82, v83, s[0:1]
	v_mul_f32_e32 v82, 0x37800000, v7
	v_cndmask_b32_e32 v7, v7, v82, vcc
	v_cmp_class_f32_e32 vcc, v5, v248
	v_fma_f32 v0, -v197, v86, v0
	v_fmac_f32_e32 v69, v0, v0
	v_cndmask_b32_e32 v5, v7, v5, vcc
	v_div_scale_f32 v7, s[0:1], v5, v5, v206
	v_rcp_f32_e32 v82, v7
	v_mul_f32_e32 v21, v21, v3
	v_mul_f32_e32 v19, v19, v3
	v_fma_f32 v83, -v7, v82, 1.0
	v_fmac_f32_e32 v82, v83, v82
	v_div_scale_f32 v83, vcc, v206, v5, v206
	v_mul_f32_e32 v84, v83, v82
	v_fma_f32 v85, -v7, v84, v83
	v_fmac_f32_e32 v84, v85, v82
	v_fma_f32 v7, -v7, v84, v83
	v_div_fmas_f32 v7, v7, v82, v84
	v_div_fixup_f32 v5, v7, v5, v206
	s_waitcnt lgkmcnt(0)
	s_nop 1
	v_add_f32_dpp v7, v81, v81 quad_perm:[1,0,3,2] row_mask:0xf bank_mask:0xf
	s_waitcnt lgkmcnt(0)
	s_nop 1
	v_add_f32_dpp v7, v7, v7 quad_perm:[2,3,0,1] row_mask:0xf bank_mask:0xf
	s_waitcnt lgkmcnt(0)
	s_nop 1
	v_add_f32_dpp v7, v7, v7 row_half_mirror row_mask:0xf bank_mask:0xf
	s_waitcnt lgkmcnt(0)
	s_nop 1
	v_add_f32_dpp v7, v7, v7 row_mirror row_mask:0xf bank_mask:0xf
	v_mov_b32_e32 v81, v7
	s_waitcnt lgkmcnt(0)
	s_nop 1
	v_permlane16_swap_b32_e32 v81, v7
	v_add_f32_e32 v7, v7, v81
	v_fmamk_f32 v7, v7, 0x3c000000, v212
	v_cmp_gt_f32_e32 vcc, s2, v7
	v_mul_f32_e32 v81, 0x4f800000, v7
	s_nop 0
	v_cndmask_b32_e32 v7, v7, v81, vcc
	v_sqrt_f32_e32 v81, v7
	s_nop 0
	v_add_u32_e32 v82, -1, v81
	v_fma_f32 v83, -v82, v81, v7
	v_cmp_ge_f32_e64 s[0:1], 0, v83
	v_add_u32_e32 v83, 1, v81
	s_nop 0
	v_cndmask_b32_e64 v82, v81, v82, s[0:1]
	v_fma_f32 v81, -v83, v81, v7
	v_cmp_lt_f32_e64 s[0:1], 0, v81
	s_nop 1
	v_cndmask_b32_e64 v81, v82, v83, s[0:1]
	v_mul_f32_e32 v82, 0x37800000, v81
	v_cndmask_b32_e32 v81, v81, v82, vcc
	v_cmp_class_f32_e32 vcc, v7, v248
	s_nop 1
	v_cndmask_b32_e32 v7, v81, v7, vcc
	v_div_scale_f32 v81, s[0:1], v7, v7, v206
	v_rcp_f32_e32 v82, v81
	s_nop 0
	v_fma_f32 v83, -v81, v82, 1.0
	v_fmac_f32_e32 v82, v83, v82
	v_div_scale_f32 v83, vcc, v206, v7, v206
	v_mul_f32_e32 v84, v83, v82
	v_fma_f32 v85, -v81, v84, v83
	v_fmac_f32_e32 v84, v85, v82
	v_fma_f32 v81, -v81, v84, v83
	v_div_fmas_f32 v81, v81, v82, v84
	v_div_fixup_f32 v7, v81, v7, v206
	s_waitcnt lgkmcnt(0)
	s_nop 1
	v_add_f32_dpp v73, v73, v73 quad_perm:[1,0,3,2] row_mask:0xf bank_mask:0xf
	s_waitcnt lgkmcnt(0)
	s_nop 1
	v_add_f32_dpp v73, v73, v73 quad_perm:[2,3,0,1] row_mask:0xf bank_mask:0xf
	s_waitcnt lgkmcnt(0)
	s_nop 1
	v_add_f32_dpp v73, v73, v73 row_half_mirror row_mask:0xf bank_mask:0xf
	s_waitcnt lgkmcnt(0)
	s_nop 1
	v_add_f32_dpp v73, v73, v73 row_mirror row_mask:0xf bank_mask:0xf
	v_mov_b32_e32 v81, v73
	s_waitcnt lgkmcnt(0)
	s_nop 1
	v_permlane16_swap_b32_e32 v81, v73
	v_add_f32_e32 v73, v73, v81
	v_fmamk_f32 v73, v73, 0x3c000000, v212
	v_cmp_gt_f32_e32 vcc, s2, v73
	v_mul_f32_e32 v81, 0x4f800000, v73
	s_nop 0
	v_cndmask_b32_e32 v73, v73, v81, vcc
	v_sqrt_f32_e32 v81, v73
	s_nop 0
	v_add_u32_e32 v82, -1, v81
	v_fma_f32 v83, -v82, v81, v73
	v_cmp_ge_f32_e64 s[0:1], 0, v83
	v_add_u32_e32 v83, 1, v81
	s_nop 0
	v_cndmask_b32_e64 v82, v81, v82, s[0:1]
	v_fma_f32 v81, -v83, v81, v73
	v_cmp_lt_f32_e64 s[0:1], 0, v81
	s_nop 1
	v_cndmask_b32_e64 v81, v82, v83, s[0:1]
	v_mul_f32_e32 v82, 0x37800000, v81
	v_cndmask_b32_e32 v81, v81, v82, vcc
	v_cmp_class_f32_e32 vcc, v73, v248
	s_nop 1
	v_cndmask_b32_e32 v73, v81, v73, vcc
	v_div_scale_f32 v81, s[0:1], v73, v73, v206
	v_rcp_f32_e32 v82, v81
	s_nop 0
	v_fma_f32 v83, -v81, v82, 1.0
	v_fmac_f32_e32 v82, v83, v82
	v_div_scale_f32 v83, vcc, v206, v73, v206
	v_mul_f32_e32 v84, v83, v82
	v_fma_f32 v85, -v81, v84, v83
	v_fmac_f32_e32 v84, v85, v82
	v_fma_f32 v81, -v81, v84, v83
	v_div_fmas_f32 v81, v81, v82, v84
	v_div_fixup_f32 v73, v81, v73, v206
	s_waitcnt lgkmcnt(0)
	s_nop 1
	v_add_f32_dpp v76, v76, v76 quad_perm:[1,0,3,2] row_mask:0xf bank_mask:0xf
	s_waitcnt lgkmcnt(0)
	s_nop 1
	v_add_f32_dpp v76, v76, v76 quad_perm:[2,3,0,1] row_mask:0xf bank_mask:0xf
	s_waitcnt lgkmcnt(0)
	s_nop 1
	v_add_f32_dpp v76, v76, v76 row_half_mirror row_mask:0xf bank_mask:0xf
	s_waitcnt lgkmcnt(0)
	s_nop 1
	v_add_f32_dpp v76, v76, v76 row_mirror row_mask:0xf bank_mask:0xf
	v_mov_b32_e32 v81, v76
	s_waitcnt lgkmcnt(0)
	s_nop 1
	v_permlane16_swap_b32_e32 v81, v76
	v_add_f32_e32 v76, v76, v81
	v_fmamk_f32 v76, v76, 0x3c000000, v212
	v_cmp_gt_f32_e32 vcc, s2, v76
	v_mul_f32_e32 v81, 0x4f800000, v76
	s_nop 0
	v_cndmask_b32_e32 v76, v76, v81, vcc
	v_sqrt_f32_e32 v81, v76
	s_nop 0
	v_add_u32_e32 v82, -1, v81
	v_fma_f32 v83, -v82, v81, v76
	v_cmp_ge_f32_e64 s[0:1], 0, v83
	v_add_u32_e32 v83, 1, v81
	s_nop 0
	v_cndmask_b32_e64 v82, v81, v82, s[0:1]
	v_fma_f32 v81, -v83, v81, v76
	v_cmp_lt_f32_e64 s[0:1], 0, v81
	s_nop 1
	v_cndmask_b32_e64 v81, v82, v83, s[0:1]
	v_mul_f32_e32 v82, 0x37800000, v81
	v_cndmask_b32_e32 v81, v81, v82, vcc
	v_cmp_class_f32_e32 vcc, v76, v248
	s_nop 1
	v_cndmask_b32_e32 v76, v81, v76, vcc
	v_div_scale_f32 v81, s[0:1], v76, v76, v206
	v_rcp_f32_e32 v82, v81
	s_nop 0
	v_fma_f32 v83, -v81, v82, 1.0
	v_fmac_f32_e32 v82, v83, v82
	v_div_scale_f32 v83, vcc, v206, v76, v206
	v_mul_f32_e32 v84, v83, v82
	v_fma_f32 v85, -v81, v84, v83
	v_fmac_f32_e32 v84, v85, v82
	v_fma_f32 v81, -v81, v84, v83
	v_div_fmas_f32 v81, v81, v82, v84
	v_div_fixup_f32 v76, v81, v76, v206
	s_waitcnt lgkmcnt(0)
; __device__ __forceinline__ float sum32(float v) { v += swz_xor<1>(v); v += swz_xor<2>(v); v += swz_xor<4>(v); v += swz_xor<8>(v); v += swz_xor<16>(v); return v; }
; __device__ __forceinline__ void diff_unit(int b, int h, int qb, const bf16_t* Q, const bf16_t* K, const bf16_t* V, bf16_t* YA, float lam, float omli, const float* subln, char* lds, const int wave_) {
;     ...
;     for (int r = 0; r < 16; ++r) {
;         ss[r] = sum32(ss[r]);
;         ss[r] = omli / sqrtf(ss[r] * (1.0f / 128.0f) + EPS); }
	s_nop 1
	v_add_f32_dpp v79, v79, v79 quad_perm:[1,0,3,2] row_mask:0xf bank_mask:0xf
	s_waitcnt lgkmcnt(0)
	s_nop 1
	v_add_f32_dpp v79, v79, v79 quad_perm:[2,3,0,1] row_mask:0xf bank_mask:0xf
	s_waitcnt lgkmcnt(0)
	s_nop 1
	v_add_f32_dpp v79, v79, v79 row_half_mirror row_mask:0xf bank_mask:0xf
	s_waitcnt lgkmcnt(0)
	s_nop 1
	v_add_f32_dpp v79, v79, v79 row_mirror row_mask:0xf bank_mask:0xf
	v_mov_b32_e32 v81, v79
	s_waitcnt lgkmcnt(0)
	s_nop 1
	v_permlane16_swap_b32_e32 v81, v79
	v_add_f32_e32 v79, v79, v81
	v_fmamk_f32 v79, v79, 0x3c000000, v212
	v_cmp_gt_f32_e32 vcc, s2, v79
	v_mul_f32_e32 v81, 0x4f800000, v79
	s_nop 0
	v_cndmask_b32_e32 v79, v79, v81, vcc
	v_sqrt_f32_e32 v81, v79
	s_nop 0
	v_add_u32_e32 v82, -1, v81
	v_fma_f32 v83, -v82, v81, v79
	v_cmp_ge_f32_e64 s[0:1], 0, v83
	v_add_u32_e32 v83, 1, v81
	s_nop 0
	v_cndmask_b32_e64 v82, v81, v82, s[0:1]
	v_fma_f32 v81, -v83, v81, v79
	v_cmp_lt_f32_e64 s[0:1], 0, v81
	s_nop 1
	v_cndmask_b32_e64 v81, v82, v83, s[0:1]
	v_mul_f32_e32 v82, 0x37800000, v81
	v_cndmask_b32_e32 v81, v81, v82, vcc
	v_cmp_class_f32_e32 vcc, v79, v248
	s_nop 1
	v_cndmask_b32_e32 v79, v81, v79, vcc
	v_div_scale_f32 v81, s[0:1], v79, v79, v206
	v_rcp_f32_e32 v82, v81
	s_nop 0
	v_fma_f32 v83, -v81, v82, 1.0
	v_fmac_f32_e32 v82, v83, v82
	v_div_scale_f32 v83, vcc, v206, v79, v206
	v_mul_f32_e32 v84, v83, v82
	v_fma_f32 v85, -v81, v84, v83
	v_fmac_f32_e32 v84, v85, v82
	v_fma_f32 v81, -v81, v84, v83
	v_div_fmas_f32 v81, v81, v82, v84
	v_div_fixup_f32 v79, v81, v79, v206
	s_waitcnt lgkmcnt(0)
	s_nop 1
	v_add_f32_dpp v80, v80, v80 quad_perm:[1,0,3,2] row_mask:0xf bank_mask:0xf
	s_waitcnt lgkmcnt(0)
	s_nop 1
	v_add_f32_dpp v80, v80, v80 quad_perm:[2,3,0,1] row_mask:0xf bank_mask:0xf
	s_waitcnt lgkmcnt(0)
	s_nop 1
	v_add_f32_dpp v80, v80, v80 row_half_mirror row_mask:0xf bank_mask:0xf
	s_waitcnt lgkmcnt(0)
	s_nop 1
	v_add_f32_dpp v80, v80, v80 row_mirror row_mask:0xf bank_mask:0xf
	v_mov_b32_e32 v81, v80
	s_waitcnt lgkmcnt(0)
	s_nop 1
	v_permlane16_swap_b32_e32 v81, v80
	v_add_f32_e32 v80, v80, v81
	v_fmamk_f32 v80, v80, 0x3c000000, v212
	v_cmp_gt_f32_e32 vcc, s2, v80
	v_mul_f32_e32 v81, 0x4f800000, v80
	s_nop 0
	v_cndmask_b32_e32 v80, v80, v81, vcc
	v_sqrt_f32_e32 v81, v80
	s_nop 0
	v_add_u32_e32 v82, -1, v81
	v_fma_f32 v83, -v82, v81, v80
	v_cmp_ge_f32_e64 s[0:1], 0, v83
	v_add_u32_e32 v83, 1, v81
	s_nop 0
	v_cndmask_b32_e64 v82, v81, v82, s[0:1]
	v_fma_f32 v81, -v83, v81, v80
	v_cmp_lt_f32_e64 s[0:1], 0, v81
	s_nop 1
	v_cndmask_b32_e64 v81, v82, v83, s[0:1]
	v_mul_f32_e32 v82, 0x37800000, v81
	v_cndmask_b32_e32 v81, v81, v82, vcc
	v_cmp_class_f32_e32 vcc, v80, v248
	s_nop 1
	v_cndmask_b32_e32 v80, v81, v80, vcc
	v_div_scale_f32 v81, s[0:1], v80, v80, v206
	v_rcp_f32_e32 v82, v81
	s_nop 0
	v_fma_f32 v83, -v81, v82, 1.0
	v_fmac_f32_e32 v82, v83, v82
	v_div_scale_f32 v83, vcc, v206, v80, v206
	v_mul_f32_e32 v84, v83, v82
	v_fma_f32 v85, -v81, v84, v83
	v_fmac_f32_e32 v84, v85, v82
	v_fma_f32 v81, -v81, v84, v83
	v_div_fmas_f32 v81, v81, v82, v84
	v_div_fixup_f32 v80, v81, v80, v206
	s_waitcnt lgkmcnt(0)
	s_nop 1
	v_add_f32_dpp v78, v78, v78 quad_perm:[1,0,3,2] row_mask:0xf bank_mask:0xf
	s_waitcnt lgkmcnt(0)
	s_nop 1
	v_add_f32_dpp v78, v78, v78 quad_perm:[2,3,0,1] row_mask:0xf bank_mask:0xf
	s_waitcnt lgkmcnt(0)
	s_nop 1
	v_add_f32_dpp v78, v78, v78 row_half_mirror row_mask:0xf bank_mask:0xf
	s_waitcnt lgkmcnt(0)
	s_nop 1
	v_add_f32_dpp v78, v78, v78 row_mirror row_mask:0xf bank_mask:0xf
	v_mov_b32_e32 v81, v78
	s_waitcnt lgkmcnt(0)
	s_nop 1
	v_permlane16_swap_b32_e32 v81, v78
	v_add_f32_e32 v78, v78, v81
	v_fmamk_f32 v78, v78, 0x3c000000, v212
	v_cmp_gt_f32_e32 vcc, s2, v78
	v_mul_f32_e32 v81, 0x4f800000, v78
	s_nop 0
	v_cndmask_b32_e32 v78, v78, v81, vcc
	v_sqrt_f32_e32 v81, v78
	s_nop 0
	v_add_u32_e32 v82, -1, v81
	v_fma_f32 v83, -v82, v81, v78
	v_cmp_ge_f32_e64 s[0:1], 0, v83
	v_add_u32_e32 v83, 1, v81
	s_nop 0
	v_cndmask_b32_e64 v82, v81, v82, s[0:1]
	v_fma_f32 v81, -v83, v81, v78
	v_cmp_lt_f32_e64 s[0:1], 0, v81
	s_nop 1
	v_cndmask_b32_e64 v81, v82, v83, s[0:1]
	v_mul_f32_e32 v82, 0x37800000, v81
	v_cndmask_b32_e32 v81, v81, v82, vcc
	v_cmp_class_f32_e32 vcc, v78, v248
	s_nop 1
	v_cndmask_b32_e32 v78, v81, v78, vcc
	v_div_scale_f32 v81, s[0:1], v78, v78, v206
	v_rcp_f32_e32 v82, v81
	s_nop 0
	v_fma_f32 v83, -v81, v82, 1.0
	v_fmac_f32_e32 v82, v83, v82
	v_div_scale_f32 v83, vcc, v206, v78, v206
	v_mul_f32_e32 v84, v83, v82
	v_fma_f32 v85, -v81, v84, v83
	v_fmac_f32_e32 v84, v85, v82
	v_fma_f32 v81, -v81, v84, v83
	v_div_fmas_f32 v81, v81, v82, v84
	v_div_fixup_f32 v78, v81, v78, v206
	s_waitcnt lgkmcnt(0)
	s_nop 1
	v_add_f32_dpp v77, v77, v77 quad_perm:[1,0,3,2] row_mask:0xf bank_mask:0xf
	s_waitcnt lgkmcnt(0)
	s_nop 1
	v_add_f32_dpp v77, v77, v77 quad_perm:[2,3,0,1] row_mask:0xf bank_mask:0xf
	s_waitcnt lgkmcnt(0)
	s_nop 1
	v_add_f32_dpp v77, v77, v77 row_half_mirror row_mask:0xf bank_mask:0xf
	s_waitcnt lgkmcnt(0)
	s_nop 1
	v_add_f32_dpp v77, v77, v77 row_mirror row_mask:0xf bank_mask:0xf
	v_mov_b32_e32 v81, v77
	s_waitcnt lgkmcnt(0)
	s_nop 1
	v_permlane16_swap_b32_e32 v81, v77
	v_add_f32_e32 v77, v77, v81
	v_fmamk_f32 v77, v77, 0x3c000000, v212
	v_cmp_gt_f32_e32 vcc, s2, v77
	v_mul_f32_e32 v81, 0x4f800000, v77
	s_nop 0
	v_cndmask_b32_e32 v77, v77, v81, vcc
	v_sqrt_f32_e32 v81, v77
	s_nop 0
	v_add_u32_e32 v82, -1, v81
	v_fma_f32 v83, -v82, v81, v77
	v_cmp_ge_f32_e64 s[0:1], 0, v83
	v_add_u32_e32 v83, 1, v81
	s_nop 0
	v_cndmask_b32_e64 v82, v81, v82, s[0:1]
	v_fma_f32 v81, -v83, v81, v77
	v_cmp_lt_f32_e64 s[0:1], 0, v81
	s_nop 1
	v_cndmask_b32_e64 v81, v82, v83, s[0:1]
	v_mul_f32_e32 v82, 0x37800000, v81
	v_cndmask_b32_e32 v81, v81, v82, vcc
	v_cmp_class_f32_e32 vcc, v77, v248
	s_nop 1
	v_cndmask_b32_e32 v77, v81, v77, vcc
	v_div_scale_f32 v81, s[0:1], v77, v77, v206
	v_rcp_f32_e32 v82, v81
	s_nop 0
	v_fma_f32 v83, -v81, v82, 1.0
	v_fmac_f32_e32 v82, v83, v82
	v_div_scale_f32 v83, vcc, v206, v77, v206
	v_mul_f32_e32 v84, v83, v82
	v_fma_f32 v85, -v81, v84, v83
	v_fmac_f32_e32 v84, v85, v82
	v_fma_f32 v81, -v81, v84, v83
	v_div_fmas_f32 v81, v81, v82, v84
	v_div_fixup_f32 v77, v81, v77, v206
	s_waitcnt lgkmcnt(0)
; __device__ __forceinline__ float sum32(float v) { v += swz_xor<1>(v); v += swz_xor<2>(v); v += swz_xor<4>(v); v += swz_xor<8>(v); v += swz_xor<16>(v); return v; }
; __device__ __forceinline__ void diff_unit(int b, int h, int qb, const bf16_t* Q, const bf16_t* K, const bf16_t* V, bf16_t* YA, float lam, float omli, const float* subln, char* lds, const int wave_) {
;     ...
;     for (int r = 0; r < 16; ++r) {
;         ss[r] = sum32(ss[r]);
;         ss[r] = omli / sqrtf(ss[r] * (1.0f / 128.0f) + EPS); }
	s_nop 1
	v_add_f32_dpp v75, v75, v75 quad_perm:[1,0,3,2] row_mask:0xf bank_mask:0xf
	s_waitcnt lgkmcnt(0)
	s_nop 1
	v_add_f32_dpp v75, v75, v75 quad_perm:[2,3,0,1] row_mask:0xf bank_mask:0xf
	s_waitcnt lgkmcnt(0)
	s_nop 1
	v_add_f32_dpp v75, v75, v75 row_half_mirror row_mask:0xf bank_mask:0xf
	s_waitcnt lgkmcnt(0)
	s_nop 1
	v_add_f32_dpp v75, v75, v75 row_mirror row_mask:0xf bank_mask:0xf
	v_mov_b32_e32 v81, v75
	s_waitcnt lgkmcnt(0)
	s_nop 1
	v_permlane16_swap_b32_e32 v81, v75
	v_add_f32_e32 v75, v75, v81
	v_fmamk_f32 v75, v75, 0x3c000000, v212
	v_cmp_gt_f32_e32 vcc, s2, v75
	v_mul_f32_e32 v81, 0x4f800000, v75
	s_nop 0
	v_cndmask_b32_e32 v75, v75, v81, vcc
	v_sqrt_f32_e32 v81, v75
	s_nop 0
	v_add_u32_e32 v82, -1, v81
	v_fma_f32 v83, -v82, v81, v75
	v_cmp_ge_f32_e64 s[0:1], 0, v83
	v_add_u32_e32 v83, 1, v81
	s_nop 0
	v_cndmask_b32_e64 v82, v81, v82, s[0:1]
	v_fma_f32 v81, -v83, v81, v75
	v_cmp_lt_f32_e64 s[0:1], 0, v81
	s_nop 1
	v_cndmask_b32_e64 v81, v82, v83, s[0:1]
	v_mul_f32_e32 v82, 0x37800000, v81
	v_cndmask_b32_e32 v81, v81, v82, vcc
	v_cmp_class_f32_e32 vcc, v75, v248
	s_nop 1
	v_cndmask_b32_e32 v75, v81, v75, vcc
	v_div_scale_f32 v81, s[0:1], v75, v75, v206
	v_rcp_f32_e32 v82, v81
	s_nop 0
	v_fma_f32 v83, -v81, v82, 1.0
	v_fmac_f32_e32 v82, v83, v82
	v_div_scale_f32 v83, vcc, v206, v75, v206
	v_mul_f32_e32 v84, v83, v82
	v_fma_f32 v85, -v81, v84, v83
	v_fmac_f32_e32 v84, v85, v82
	v_fma_f32 v81, -v81, v84, v83
	v_div_fmas_f32 v81, v81, v82, v84
	v_div_fixup_f32 v75, v81, v75, v206
	s_waitcnt lgkmcnt(0)
	s_nop 1
	v_add_f32_dpp v72, v72, v72 quad_perm:[1,0,3,2] row_mask:0xf bank_mask:0xf
	s_waitcnt lgkmcnt(0)
	s_nop 1
	v_add_f32_dpp v72, v72, v72 quad_perm:[2,3,0,1] row_mask:0xf bank_mask:0xf
	s_waitcnt lgkmcnt(0)
	s_nop 1
	v_add_f32_dpp v72, v72, v72 row_half_mirror row_mask:0xf bank_mask:0xf
	s_waitcnt lgkmcnt(0)
	s_nop 1
	v_add_f32_dpp v72, v72, v72 row_mirror row_mask:0xf bank_mask:0xf
	v_mov_b32_e32 v81, v72
	s_waitcnt lgkmcnt(0)
	s_nop 1
	v_permlane16_swap_b32_e32 v81, v72
	v_add_f32_e32 v72, v72, v81
	v_fmamk_f32 v72, v72, 0x3c000000, v212
	v_cmp_gt_f32_e32 vcc, s2, v72
	v_mul_f32_e32 v81, 0x4f800000, v72
	s_nop 0
	v_cndmask_b32_e32 v72, v72, v81, vcc
	v_sqrt_f32_e32 v81, v72
	s_nop 0
	v_add_u32_e32 v82, -1, v81
	v_fma_f32 v83, -v82, v81, v72
	v_cmp_ge_f32_e64 s[0:1], 0, v83
	v_add_u32_e32 v83, 1, v81
	s_nop 0
	v_cndmask_b32_e64 v82, v81, v82, s[0:1]
	v_fma_f32 v81, -v83, v81, v72
	v_cmp_lt_f32_e64 s[0:1], 0, v81
	s_nop 1
	v_cndmask_b32_e64 v81, v82, v83, s[0:1]
	v_mul_f32_e32 v82, 0x37800000, v81
	v_cndmask_b32_e32 v81, v81, v82, vcc
	v_cmp_class_f32_e32 vcc, v72, v248
	s_nop 1
	v_cndmask_b32_e32 v72, v81, v72, vcc
	v_div_scale_f32 v81, s[0:1], v72, v72, v206
	v_rcp_f32_e32 v82, v81
	s_nop 0
	v_fma_f32 v83, -v81, v82, 1.0
	v_fmac_f32_e32 v82, v83, v82
	v_div_scale_f32 v83, vcc, v206, v72, v206
	v_mul_f32_e32 v84, v83, v82
	v_fma_f32 v85, -v81, v84, v83
	v_fmac_f32_e32 v84, v85, v82
	v_fma_f32 v81, -v81, v84, v83
	v_div_fmas_f32 v81, v81, v82, v84
	v_div_fixup_f32 v72, v81, v72, v206
	s_waitcnt lgkmcnt(0)
	s_nop 1
	v_add_f32_dpp v68, v68, v68 quad_perm:[1,0,3,2] row_mask:0xf bank_mask:0xf
	s_waitcnt lgkmcnt(0)
	s_nop 1
	v_add_f32_dpp v68, v68, v68 quad_perm:[2,3,0,1] row_mask:0xf bank_mask:0xf
	s_waitcnt lgkmcnt(0)
	s_nop 1
	v_add_f32_dpp v68, v68, v68 row_half_mirror row_mask:0xf bank_mask:0xf
	s_waitcnt lgkmcnt(0)
	s_nop 1
	v_add_f32_dpp v68, v68, v68 row_mirror row_mask:0xf bank_mask:0xf
	v_mov_b32_e32 v81, v68
	s_waitcnt lgkmcnt(0)
	s_nop 1
	v_permlane16_swap_b32_e32 v81, v68
	v_add_f32_e32 v68, v68, v81
	v_fmamk_f32 v68, v68, 0x3c000000, v212
	v_cmp_gt_f32_e32 vcc, s2, v68
	v_mul_f32_e32 v81, 0x4f800000, v68
	s_nop 0
	v_cndmask_b32_e32 v68, v68, v81, vcc
	v_sqrt_f32_e32 v81, v68
	s_nop 0
	v_add_u32_e32 v82, -1, v81
	v_fma_f32 v83, -v82, v81, v68
	v_cmp_ge_f32_e64 s[0:1], 0, v83
	v_add_u32_e32 v83, 1, v81
	s_nop 0
	v_cndmask_b32_e64 v82, v81, v82, s[0:1]
	v_fma_f32 v81, -v83, v81, v68
	v_cmp_lt_f32_e64 s[0:1], 0, v81
	s_nop 1
	v_cndmask_b32_e64 v81, v82, v83, s[0:1]
	v_mul_f32_e32 v82, 0x37800000, v81
	v_cndmask_b32_e32 v81, v81, v82, vcc
	v_cmp_class_f32_e32 vcc, v68, v248
	s_nop 1
	v_cndmask_b32_e32 v68, v81, v68, vcc
	v_div_scale_f32 v81, s[0:1], v68, v68, v206
	v_rcp_f32_e32 v82, v81
	s_nop 0
	v_fma_f32 v83, -v81, v82, 1.0
	v_fmac_f32_e32 v82, v83, v82
	v_div_scale_f32 v83, vcc, v206, v68, v206
	v_mul_f32_e32 v84, v83, v82
	v_fma_f32 v85, -v81, v84, v83
	v_fmac_f32_e32 v84, v85, v82
	v_fma_f32 v81, -v81, v84, v83
	v_div_fmas_f32 v81, v81, v82, v84
	v_div_fixup_f32 v68, v81, v68, v206
	s_waitcnt lgkmcnt(0)
	s_nop 1
	v_add_f32_dpp v70, v70, v70 quad_perm:[1,0,3,2] row_mask:0xf bank_mask:0xf
	s_waitcnt lgkmcnt(0)
	s_nop 1
	v_add_f32_dpp v70, v70, v70 quad_perm:[2,3,0,1] row_mask:0xf bank_mask:0xf
	s_waitcnt lgkmcnt(0)
	s_nop 1
	v_add_f32_dpp v70, v70, v70 row_half_mirror row_mask:0xf bank_mask:0xf
	s_waitcnt lgkmcnt(0)
	s_nop 1
	v_add_f32_dpp v70, v70, v70 row_mirror row_mask:0xf bank_mask:0xf
	v_mov_b32_e32 v81, v70
	s_waitcnt lgkmcnt(0)
	s_nop 1
	v_permlane16_swap_b32_e32 v81, v70
	v_add_f32_e32 v70, v70, v81
	v_fmamk_f32 v70, v70, 0x3c000000, v212
	v_cmp_gt_f32_e32 vcc, s2, v70
	v_mul_f32_e32 v81, 0x4f800000, v70
	s_nop 0
	v_cndmask_b32_e32 v70, v70, v81, vcc
	v_sqrt_f32_e32 v81, v70
	s_nop 0
	v_add_u32_e32 v82, -1, v81
	v_fma_f32 v83, -v82, v81, v70
	v_cmp_ge_f32_e64 s[0:1], 0, v83
	v_add_u32_e32 v83, 1, v81
	s_nop 0
	v_cndmask_b32_e64 v82, v81, v82, s[0:1]
	v_fma_f32 v81, -v83, v81, v70
	v_cmp_lt_f32_e64 s[0:1], 0, v81
	s_nop 1
	v_cndmask_b32_e64 v81, v82, v83, s[0:1]
	v_mul_f32_e32 v82, 0x37800000, v81
	v_cndmask_b32_e32 v81, v81, v82, vcc
	v_cmp_class_f32_e32 vcc, v70, v248
	s_nop 1
	v_cndmask_b32_e32 v70, v81, v70, vcc
	v_div_scale_f32 v81, s[0:1], v70, v70, v206
	v_rcp_f32_e32 v82, v81
	s_nop 0
	v_fma_f32 v83, -v81, v82, 1.0
	v_fmac_f32_e32 v82, v83, v82
	v_div_scale_f32 v83, vcc, v206, v70, v206
	v_mul_f32_e32 v84, v83, v82
	v_fma_f32 v85, -v81, v84, v83
	v_fmac_f32_e32 v84, v85, v82
	v_fma_f32 v81, -v81, v84, v83
	v_div_fmas_f32 v81, v81, v82, v84
	v_div_fixup_f32 v70, v81, v70, v206
	s_waitcnt lgkmcnt(0)
; __device__ __forceinline__ unsigned cvt_pk_bf16(float lo, float hi) { unsigned r; asm volatile("v_cvt_pk_bf16_f32 %0, %1, %2" : "=v"(r) : "v"(lo), "v"(hi)); return r; }
; __device__ __forceinline__ float bf_lo(unsigned w) { return __uint_as_float(w << 16); }
; __device__ __forceinline__ float bf_hi(unsigned w) { return __uint_as_float(w & 0xffff0000u); }
; __device__ __forceinline__ float sum32(float v) { v += swz_xor<1>(v); v += swz_xor<2>(v); v += swz_xor<4>(v); v += swz_xor<8>(v); v += swz_xor<16>(v); return v; }
; __device__ __forceinline__ int crow(int r, int hi) { return (r & 3) + 8 * (r >> 2) + 4 * hi; }
; __device__ __forceinline__ void diff_unit(int b, int h, int qb, const bf16_t* Q, const bf16_t* K, const bf16_t* V, bf16_t* YA, float lam, float omli, const float* subln, char* lds, const int wave_) {
;     ...
;     for (int r = 0; r < 16; ++r) { float s = 0.f;
; #pragma unroll
;         for (int d = 0; d < 4; ++d) { const unsigned pw = park[(d * 8 + (r >> 1)) * 64]; const float a = (r & 1) ? bf_hi(pw) : bf_lo(pw); const float v = a - lam * o[d][r]; o[d][r] = v; s += v * v; }
;         ss[r] = s; }
; #pragma unroll
;     for (int r = 0; r < 16; ++r) {
;         ss[r] = sum32(ss[r]);
;         ss[r] = omli / sqrtf(ss[r] * (1.0f / 128.0f) + EPS); }
;     float gl[4];
; #pragma unroll
;     for (int d = 0; d < 4; ++d) gl[d] = subln[32 * d + r32];
;     asm volatile("s_waitcnt lgkmcnt(0)" ::: "memory");
;     bf16_t* stg = (bf16_t*)(lds + DA_LDS) + wid * 4096;
; #pragma unroll
;     for (int r = 0; r < 16; ++r) { const int orow = crow(r, hi);
; #pragma unroll
;         for (int d = 0; d < 4; ++d) stg[orow * 128 + 32 * d + r32] = (bf16_t)(cvt_pk_bf16(o[d][r] * ss[r] * gl[d], 0.f) & 0xffffu); }
	s_nop 1
	v_add_f32_dpp v74, v74, v74 quad_perm:[1,0,3,2] row_mask:0xf bank_mask:0xf
	s_waitcnt lgkmcnt(0)
	s_nop 1
	v_add_f32_dpp v74, v74, v74 quad_perm:[2,3,0,1] row_mask:0xf bank_mask:0xf
	s_waitcnt lgkmcnt(0)
	s_nop 1
	v_add_f32_dpp v74, v74, v74 row_half_mirror row_mask:0xf bank_mask:0xf
	s_waitcnt lgkmcnt(0)
	s_nop 1
	v_add_f32_dpp v74, v74, v74 row_mirror row_mask:0xf bank_mask:0xf
	v_mov_b32_e32 v81, v74
	s_waitcnt lgkmcnt(0)
	s_nop 1
	v_permlane16_swap_b32_e32 v81, v74
	v_add_f32_e32 v74, v74, v81
	v_fmamk_f32 v74, v74, 0x3c000000, v212
	v_cmp_gt_f32_e32 vcc, s2, v74
	v_mul_f32_e32 v81, 0x4f800000, v74
	s_nop 0
	v_cndmask_b32_e32 v74, v74, v81, vcc
	v_sqrt_f32_e32 v81, v74
	s_nop 0
	v_add_u32_e32 v82, -1, v81
	v_fma_f32 v83, -v82, v81, v74
	v_cmp_ge_f32_e64 s[0:1], 0, v83
	v_add_u32_e32 v83, 1, v81
	s_nop 0
	v_cndmask_b32_e64 v82, v81, v82, s[0:1]
	v_fma_f32 v81, -v83, v81, v74
	v_cmp_lt_f32_e64 s[0:1], 0, v81
	s_nop 1
	v_cndmask_b32_e64 v81, v82, v83, s[0:1]
	v_mul_f32_e32 v82, 0x37800000, v81
	v_cndmask_b32_e32 v81, v81, v82, vcc
	v_cmp_class_f32_e32 vcc, v74, v248
	s_nop 1
	v_cndmask_b32_e32 v74, v81, v74, vcc
	v_div_scale_f32 v81, s[0:1], v74, v74, v206
	v_rcp_f32_e32 v82, v81
	s_nop 0
	v_fma_f32 v83, -v81, v82, 1.0
	v_fmac_f32_e32 v82, v83, v82
	v_div_scale_f32 v83, vcc, v206, v74, v206
	v_mul_f32_e32 v84, v83, v82
	v_fma_f32 v85, -v81, v84, v83
	v_fmac_f32_e32 v84, v85, v82
	v_fma_f32 v81, -v81, v84, v83
	v_div_fmas_f32 v81, v81, v82, v84
	v_div_fixup_f32 v74, v81, v74, v206
	s_waitcnt lgkmcnt(0)
	s_nop 1
	v_add_f32_dpp v71, v71, v71 quad_perm:[1,0,3,2] row_mask:0xf bank_mask:0xf
	s_waitcnt lgkmcnt(0)
	s_nop 1
	v_add_f32_dpp v71, v71, v71 quad_perm:[2,3,0,1] row_mask:0xf bank_mask:0xf
	s_waitcnt lgkmcnt(0)
	s_nop 1
	v_add_f32_dpp v71, v71, v71 row_half_mirror row_mask:0xf bank_mask:0xf
	s_waitcnt lgkmcnt(0)
	s_nop 1
	v_add_f32_dpp v71, v71, v71 row_mirror row_mask:0xf bank_mask:0xf
	v_mov_b32_e32 v81, v71
	s_waitcnt lgkmcnt(0)
	s_nop 1
	v_permlane16_swap_b32_e32 v81, v71
	v_add_f32_e32 v71, v71, v81
	v_fmamk_f32 v71, v71, 0x3c000000, v212
	v_cmp_gt_f32_e32 vcc, s2, v71
	v_mul_f32_e32 v81, 0x4f800000, v71
	s_nop 0
	v_cndmask_b32_e32 v71, v71, v81, vcc
	v_sqrt_f32_e32 v81, v71
	s_nop 0
	v_add_u32_e32 v82, -1, v81
	v_fma_f32 v83, -v82, v81, v71
	v_cmp_ge_f32_e64 s[0:1], 0, v83
	v_add_u32_e32 v83, 1, v81
	s_nop 0
	v_cndmask_b32_e64 v82, v81, v82, s[0:1]
	v_fma_f32 v81, -v83, v81, v71
	v_cmp_lt_f32_e64 s[0:1], 0, v81
	s_nop 1
	v_cndmask_b32_e64 v81, v82, v83, s[0:1]
	v_mul_f32_e32 v82, 0x37800000, v81
	v_cndmask_b32_e32 v81, v81, v82, vcc
	v_cmp_class_f32_e32 vcc, v71, v248
	s_nop 1
	v_cndmask_b32_e32 v71, v81, v71, vcc
	v_div_scale_f32 v81, s[0:1], v71, v71, v206
	v_rcp_f32_e32 v82, v81
	s_nop 0
	v_fma_f32 v83, -v81, v82, 1.0
	v_fmac_f32_e32 v82, v83, v82
	v_div_scale_f32 v83, vcc, v206, v71, v206
	v_mul_f32_e32 v84, v83, v82
	v_fma_f32 v85, -v81, v84, v83
	v_fmac_f32_e32 v84, v85, v82
	v_fma_f32 v81, -v81, v84, v83
	v_div_fmas_f32 v81, v81, v82, v84
	v_div_fixup_f32 v71, v81, v71, v206
	s_waitcnt lgkmcnt(0)
	s_nop 1
	v_add_f32_dpp v69, v69, v69 quad_perm:[1,0,3,2] row_mask:0xf bank_mask:0xf
	s_waitcnt lgkmcnt(0)
	s_nop 1
	v_add_f32_dpp v69, v69, v69 quad_perm:[2,3,0,1] row_mask:0xf bank_mask:0xf
	s_waitcnt lgkmcnt(0)
	s_nop 1
	v_add_f32_dpp v69, v69, v69 row_half_mirror row_mask:0xf bank_mask:0xf
	s_waitcnt lgkmcnt(0)
	s_nop 1
	v_add_f32_dpp v69, v69, v69 row_mirror row_mask:0xf bank_mask:0xf
	v_mov_b32_e32 v81, v69
	s_waitcnt lgkmcnt(0)
	s_nop 1
	v_permlane16_swap_b32_e32 v81, v69
	v_add_f32_e32 v69, v69, v81
	v_fmamk_f32 v69, v69, 0x3c000000, v212
	v_cmp_gt_f32_e32 vcc, s2, v69
	v_mul_f32_e32 v81, 0x4f800000, v69
	s_nop 0
	v_cndmask_b32_e32 v69, v69, v81, vcc
	v_sqrt_f32_e32 v81, v69
	s_nop 0
	v_add_u32_e32 v82, -1, v81
	v_fma_f32 v83, -v82, v81, v69
	v_cmp_ge_f32_e64 s[0:1], 0, v83
	v_add_u32_e32 v83, 1, v81
	s_nop 0
	v_cndmask_b32_e64 v82, v81, v82, s[0:1]
	v_fma_f32 v81, -v83, v81, v69
	v_cmp_lt_f32_e64 s[0:1], 0, v81
	s_nop 1
	v_cndmask_b32_e64 v81, v82, v83, s[0:1]
	v_mul_f32_e32 v82, 0x37800000, v81
	v_cndmask_b32_e32 v81, v81, v82, vcc
	v_cmp_class_f32_e32 vcc, v69, v248
	s_nop 1
	v_cndmask_b32_e32 v69, v81, v69, vcc
	v_div_scale_f32 v81, s[0:1], v69, v69, v206
	v_rcp_f32_e32 v82, v81
	v_readlane_b32 s0, v253, 62
	v_readlane_b32 s1, v253, 63
	v_fma_f32 v83, -v81, v82, 1.0
	v_fmac_f32_e32 v82, v83, v82
	v_div_scale_f32 v83, vcc, v206, v69, v206
	v_mul_f32_e32 v84, v83, v82
	v_fma_f32 v85, -v81, v84, v83
	v_fmac_f32_e32 v84, v85, v82
	v_fma_f32 v81, -v81, v84, v83
	v_div_fmas_f32 v81, v81, v82, v84
	v_lshlrev_b32_e32 v83, 2, v64
	v_div_fixup_f32 v69, v81, v69, v206
	global_load_dword v81, v83, s[4:5]
	global_load_dword v82, v83, s[4:5] offset:128
	global_load_dword v84, v83, s[4:5] offset:256
	s_nop 0
	global_load_dword v83, v83, s[4:5] offset:384
	v_lshlrev_b32_e32 v85, 5, v207
	v_lshlrev_b32_e32 v64, 1, v64
	v_and_b32_e32 v85, 0x400, v85
	v_add3_u32 v64, v215, v64, v85
	s_waitcnt lgkmcnt(0)
	v_mul_f32_e32 v1, v1, v69
	v_mul_f32_e32 v0, v0, v69
	s_waitcnt vmcnt(3)
	v_mul_f32_e32 v21, v21, v81
	s_waitcnt vmcnt(2)
	v_mul_f32_e32 v19, v19, v82
	v_cvt_pk_bf16_f32 v21, v21, v161
	ds_write_b16 v64, v21
	v_cvt_pk_bf16_f32 v19, v19, v161
	ds_write_b16 v64, v19 offset:64
	v_mul_f32_e32 v19, v22, v3
	v_mul_f32_e32 v3, v23, v3
	s_waitcnt vmcnt(1)
	v_mul_f32_e32 v19, v19, v84
	s_waitcnt vmcnt(0)
; __device__ __forceinline__ unsigned cvt_pk_bf16(float lo, float hi) { unsigned r; asm volatile("v_cvt_pk_bf16_f32 %0, %1, %2" : "=v"(r) : "v"(lo), "v"(hi)); return r; }
; __device__ __forceinline__ int crow(int r, int hi) { return (r & 3) + 8 * (r >> 2) + 4 * hi; }
; __device__ __forceinline__ void diff_unit(int b, int h, int qb, const bf16_t* Q, const bf16_t* K, const bf16_t* V, bf16_t* YA, float lam, float omli, const float* subln, char* lds, const int wave_) {
;     ...
;     for (int r = 0; r < 16; ++r) { const int orow = crow(r, hi);
; #pragma unroll
;         for (int d = 0; d < 4; ++d) stg[orow * 128 + 32 * d + r32] = (bf16_t)(cvt_pk_bf16(o[d][r] * ss[r] * gl[d], 0.f) & 0xffffu); }
	v_mul_f32_e32 v3, v3, v83
	v_cvt_pk_bf16_f32 v19, v19, v161
	ds_write_b16 v64, v19 offset:128
	v_cvt_pk_bf16_f32 v3, v3, v161
	ds_write_b16 v64, v3 offset:192
	v_mul_f32_e32 v3, v20, v5
	v_mul_f32_e32 v3, v3, v81
	v_cvt_pk_bf16_f32 v3, v3, v161
	ds_write_b16 v64, v3 offset:256
	v_mul_f32_e32 v3, v17, v5
	v_mul_f32_e32 v3, v3, v82
	v_cvt_pk_bf16_f32 v3, v3, v161
	ds_write_b16 v64, v3 offset:320
	v_mul_f32_e32 v3, v18, v5
	v_mul_f32_e32 v3, v3, v84
	v_cvt_pk_bf16_f32 v3, v3, v161
	ds_write_b16 v64, v3 offset:384
	v_mul_f32_e32 v3, v16, v5
	v_mul_f32_e32 v3, v3, v83
	v_cvt_pk_bf16_f32 v3, v3, v161
	ds_write_b16 v64, v3 offset:448
	v_mul_f32_e32 v3, v15, v7
	v_mul_f32_e32 v3, v3, v81
	v_cvt_pk_bf16_f32 v3, v3, v161
	ds_write_b16 v64, v3 offset:512
	v_mul_f32_e32 v3, v13, v7
	v_mul_f32_e32 v3, v3, v82
	v_cvt_pk_bf16_f32 v3, v3, v161
	ds_write_b16 v64, v3 offset:576
	v_mul_f32_e32 v3, v14, v7
	v_mul_f32_e32 v3, v3, v84
	v_cvt_pk_bf16_f32 v3, v3, v161
	ds_write_b16 v64, v3 offset:640
	v_mul_f32_e32 v3, v12, v7
	v_mul_f32_e32 v3, v3, v83
	v_cvt_pk_bf16_f32 v3, v3, v161
	ds_write_b16 v64, v3 offset:704
	v_mul_f32_e32 v3, v11, v73
	v_mul_f32_e32 v3, v3, v81
	v_cvt_pk_bf16_f32 v3, v3, v161
	ds_write_b16 v64, v3 offset:768
	v_mul_f32_e32 v3, v9, v73
	v_mul_f32_e32 v3, v3, v82
	v_cvt_pk_bf16_f32 v3, v3, v161
	ds_write_b16 v64, v3 offset:832
	v_mul_f32_e32 v3, v10, v73
	v_mul_f32_e32 v3, v3, v84
	v_cvt_pk_bf16_f32 v3, v3, v161
	ds_write_b16 v64, v3 offset:896
	v_mul_f32_e32 v3, v8, v73
	v_mul_f32_e32 v3, v3, v83
	v_cvt_pk_bf16_f32 v3, v3, v161
	ds_write_b16 v64, v3 offset:960
	v_mul_f32_e32 v3, v37, v76
	v_mul_f32_e32 v3, v3, v81
	v_cvt_pk_bf16_f32 v3, v3, v161
	ds_write_b16 v64, v3 offset:2048
	v_mul_f32_e32 v3, v35, v76
	v_mul_f32_e32 v3, v3, v82
	v_cvt_pk_bf16_f32 v3, v3, v161
	ds_write_b16 v64, v3 offset:2112
	v_mul_f32_e32 v3, v38, v76
	v_mul_f32_e32 v3, v3, v84
	v_cvt_pk_bf16_f32 v3, v3, v161
	ds_write_b16 v64, v3 offset:2176
	v_mul_f32_e32 v3, v39, v76
	v_mul_f32_e32 v3, v3, v83
	v_cvt_pk_bf16_f32 v3, v3, v161
	ds_write_b16 v64, v3 offset:2240
	v_mul_f32_e32 v3, v36, v79
	v_mul_f32_e32 v3, v3, v81
	v_cvt_pk_bf16_f32 v3, v3, v161
	ds_write_b16 v64, v3 offset:2304
	v_mul_f32_e32 v3, v33, v79
	v_mul_f32_e32 v3, v3, v82
	v_cvt_pk_bf16_f32 v3, v3, v161
	ds_write_b16 v64, v3 offset:2368
	v_mul_f32_e32 v3, v34, v79
	v_mul_f32_e32 v3, v3, v84
	v_cvt_pk_bf16_f32 v3, v3, v161
	ds_write_b16 v64, v3 offset:2432
	v_mul_f32_e32 v3, v32, v79
	v_mul_f32_e32 v3, v3, v83
	v_cvt_pk_bf16_f32 v3, v3, v161
	ds_write_b16 v64, v3 offset:2496
	v_mul_f32_e32 v3, v31, v80
	v_mul_f32_e32 v3, v3, v81
	v_cvt_pk_bf16_f32 v3, v3, v161
	ds_write_b16 v64, v3 offset:2560
	v_mul_f32_e32 v3, v29, v80
	v_mul_f32_e32 v3, v3, v82
	v_cvt_pk_bf16_f32 v3, v3, v161
	ds_write_b16 v64, v3 offset:2624
	v_mul_f32_e32 v3, v30, v80
	v_mul_f32_e32 v3, v3, v84
	v_cvt_pk_bf16_f32 v3, v3, v161
	ds_write_b16 v64, v3 offset:2688
	v_mul_f32_e32 v3, v28, v80
	v_mul_f32_e32 v3, v3, v83
	v_cvt_pk_bf16_f32 v3, v3, v161
	ds_write_b16 v64, v3 offset:2752
	v_mul_f32_e32 v3, v27, v78
	v_mul_f32_e32 v3, v3, v81
	v_cvt_pk_bf16_f32 v3, v3, v161
	ds_write_b16 v64, v3 offset:2816
	v_mul_f32_e32 v3, v25, v78
	v_mul_f32_e32 v3, v3, v82
	v_cvt_pk_bf16_f32 v3, v3, v161
	ds_write_b16 v64, v3 offset:2880
	v_mul_f32_e32 v3, v26, v78
	v_mul_f32_e32 v3, v3, v84
	v_cvt_pk_bf16_f32 v3, v3, v161
	ds_write_b16 v64, v3 offset:2944
	v_mul_f32_e32 v3, v24, v78
	v_mul_f32_e32 v3, v3, v83
	v_cvt_pk_bf16_f32 v3, v3, v161
	ds_write_b16 v64, v3 offset:3008
	v_mul_f32_e32 v3, v53, v77
	v_mul_f32_e32 v3, v3, v81
	v_cvt_pk_bf16_f32 v3, v3, v161
	ds_write_b16 v64, v3 offset:4096
	v_mul_f32_e32 v3, v51, v77
	v_mul_f32_e32 v3, v3, v82
	v_cvt_pk_bf16_f32 v3, v3, v161
	ds_write_b16 v64, v3 offset:4160
	v_mul_f32_e32 v3, v54, v77
	v_mul_f32_e32 v3, v3, v84
	v_cvt_pk_bf16_f32 v3, v3, v161
	ds_write_b16 v64, v3 offset:4224
	v_mul_f32_e32 v3, v55, v77
	v_mul_f32_e32 v3, v3, v83
	v_cvt_pk_bf16_f32 v3, v3, v161
	ds_write_b16 v64, v3 offset:4288
	v_mul_f32_e32 v3, v52, v75
	v_mul_f32_e32 v3, v3, v81
	v_cvt_pk_bf16_f32 v3, v3, v161
	ds_write_b16 v64, v3 offset:4352
	v_mul_f32_e32 v3, v49, v75
	v_mul_f32_e32 v3, v3, v82
	v_cvt_pk_bf16_f32 v3, v3, v161
	ds_write_b16 v64, v3 offset:4416
	v_mul_f32_e32 v3, v50, v75
	v_mul_f32_e32 v3, v3, v84
	v_cvt_pk_bf16_f32 v3, v3, v161
	ds_write_b16 v64, v3 offset:4480
	v_mul_f32_e32 v3, v48, v75
	v_mul_f32_e32 v3, v3, v83
	v_cvt_pk_bf16_f32 v3, v3, v161
	ds_write_b16 v64, v3 offset:4544
	v_mul_f32_e32 v3, v47, v72
	v_mul_f32_e32 v3, v3, v81
	v_cvt_pk_bf16_f32 v3, v3, v161
	ds_write_b16 v64, v3 offset:4608
	v_mul_f32_e32 v3, v45, v72
	v_mul_f32_e32 v3, v3, v82
	v_cvt_pk_bf16_f32 v3, v3, v161
	ds_write_b16 v64, v3 offset:4672
	v_mul_f32_e32 v3, v46, v72
	v_mul_f32_e32 v3, v3, v84
	v_cvt_pk_bf16_f32 v3, v3, v161
	ds_write_b16 v64, v3 offset:4736
	v_mul_f32_e32 v3, v44, v72
; __device__ __forceinline__ unsigned cvt_pk_bf16(float lo, float hi) { unsigned r; asm volatile("v_cvt_pk_bf16_f32 %0, %1, %2" : "=v"(r) : "v"(lo), "v"(hi)); return r; }
; __device__ __forceinline__ int crow(int r, int hi) { return (r & 3) + 8 * (r >> 2) + 4 * hi; }
; __device__ __forceinline__ void diff_unit(int b, int h, int qb, const bf16_t* Q, const bf16_t* K, const bf16_t* V, bf16_t* YA, float lam, float omli, const float* subln, char* lds, const int wave_) {
;     ...
;     for (int r = 0; r < 16; ++r) { const int orow = crow(r, hi);
; #pragma unroll
;         for (int d = 0; d < 4; ++d) stg[orow * 128 + 32 * d + r32] = (bf16_t)(cvt_pk_bf16(o[d][r] * ss[r] * gl[d], 0.f) & 0xffffu); }
;     asm volatile("s_waitcnt lgkmcnt(0)" ::: "memory");
;     bf16_t* Ow = YA + (rowbase + q0 + wid * 32) * DM + h * 128;
; #pragma unroll
;     for (int i = 0; i < 8; ++i) { const int row = i * 4 + (lane >> 4), ch = lane & 15; const u32x4 v = *(const u32x4*)(stg + row * 128 + ch * 8); *(u32x4*)(Ow + (size_t)row * DM + ch * 8) = v; }
;     asm volatile("s_waitcnt lgkmcnt(0)" ::: "memory");
	v_mul_f32_e32 v3, v3, v83
	v_cvt_pk_bf16_f32 v3, v3, v161
	ds_write_b16 v64, v3 offset:4800
	v_mul_f32_e32 v3, v43, v68
	v_mul_f32_e32 v3, v3, v81
	v_cvt_pk_bf16_f32 v3, v3, v161
	ds_write_b16 v64, v3 offset:4864
	v_mul_f32_e32 v3, v41, v68
	v_mul_f32_e32 v3, v3, v82
	v_cvt_pk_bf16_f32 v3, v3, v161
	ds_write_b16 v64, v3 offset:4928
	v_mul_f32_e32 v3, v42, v68
	v_mul_f32_e32 v3, v3, v84
	v_cvt_pk_bf16_f32 v3, v3, v161
	ds_write_b16 v64, v3 offset:4992
	v_mul_f32_e32 v3, v40, v68
	v_mul_f32_e32 v3, v3, v83
	v_cvt_pk_bf16_f32 v3, v3, v161
	ds_write_b16 v64, v3 offset:5056
	v_mul_f32_e32 v3, v56, v70
	v_mul_f32_e32 v3, v3, v81
	v_cvt_pk_bf16_f32 v3, v3, v161
	ds_write_b16 v64, v3 offset:6144
	v_mul_f32_e32 v3, v57, v70
	v_mul_f32_e32 v3, v3, v82
	v_cvt_pk_bf16_f32 v3, v3, v161
	ds_write_b16 v64, v3 offset:6208
	v_mul_f32_e32 v3, v58, v70
	v_mul_f32_e32 v3, v3, v84
	v_cvt_pk_bf16_f32 v3, v3, v161
	ds_write_b16 v64, v3 offset:6272
	v_mul_f32_e32 v3, v66, v70
	v_mul_f32_e32 v3, v3, v83
	v_cvt_pk_bf16_f32 v3, v3, v161
	ds_write_b16 v64, v3 offset:6336
	v_mul_f32_e32 v3, v67, v74
	v_mul_f32_e32 v3, v3, v81
	v_cvt_pk_bf16_f32 v3, v3, v161
	ds_write_b16 v64, v3 offset:6400
	v_mul_f32_e32 v3, v61, v74
	v_mul_f32_e32 v3, v3, v82
	v_cvt_pk_bf16_f32 v3, v3, v161
	ds_write_b16 v64, v3 offset:6464
	v_mul_f32_e32 v3, v63, v74
	v_mul_f32_e32 v3, v3, v84
	v_cvt_pk_bf16_f32 v3, v3, v161
	ds_write_b16 v64, v3 offset:6528
	v_mul_f32_e32 v3, v65, v74
	v_mul_f32_e32 v3, v3, v83
	v_cvt_pk_bf16_f32 v3, v3, v161
	ds_write_b16 v64, v3 offset:6592
	v_mul_f32_e32 v3, v62, v71
	v_mul_f32_e32 v3, v81, v3
	v_cvt_pk_bf16_f32 v3, v3, v161
	ds_write_b16 v64, v3 offset:6656
	v_mul_f32_e32 v3, v59, v71
	v_mul_f32_e32 v3, v3, v82
	v_cvt_pk_bf16_f32 v3, v3, v161
	ds_write_b16 v64, v3 offset:6720
	v_mul_f32_e32 v3, v60, v71
	v_mul_f32_e32 v3, v3, v84
	v_cvt_pk_bf16_f32 v3, v3, v161
	ds_write_b16 v64, v3 offset:6784
	v_mul_f32_e32 v3, v6, v71
	v_mul_f32_e32 v3, v3, v83
	v_cvt_pk_bf16_f32 v3, v3, v161
	ds_write_b16 v64, v3 offset:6848
	v_mul_f32_e32 v3, v4, v69
	v_mul_f32_e32 v3, v81, v3
	v_mul_f32_e32 v1, v82, v1
	v_cvt_pk_bf16_f32 v3, v3, v161
	ds_write_b16 v64, v3 offset:6912
	v_cvt_pk_bf16_f32 v1, v1, v161
	ds_write_b16 v64, v1 offset:6976
	v_mul_f32_e32 v1, v2, v69
	v_mul_f32_e32 v1, v84, v1
	v_mul_f32_e32 v0, v83, v0
	v_cvt_pk_bf16_f32 v1, v1, v161
	ds_write_b16 v64, v1 offset:7040
	v_cvt_pk_bf16_f32 v0, v0, v161
	ds_write_b16 v64, v0 offset:7104
	v_lshlrev_b32_e32 v0, 5, v214
	v_ashrrev_i32_e32 v1, 31, v0
	v_lshl_add_u64 v[0:1], s[6:7], 0, v[0:1]
	v_lshlrev_b64 v[0:1], 11, v[0:1]
	v_lshlrev_b32_e32 v2, 4, v207
	v_lshl_add_u64 v[0:1], s[0:1], 0, v[0:1]
	v_and_b32_e32 v160, 0xf0, v2
	v_lshl_add_u64 v[0:1], v[0:1], 0, s[64:65]
	v_lshrrev_b32_e32 v8, 4, v213
	v_add_u32_e32 v9, v215, v160
	s_waitcnt lgkmcnt(0)
	v_lshl_add_u64 v[4:5], v[0:1], 0, v[160:161]
	v_lshl_add_u32 v0, v8, 8, v9
	ds_read_b128 v[0:3], v0
	v_lshlrev_b32_e32 v160, 11, v8
	v_lshl_add_u64 v[6:7], v[4:5], 0, v[160:161]
	v_readlane_b32 s0, v251, 2
	s_add_i32 s37, s37, s0
	s_waitcnt lgkmcnt(0)
	global_store_dwordx4 v[6:7], v[0:3], off sc1
	v_or_b32_e32 v6, 4, v8
	v_lshlrev_b32_e32 v160, 11, v6
	v_lshl_add_u32 v0, v6, 8, v9
	ds_read_b128 v[0:3], v0
	v_lshl_add_u64 v[6:7], v[4:5], 0, v[160:161]
	v_readlane_b32 s0, v252, 24
	s_add_i32 s36, s36, s0
	s_cmpk_gt_i32 s37, 0x1ff
	s_waitcnt lgkmcnt(0)
	global_store_dwordx4 v[6:7], v[0:3], off sc1
	v_or_b32_e32 v6, 8, v8
	v_lshlrev_b32_e32 v160, 11, v6
	v_lshl_add_u32 v0, v6, 8, v9
	ds_read_b128 v[0:3], v0
	v_lshl_add_u64 v[6:7], v[4:5], 0, v[160:161]
	s_waitcnt lgkmcnt(0)
	global_store_dwordx4 v[6:7], v[0:3], off sc1
	v_or_b32_e32 v6, 12, v8
	s_nop 0
	v_lshl_add_u32 v0, v6, 8, v9
	ds_read_b128 v[0:3], v0
	v_lshlrev_b32_e32 v160, 11, v6
	v_lshl_add_u64 v[6:7], v[4:5], 0, v[160:161]
	s_waitcnt lgkmcnt(0)
	global_store_dwordx4 v[6:7], v[0:3], off sc1
	v_or_b32_e32 v6, 16, v8
	s_nop 0
	v_lshl_add_u32 v0, v6, 8, v9
	ds_read_b128 v[0:3], v0
	v_lshlrev_b32_e32 v160, 11, v6
	v_lshl_add_u64 v[6:7], v[4:5], 0, v[160:161]
	s_waitcnt lgkmcnt(0)
	global_store_dwordx4 v[6:7], v[0:3], off sc1
	v_or_b32_e32 v6, 20, v8
	s_nop 0
	v_lshl_add_u32 v0, v6, 8, v9
	ds_read_b128 v[0:3], v0
	v_lshlrev_b32_e32 v160, 11, v6
	v_lshl_add_u64 v[6:7], v[4:5], 0, v[160:161]
	s_waitcnt lgkmcnt(0)
	global_store_dwordx4 v[6:7], v[0:3], off sc1
	v_or_b32_e32 v6, 24, v8
	s_nop 0
	v_lshl_add_u32 v0, v6, 8, v9
	ds_read_b128 v[0:3], v0
	v_lshlrev_b32_e32 v160, 11, v6
	v_lshl_add_u64 v[6:7], v[4:5], 0, v[160:161]
	s_waitcnt lgkmcnt(0)
	global_store_dwordx4 v[6:7], v[0:3], off sc1
	v_or_b32_e32 v6, 28, v8
	s_nop 0
	v_lshl_add_u32 v0, v6, 8, v9
	ds_read_b128 v[0:3], v0
	v_lshlrev_b32_e32 v160, 11, v6
	v_lshl_add_u64 v[4:5], v[4:5], 0, v[160:161]
	s_waitcnt lgkmcnt(0)
	global_store_dwordx4 v[4:5], v[0:3], off sc1
	s_waitcnt lgkmcnt(0)
	s_cbranch_scc1 .LBB0_870

;     __device__ __forceinline__ bool operator()(f32x4 (&acc)[2][2][4][2], const pg8::Unit& u, int wr, int wc, int fr, int fq) const {
;     ...
;             for (int m = 0; m < 4; ++m) { const int row = row0 + ai * 128 + m * 16; const float s = part ? rs_[ai][m] * scale : scale;
; #pragma unroll
;                 for (int bj = 0; bj < 2; ++bj) st8(base + (size_t)row * ldc + colb + bj * 128, acc[ai][bj][m][0] * s, acc[ai][bj][m][1] * s); }
.LBB0_1579:
	v_lshl_add_u32 v134, s35, 8, v136
	v_lshl_or_b32 v140, s34, 8, v138
	v_readlane_b32 s2, v251, 56
	v_ashrrev_i32_e32 v135, 31, v134
	v_ashrrev_i32_e32 v141, 31, v140
	v_readlane_b32 s3, v251, 57
	v_or_b32_e32 v144, 16, v134
	v_or_b32_e32 v146, 32, v134
	v_or_b32_e32 v148, 48, v134
	v_lshl_add_u64 v[150:151], v[140:141], 1, s[2:3]
	v_lshlrev_b64 v[134:135], 11, v[134:135]
	v_lshl_add_u64 v[134:135], v[150:151], 0, v[134:135]
	v_cvt_pk_bf16_f32 v140, v124, v125
	v_cvt_pk_bf16_f32 v141, v126, v127
	v_ashrrev_i32_e32 v145, 31, v144
	v_cvt_pk_bf16_f32 v142, v120, v121
	v_cvt_pk_bf16_f32 v143, v122, v123
	global_store_dwordx4 v[134:135], v[140:143], off sc1
	v_ashrrev_i32_e32 v147, 31, v146
	v_ashrrev_i32_e32 v149, 31, v148
	v_cvt_pk_bf16_f32 v140, v92, v93
	v_cvt_pk_bf16_f32 v141, v94, v95
	v_cvt_pk_bf16_f32 v142, v88, v89
	v_cvt_pk_bf16_f32 v143, v90, v91
	global_store_dwordx4 v[134:135], v[140:143], off offset:256 sc1
	s_mov_b64 s[2:3], 0x40000
	s_nop 0
	v_lshlrev_b64 v[140:141], 11, v[144:145]
	v_lshl_add_u64 v[144:145], v[150:151], 0, v[140:141]
	v_cvt_pk_bf16_f32 v140, v116, v117
	v_cvt_pk_bf16_f32 v141, v118, v119
	v_cvt_pk_bf16_f32 v142, v112, v113
	v_cvt_pk_bf16_f32 v143, v114, v115
	global_store_dwordx4 v[144:145], v[140:143], off sc1
	s_nop 1
	v_cvt_pk_bf16_f32 v140, v84, v85
	v_cvt_pk_bf16_f32 v141, v86, v87
	v_cvt_pk_bf16_f32 v142, v80, v81
	v_cvt_pk_bf16_f32 v143, v82, v83
	global_store_dwordx4 v[144:145], v[140:143], off offset:256 sc1
	s_nop 1
	v_lshlrev_b64 v[140:141], 11, v[146:147]
	v_lshl_add_u64 v[144:145], v[150:151], 0, v[140:141]
	v_cvt_pk_bf16_f32 v140, v108, v109
	v_cvt_pk_bf16_f32 v141, v110, v111
	v_cvt_pk_bf16_f32 v142, v104, v105
	v_cvt_pk_bf16_f32 v143, v106, v107
	global_store_dwordx4 v[144:145], v[140:143], off sc1
	s_nop 1
	v_cvt_pk_bf16_f32 v140, v76, v77
	v_cvt_pk_bf16_f32 v141, v78, v79
	v_cvt_pk_bf16_f32 v142, v72, v73
	v_cvt_pk_bf16_f32 v143, v74, v75
	global_store_dwordx4 v[144:145], v[140:143], off offset:256 sc1
	s_nop 1
	v_lshlrev_b64 v[140:141], 11, v[148:149]
	v_lshl_add_u64 v[144:145], v[150:151], 0, v[140:141]
	v_cvt_pk_bf16_f32 v140, v100, v101
	v_cvt_pk_bf16_f32 v141, v102, v103
	v_cvt_pk_bf16_f32 v142, v96, v97
	v_cvt_pk_bf16_f32 v143, v98, v99
	global_store_dwordx4 v[144:145], v[140:143], off sc1
	s_nop 1
	v_cvt_pk_bf16_f32 v140, v68, v69
	v_cvt_pk_bf16_f32 v141, v70, v71
	v_cvt_pk_bf16_f32 v142, v64, v65
	v_cvt_pk_bf16_f32 v143, v66, v67
	global_store_dwordx4 v[144:145], v[140:143], off offset:256 sc1
	v_lshl_add_u64 v[144:145], v[134:135], 0, s[2:3]
	s_mov_b32 s2, 0x40000
	v_add_co_u32_e32 v146, vcc, s2, v134
	v_cvt_pk_bf16_f32 v140, v60, v61
	v_cvt_pk_bf16_f32 v141, v62, v63
	v_cvt_pk_bf16_f32 v142, v56, v57
	v_cvt_pk_bf16_f32 v143, v58, v59
	s_nop 1
	v_addc_co_u32_e32 v147, vcc, 0, v135, vcc
	s_mov_b64 s[2:3], 0x48000
	global_store_dwordx4 v[146:147], v[140:143], off sc1
	s_nop 1
	v_cvt_pk_bf16_f32 v140, v28, v29
	v_cvt_pk_bf16_f32 v141, v30, v31
	v_cvt_pk_bf16_f32 v142, v24, v25
	v_cvt_pk_bf16_f32 v143, v26, v27
	global_store_dwordx4 v[144:145], v[140:143], off offset:256 sc1
	v_lshl_add_u64 v[144:145], v[134:135], 0, s[2:3]
	s_mov_b32 s2, 0x48000
	v_add_co_u32_e32 v146, vcc, s2, v134
	v_cvt_pk_bf16_f32 v140, v52, v53
	v_cvt_pk_bf16_f32 v141, v54, v55
	v_cvt_pk_bf16_f32 v142, v48, v49
	v_cvt_pk_bf16_f32 v143, v50, v51
	s_nop 1
	v_addc_co_u32_e32 v147, vcc, 0, v135, vcc
	s_mov_b64 s[2:3], 0x50000
	global_store_dwordx4 v[146:147], v[140:143], off sc1
	s_nop 1
	v_cvt_pk_bf16_f32 v140, v20, v21
	v_cvt_pk_bf16_f32 v141, v22, v23
	v_cvt_pk_bf16_f32 v142, v16, v17
	v_cvt_pk_bf16_f32 v143, v18, v19
	global_store_dwordx4 v[144:145], v[140:143], off offset:256 sc1
	v_lshl_add_u64 v[144:145], v[134:135], 0, s[2:3]
	s_mov_b32 s2, 0x50000
	v_add_co_u32_e32 v146, vcc, s2, v134
	v_cvt_pk_bf16_f32 v140, v44, v45
	v_cvt_pk_bf16_f32 v141, v46, v47
	v_cvt_pk_bf16_f32 v142, v40, v41
	v_cvt_pk_bf16_f32 v143, v42, v43
	s_nop 1
	v_addc_co_u32_e32 v147, vcc, 0, v135, vcc
	s_mov_b64 s[2:3], 0x58000
	global_store_dwordx4 v[146:147], v[140:143], off sc1
	s_nop 1
	v_cvt_pk_bf16_f32 v140, v12, v13
	v_cvt_pk_bf16_f32 v141, v14, v15
	v_cvt_pk_bf16_f32 v142, v8, v9
	v_cvt_pk_bf16_f32 v143, v10, v11
	global_store_dwordx4 v[144:145], v[140:143], off offset:256 sc1
	v_lshl_add_u64 v[144:145], v[134:135], 0, s[2:3]
	s_mov_b32 s2, 0x58000
	v_add_co_u32_e32 v134, vcc, s2, v134
	v_cvt_pk_bf16_f32 v140, v36, v37
	v_cvt_pk_bf16_f32 v141, v38, v39
	v_cvt_pk_bf16_f32 v142, v32, v33
	v_cvt_pk_bf16_f32 v143, v34, v35
	s_nop 1
	v_addc_co_u32_e32 v135, vcc, 0, v135, vcc
	s_andn2_b64 vcc, exec, s[14:15]
	global_store_dwordx4 v[134:135], v[140:143], off sc1
	s_nop 1
	v_cvt_pk_bf16_f32 v140, v4, v5
	v_cvt_pk_bf16_f32 v141, v6, v7
	v_cvt_pk_bf16_f32 v142, v0, v1
	v_cvt_pk_bf16_f32 v143, v2, v3
	global_store_dwordx4 v[144:145], v[140:143], off offset:256 sc1
	s_cbranch_vccnz .LBB0_1547
	v_readlane_b32 s2, v252, 46
	v_readlane_b32 s3, v252, 47
	s_and_b64 vcc, exec, s[2:3]
	s_cbranch_vccnz .LBB0_1546
	s_barrier
	s_branch .LBB0_1546
